# P6 epilogue: gate quads prefetched 3 store-groups ahead into dead registers; per-group counted wait no longer covers the previous store
# speedup vs baseline: 1.0105x; 1.0105x over previous
.LBB0_977:
	v_mov_b32_e32 v213, s6
	v_min_u32_e32 v213, 2, v213
	v_lshlrev_b32_e32 v213, 11, v213
	v_add_u32_e32 v213, 0x1800, v213
	v_mul_u32_u24_e32 v240, 0x3000, v134
	v_add_u32_e32 v240, v240, v213
	v_mov_b32_e32 v241, 0
	v_lshl_add_u64 v[238:239], v[148:149], 1, v[240:241]
	v_lshl_add_u64 v[238:239], s[8:9], 0, v[238:239]
	global_load_dwordx4 v[226:229], v[238:239], off
	v_mul_u32_u24_e32 v240, 0x3000, v134
	v_add_u32_e32 v240, v240, v213
	v_mov_b32_e32 v241, 0
	v_lshl_add_u64 v[238:239], v[150:151], 1, v[240:241]
	v_lshl_add_u64 v[238:239], s[8:9], 0, v[238:239]
	global_load_dwordx4 v[230:233], v[238:239], off
	v_mul_u32_u24_e32 v240, 0x3000, v164
	v_add_u32_e32 v240, v240, v213
	v_mov_b32_e32 v241, 0
	v_lshl_add_u64 v[238:239], v[148:149], 1, v[240:241]
	v_lshl_add_u64 v[238:239], s[8:9], 0, v[238:239]
	global_load_dwordx4 v[234:237], v[238:239], off
	s_cmp_lt_i32 s6, 0
	s_cselect_b64 s[36:37], -1, 0
	v_ashrrev_i32_e32 v135, 31, v134
	s_cmp_eq_u32 s6, 0
	v_lshlrev_b64 v[168:169], 11, v[134:135]
	v_mov_b64_e32 v[4:5], s[8:9]
	s_cselect_b64 s[4:5], -1, 0
	v_mad_i64_i32 v[166:167], s[34:35], v134, s64, v[4:5]
	s_mov_b64 s[38:39], -1
	s_and_b64 vcc, exec, s[36:37]
	v_lshl_add_u64 v[4:5], s[10:11], 0, v[168:169]
	s_cbranch_vccz .LBB0_979
	v_lshl_add_u64 v[134:135], v[148:149], 1, v[166:167]
	v_add_co_u32_e32 v134, vcc, 0x2000, v134
	v_mov_b32_e32 v176, v131
	s_nop 0
	v_addc_co_u32_e32 v135, vcc, 0, v135, vcc
	v_mov_b32_e32 v177, v132
	v_pk_mov_b32 v[178:179], v[132:133], v[126:127] op_sel:[1,0]
	v_mov_b32_e32 v180, v127
	v_mov_b32_e32 v181, v128
	v_lshl_add_u64 v[170:171], s[10:11], 0, v[168:169]
	s_mov_b64 s[38:39], 0
	s_waitcnt vmcnt(2)
	v_mov_b32_e32 v134, v226
	v_mov_b32_e32 v135, v227
	v_mov_b32_e32 v136, v228
	v_mov_b32_e32 v137, v229
	v_cvt_f32_f16_e32 v3, v134
	v_cvt_f32_f16_sdwa v134, v134 dst_sel:DWORD dst_unused:UNUSED_PAD src0_sel:WORD_1
	v_cvt_f32_f16_e32 v153, v135
	v_cvt_f32_f16_sdwa v155, v135 dst_sel:DWORD dst_unused:UNUSED_PAD src0_sel:WORD_1
	v_cvt_f32_f16_e32 v157, v136
	v_cvt_f32_f16_sdwa v159, v136 dst_sel:DWORD dst_unused:UNUSED_PAD src0_sel:WORD_1
	v_cvt_f32_f16_e32 v161, v137
	v_cvt_f32_f16_sdwa v163, v137 dst_sel:DWORD dst_unused:UNUSED_PAD src0_sel:WORD_1
	v_max_f32_e32 v134, 0x38d1b717, v134
	v_max_f32_e32 v135, 0x38d1b717, v153
	v_max_f32_e32 v136, 0x38d1b717, v155
	v_max_f32_e32 v137, 0x38d1b717, v157
	v_max_f32_e32 v182, 0x38d1b717, v159
	v_max_f32_e32 v183, 0x38d1b717, v161
	v_max_f32_e32 v3, 0x38d1b717, v3
	v_pk_mul_f32 v[134:135], v[176:177], v[134:135]
	v_pk_mul_f32 v[136:137], v[178:179], v[136:137]
	v_pk_mul_f32 v[176:177], v[180:181], v[182:183]
	v_fma_mixlo_f16 v3, v130, v3, 0
	v_cvt_pk_f16_f32 v135, v134, v135
	v_cvt_pk_f16_f32 v136, v136, v137
	v_cvt_pk_f16_f32 v137, v176, v177
	v_max_f32_e32 v153, 0x38d1b717, v163
	v_pack_b32_f16 v134, v3, v135
	v_alignbit_b32 v135, v136, v135, 16
	v_alignbit_b32 v136, v137, v136, 16
	v_lshrrev_b32_e32 v137, 16, v137
	v_fma_mixhi_f16 v137, v129, v153, 0
.LBB0_979:
	s_min_u32 s0, s6, 2
	s_mov_b32 s7, s1
	s_lshl_b32 s21, s0, 10
	s_lshl_b64 s[34:35], s[6:7], 22
	s_andn2_b64 vcc, exec, s[38:39]
	v_lshl_add_u64 v[168:169], v[168:169], 0, s[18:19]
	s_cbranch_vccnz .LBB0_981
	s_lshl_b32 s0, s21, 1
	v_lshl_add_u64 v[134:135], v[166:167], 0, s[0:1]
	v_lshl_add_u64 v[134:135], v[148:149], 1, v[134:135]
	v_add_co_u32_e32 v134, vcc, 0x1000, v134
	s_add_u32 s6, s55, s34
	s_nop 0
	v_addc_co_u32_e32 v135, vcc, 0, v135, vcc
	s_addc_u32 s7, s56, s35
	v_lshl_add_u64 v[170:171], s[6:7], 0, v[168:169]
	s_waitcnt vmcnt(2)
	v_mov_b32_e32 v134, v226
	v_mov_b32_e32 v135, v227
	v_mov_b32_e32 v136, v228
	v_mov_b32_e32 v137, v229
	v_cvt_f32_f16_e32 v3, v134
	v_cvt_f32_f16_sdwa v134, v134 dst_sel:DWORD dst_unused:UNUSED_PAD src0_sel:WORD_1
	v_cvt_f32_f16_e32 v153, v135
	v_cvt_f32_f16_sdwa v135, v135 dst_sel:DWORD dst_unused:UNUSED_PAD src0_sel:WORD_1
	v_cvt_f32_f16_e32 v155, v136
	v_cvt_f32_f16_sdwa v136, v136 dst_sel:DWORD dst_unused:UNUSED_PAD src0_sel:WORD_1
	v_cvt_f32_f16_e32 v157, v137
	v_cvt_f32_f16_sdwa v137, v137 dst_sel:DWORD dst_unused:UNUSED_PAD src0_sel:WORD_1
	v_max_f32_e32 v159, 0x38d1b717, v3
	v_max_f32_e32 v161, 0x38d1b717, v134
	v_max_f32_e32 v163, 0x38d1b717, v153
	v_max_f32_e32 v165, 0x38d1b717, v135
	v_max_f32_e32 v175, 0x38d1b717, v155
	v_max_f32_e32 v176, 0x38d1b717, v136
	v_max_f32_e32 v177, 0x38d1b717, v157
	v_max_f32_e32 v178, 0x38d1b717, v137
	v_cndmask_b32_e64 v3, v159, v3, s[4:5]
	v_cndmask_b32_e64 v134, v161, v134, s[4:5]
	v_cndmask_b32_e64 v153, v163, v153, s[4:5]
	v_cndmask_b32_e64 v135, v165, v135, s[4:5]
	v_cndmask_b32_e64 v155, v175, v155, s[4:5]
	v_cndmask_b32_e64 v136, v176, v136, s[4:5]
	v_cndmask_b32_e64 v157, v177, v157, s[4:5]
	v_cndmask_b32_e64 v137, v178, v137, s[4:5]
	v_mul_f32_e32 v128, v128, v157
	v_mul_f32_e32 v127, v127, v136
	v_mul_f32_e32 v126, v126, v155
	v_mul_f32_e32 v133, v133, v135
	v_mul_f32_e32 v132, v132, v153
	v_mul_f32_e32 v131, v131, v134
	v_mul_f32_e32 v3, v130, v3
	v_mul_f32_e32 v129, v129, v137
	v_cvt_pk_f16_f32 v134, v3, v131
	v_cvt_pk_f16_f32 v135, v132, v133
	v_cvt_pk_f16_f32 v136, v126, v127
	v_cvt_pk_f16_f32 v137, v128, v129
.LBB0_981:
	v_cndmask_b32_e64 v3, 0, 1, s[36:37]
	v_lshl_add_u64 v[126:127], v[148:149], 1, v[170:171]
	v_cmp_ne_u32_e64 s[6:7], 1, v3
	s_andn2_b64 vcc, exec, s[36:37]
	s_mov_b64 s[36:37], -1
	global_store_dwordx4 v[126:127], v[134:137], off
	v_mul_u32_u24_e32 v240, 0x3000, v164
	v_add_u32_e32 v240, v240, v213
	v_mov_b32_e32 v241, 0
	v_lshl_add_u64 v[238:239], v[150:151], 1, v[240:241]
	v_lshl_add_u64 v[238:239], s[8:9], 0, v[238:239]
	global_load_dwordx4 v[226:229], v[238:239], off
	s_cbranch_vccnz .LBB0_983
	v_lshl_add_u64 v[126:127], v[150:151], 1, v[166:167]
	v_add_co_u32_e32 v126, vcc, 0x2000, v126
	v_mov_b32_e32 v130, v123
	s_nop 0
	v_addc_co_u32_e32 v127, vcc, 0, v127, vcc
	v_mov_b32_e32 v131, v124
	v_pk_mov_b32 v[132:133], v[124:125], v[118:119] op_sel:[1,0]
	v_mov_b32_e32 v134, v119
	v_mov_b32_e32 v135, v120
	s_mov_b64 s[36:37], 0
	s_waitcnt vmcnt(3)
	v_mov_b32_e32 v126, v230
	v_mov_b32_e32 v127, v231
	v_mov_b32_e32 v128, v232
	v_mov_b32_e32 v129, v233
	v_cvt_f32_f16_e32 v3, v126
	v_cvt_f32_f16_sdwa v126, v126 dst_sel:DWORD dst_unused:UNUSED_PAD src0_sel:WORD_1
	v_cvt_f32_f16_e32 v136, v127
	v_cvt_f32_f16_sdwa v137, v127 dst_sel:DWORD dst_unused:UNUSED_PAD src0_sel:WORD_1
	v_cvt_f32_f16_e32 v153, v128
	v_cvt_f32_f16_sdwa v155, v128 dst_sel:DWORD dst_unused:UNUSED_PAD src0_sel:WORD_1
	v_cvt_f32_f16_e32 v157, v129
	v_cvt_f32_f16_sdwa v159, v129 dst_sel:DWORD dst_unused:UNUSED_PAD src0_sel:WORD_1
	v_max_f32_e32 v126, 0x38d1b717, v126
	v_max_f32_e32 v127, 0x38d1b717, v136
	v_max_f32_e32 v128, 0x38d1b717, v137
	v_max_f32_e32 v129, 0x38d1b717, v153
	v_max_f32_e32 v136, 0x38d1b717, v155
	v_max_f32_e32 v137, 0x38d1b717, v157
	v_max_f32_e32 v3, 0x38d1b717, v3
	v_pk_mul_f32 v[126:127], v[130:131], v[126:127]
	v_pk_mul_f32 v[128:129], v[132:133], v[128:129]
	v_pk_mul_f32 v[130:131], v[134:135], v[136:137]
	v_fma_mixlo_f16 v3, v122, v3, 0
	v_cvt_pk_f16_f32 v127, v126, v127
	v_cvt_pk_f16_f32 v128, v128, v129
	v_cvt_pk_f16_f32 v129, v130, v131
	v_max_f32_e32 v153, 0x38d1b717, v159
	v_pack_b32_f16 v126, v3, v127
	v_alignbit_b32 v127, v128, v127, 16
	v_alignbit_b32 v128, v129, v128, 16
	v_lshrrev_b32_e32 v129, 16, v129
	v_fma_mixhi_f16 v129, v121, v153, 0
.LBB0_983:
	s_andn2_b64 vcc, exec, s[36:37]
	s_cbranch_vccnz .LBB0_985
	s_lshl_b32 s0, s21, 1
	v_lshl_add_u64 v[4:5], v[166:167], 0, s[0:1]
	v_lshl_add_u64 v[4:5], v[148:149], 1, v[4:5]
	v_add_co_u32_e32 v4, vcc, 0x1000, v4
	s_add_u32 s36, s55, s34
	s_nop 0
	v_addc_co_u32_e32 v5, vcc, 0, v5, vcc
	s_addc_u32 s37, s56, s35
	v_lshl_add_u64 v[4:5], s[36:37], 0, v[168:169]
	s_waitcnt vmcnt(3)
	v_mov_b32_e32 v126, v230
	v_mov_b32_e32 v127, v231
	v_mov_b32_e32 v128, v232
	v_mov_b32_e32 v129, v233
	v_cvt_f32_f16_e32 v3, v126
	v_cvt_f32_f16_sdwa v126, v126 dst_sel:DWORD dst_unused:UNUSED_PAD src0_sel:WORD_1
	v_cvt_f32_f16_e32 v130, v127
	v_cvt_f32_f16_sdwa v127, v127 dst_sel:DWORD dst_unused:UNUSED_PAD src0_sel:WORD_1
	v_cvt_f32_f16_e32 v131, v128
	v_cvt_f32_f16_sdwa v128, v128 dst_sel:DWORD dst_unused:UNUSED_PAD src0_sel:WORD_1
	v_cvt_f32_f16_e32 v132, v129
	v_cvt_f32_f16_sdwa v129, v129 dst_sel:DWORD dst_unused:UNUSED_PAD src0_sel:WORD_1
	v_max_f32_e32 v133, 0x38d1b717, v3
	v_max_f32_e32 v134, 0x38d1b717, v126
	v_max_f32_e32 v135, 0x38d1b717, v130
	v_max_f32_e32 v136, 0x38d1b717, v127
	v_max_f32_e32 v137, 0x38d1b717, v131
	v_max_f32_e32 v153, 0x38d1b717, v128
	v_max_f32_e32 v155, 0x38d1b717, v132
	v_max_f32_e32 v157, 0x38d1b717, v129
	v_cndmask_b32_e64 v3, v133, v3, s[4:5]
	v_cndmask_b32_e64 v126, v134, v126, s[4:5]
	v_cndmask_b32_e64 v130, v135, v130, s[4:5]
	v_cndmask_b32_e64 v127, v136, v127, s[4:5]
	v_cndmask_b32_e64 v131, v137, v131, s[4:5]
	v_cndmask_b32_e64 v128, v153, v128, s[4:5]
	v_cndmask_b32_e64 v132, v155, v132, s[4:5]
	v_cndmask_b32_e64 v129, v157, v129, s[4:5]
	v_mul_f32_e32 v120, v120, v132
	v_mul_f32_e32 v119, v119, v128
	v_mul_f32_e32 v118, v118, v131
	v_mul_f32_e32 v125, v125, v127
	v_mul_f32_e32 v124, v124, v130
	v_mul_f32_e32 v123, v123, v126
	v_mul_f32_e32 v3, v122, v3
	v_mul_f32_e32 v121, v121, v129
	v_cvt_pk_f16_f32 v126, v3, v123
	v_cvt_pk_f16_f32 v127, v124, v125
	v_cvt_pk_f16_f32 v128, v118, v119
	v_cvt_pk_f16_f32 v129, v120, v121
.LBB0_985:
	v_lshl_add_u64 v[4:5], v[148:149], 1, v[4:5]
	global_store_dwordx4 v[4:5], v[126:129], off offset:256
	v_mul_u32_u24_e32 v240, 0x3000, v162
	v_add_u32_e32 v240, v240, v213
	v_mov_b32_e32 v241, 0
	v_lshl_add_u64 v[238:239], v[148:149], 1, v[240:241]
	v_lshl_add_u64 v[238:239], s[8:9], 0, v[238:239]
	global_load_dwordx4 v[230:233], v[238:239], off
	v_mov_b64_e32 v[4:5], s[8:9]
	v_ashrrev_i32_e32 v165, 31, v164
	v_lshlrev_b64 v[124:125], 11, v[164:165]
	v_mad_i64_i32 v[122:123], s[36:37], v164, s64, v[4:5]
	s_mov_b64 s[36:37], -1
	s_and_b64 vcc, exec, s[6:7]
	v_lshl_add_u64 v[4:5], s[10:11], 0, v[124:125]
	s_cbranch_vccnz .LBB0_987
	v_lshl_add_u64 v[118:119], v[148:149], 1, v[122:123]
	v_add_co_u32_e32 v118, vcc, 0x2000, v118
	v_mov_b32_e32 v128, v115
	s_nop 0
	v_addc_co_u32_e32 v119, vcc, 0, v119, vcc
	v_mov_b32_e32 v129, v116
	v_pk_mov_b32 v[130:131], v[116:117], v[110:111] op_sel:[1,0]
	v_mov_b32_e32 v132, v111
	v_mov_b32_e32 v133, v112
	v_lshl_add_u64 v[126:127], s[10:11], 0, v[124:125]
	s_mov_b64 s[36:37], 0
	s_waitcnt vmcnt(4)
	v_mov_b32_e32 v118, v234
	v_mov_b32_e32 v119, v235
	v_mov_b32_e32 v120, v236
	v_mov_b32_e32 v121, v237
	v_cvt_f32_f16_e32 v3, v118
	v_cvt_f32_f16_sdwa v118, v118 dst_sel:DWORD dst_unused:UNUSED_PAD src0_sel:WORD_1
	v_cvt_f32_f16_e32 v134, v119
	v_cvt_f32_f16_sdwa v135, v119 dst_sel:DWORD dst_unused:UNUSED_PAD src0_sel:WORD_1
	v_cvt_f32_f16_e32 v136, v120
	v_cvt_f32_f16_sdwa v137, v120 dst_sel:DWORD dst_unused:UNUSED_PAD src0_sel:WORD_1
	v_cvt_f32_f16_e32 v153, v121
	v_cvt_f32_f16_sdwa v155, v121 dst_sel:DWORD dst_unused:UNUSED_PAD src0_sel:WORD_1
	v_max_f32_e32 v118, 0x38d1b717, v118
	v_max_f32_e32 v119, 0x38d1b717, v134
	v_max_f32_e32 v120, 0x38d1b717, v135
	v_max_f32_e32 v121, 0x38d1b717, v136
	v_max_f32_e32 v134, 0x38d1b717, v137
	v_max_f32_e32 v135, 0x38d1b717, v153
	v_max_f32_e32 v3, 0x38d1b717, v3
	v_pk_mul_f32 v[118:119], v[128:129], v[118:119]
	v_pk_mul_f32 v[120:121], v[130:131], v[120:121]
	v_pk_mul_f32 v[128:129], v[132:133], v[134:135]
	v_fma_mixlo_f16 v3, v114, v3, 0
	v_cvt_pk_f16_f32 v119, v118, v119
	v_cvt_pk_f16_f32 v120, v120, v121
	v_cvt_pk_f16_f32 v121, v128, v129
	v_max_f32_e32 v136, 0x38d1b717, v155
	v_pack_b32_f16 v118, v3, v119
	v_alignbit_b32 v119, v120, v119, 16
	v_alignbit_b32 v120, v121, v120, 16
	v_lshrrev_b32_e32 v121, 16, v121
	v_fma_mixhi_f16 v121, v113, v136, 0
.LBB0_987:
	s_andn2_b64 vcc, exec, s[36:37]
	v_lshl_add_u64 v[124:125], v[124:125], 0, s[18:19]
	s_cbranch_vccnz .LBB0_989
	s_lshl_b32 s0, s21, 1
	v_lshl_add_u64 v[118:119], v[122:123], 0, s[0:1]
	v_lshl_add_u64 v[118:119], v[148:149], 1, v[118:119]
	v_add_co_u32_e32 v118, vcc, 0x1000, v118
	s_add_u32 s36, s55, s34
	s_nop 0
	v_addc_co_u32_e32 v119, vcc, 0, v119, vcc
	s_addc_u32 s37, s56, s35
	v_lshl_add_u64 v[126:127], s[36:37], 0, v[124:125]
	s_waitcnt vmcnt(4)
	v_mov_b32_e32 v118, v234
	v_mov_b32_e32 v119, v235
	v_mov_b32_e32 v120, v236
	v_mov_b32_e32 v121, v237
	v_cvt_f32_f16_e32 v3, v118
	v_cvt_f32_f16_sdwa v118, v118 dst_sel:DWORD dst_unused:UNUSED_PAD src0_sel:WORD_1
	v_cvt_f32_f16_e32 v128, v119
	v_cvt_f32_f16_sdwa v119, v119 dst_sel:DWORD dst_unused:UNUSED_PAD src0_sel:WORD_1
	v_cvt_f32_f16_e32 v129, v120
	v_cvt_f32_f16_sdwa v120, v120 dst_sel:DWORD dst_unused:UNUSED_PAD src0_sel:WORD_1
	v_cvt_f32_f16_e32 v130, v121
	v_cvt_f32_f16_sdwa v121, v121 dst_sel:DWORD dst_unused:UNUSED_PAD src0_sel:WORD_1
	v_max_f32_e32 v131, 0x38d1b717, v3
	v_max_f32_e32 v132, 0x38d1b717, v118
	v_max_f32_e32 v133, 0x38d1b717, v128
	v_max_f32_e32 v134, 0x38d1b717, v119
	v_max_f32_e32 v135, 0x38d1b717, v129
	v_max_f32_e32 v136, 0x38d1b717, v120
	v_max_f32_e32 v137, 0x38d1b717, v130
	v_max_f32_e32 v153, 0x38d1b717, v121
	v_cndmask_b32_e64 v3, v131, v3, s[4:5]
	v_cndmask_b32_e64 v118, v132, v118, s[4:5]
	v_cndmask_b32_e64 v128, v133, v128, s[4:5]
	v_cndmask_b32_e64 v119, v134, v119, s[4:5]
	v_cndmask_b32_e64 v129, v135, v129, s[4:5]
	v_cndmask_b32_e64 v120, v136, v120, s[4:5]
	v_cndmask_b32_e64 v130, v137, v130, s[4:5]
	v_cndmask_b32_e64 v121, v153, v121, s[4:5]
	v_mul_f32_e32 v112, v112, v130
	v_mul_f32_e32 v111, v111, v120
	v_mul_f32_e32 v110, v110, v129
	v_mul_f32_e32 v117, v117, v119
	v_mul_f32_e32 v116, v116, v128
	v_mul_f32_e32 v115, v115, v118
	v_mul_f32_e32 v3, v114, v3
	v_mul_f32_e32 v113, v113, v121
	v_cvt_pk_f16_f32 v118, v3, v115
	v_cvt_pk_f16_f32 v119, v116, v117
	v_cvt_pk_f16_f32 v120, v110, v111
	v_cvt_pk_f16_f32 v121, v112, v113
.LBB0_989:
	v_lshl_add_u64 v[110:111], v[148:149], 1, v[126:127]
	s_and_b64 vcc, exec, s[6:7]
	s_mov_b64 s[36:37], -1
	global_store_dwordx4 v[110:111], v[118:121], off
	v_mul_u32_u24_e32 v240, 0x3000, v162
	v_add_u32_e32 v240, v240, v213
	v_mov_b32_e32 v241, 0
	v_lshl_add_u64 v[238:239], v[150:151], 1, v[240:241]
	v_lshl_add_u64 v[238:239], s[8:9], 0, v[238:239]
	global_load_dwordx4 v[234:237], v[238:239], off
	s_cbranch_vccnz .LBB0_991
	v_lshl_add_u64 v[110:111], v[150:151], 1, v[122:123]
	v_add_co_u32_e32 v110, vcc, 0x2000, v110
	v_mov_b32_e32 v114, v107
	s_nop 0
	v_addc_co_u32_e32 v111, vcc, 0, v111, vcc
	v_mov_b32_e32 v115, v108
	v_pk_mov_b32 v[116:117], v[108:109], v[102:103] op_sel:[1,0]
	v_mov_b32_e32 v118, v103
	v_mov_b32_e32 v119, v104
	s_mov_b64 s[36:37], 0
	s_waitcnt vmcnt(4)
	v_mov_b32_e32 v110, v226
	v_mov_b32_e32 v111, v227
	v_mov_b32_e32 v112, v228
	v_mov_b32_e32 v113, v229
	v_cvt_f32_f16_e32 v3, v110
	v_cvt_f32_f16_sdwa v110, v110 dst_sel:DWORD dst_unused:UNUSED_PAD src0_sel:WORD_1
	v_cvt_f32_f16_e32 v120, v111
	v_cvt_f32_f16_sdwa v121, v111 dst_sel:DWORD dst_unused:UNUSED_PAD src0_sel:WORD_1
	v_cvt_f32_f16_e32 v126, v112
	v_cvt_f32_f16_sdwa v127, v112 dst_sel:DWORD dst_unused:UNUSED_PAD src0_sel:WORD_1
	v_cvt_f32_f16_e32 v128, v113
	v_cvt_f32_f16_sdwa v129, v113 dst_sel:DWORD dst_unused:UNUSED_PAD src0_sel:WORD_1
	v_max_f32_e32 v110, 0x38d1b717, v110
	v_max_f32_e32 v111, 0x38d1b717, v120
	v_max_f32_e32 v112, 0x38d1b717, v121
	v_max_f32_e32 v113, 0x38d1b717, v126
	v_max_f32_e32 v120, 0x38d1b717, v127
	v_max_f32_e32 v121, 0x38d1b717, v128
	v_max_f32_e32 v3, 0x38d1b717, v3
	v_pk_mul_f32 v[110:111], v[114:115], v[110:111]
	v_pk_mul_f32 v[112:113], v[116:117], v[112:113]
	v_pk_mul_f32 v[114:115], v[118:119], v[120:121]
	v_fma_mixlo_f16 v3, v106, v3, 0
	v_cvt_pk_f16_f32 v111, v110, v111
	v_cvt_pk_f16_f32 v112, v112, v113
	v_cvt_pk_f16_f32 v113, v114, v115
	v_max_f32_e32 v126, 0x38d1b717, v129
	v_pack_b32_f16 v110, v3, v111
	v_alignbit_b32 v111, v112, v111, 16
	v_alignbit_b32 v112, v113, v112, 16
	v_lshrrev_b32_e32 v113, 16, v113
	v_fma_mixhi_f16 v113, v105, v126, 0
.LBB0_991:
	s_andn2_b64 vcc, exec, s[36:37]
	s_cbranch_vccnz .LBB0_993
	s_lshl_b32 s0, s21, 1
	v_lshl_add_u64 v[4:5], v[122:123], 0, s[0:1]
	v_lshl_add_u64 v[4:5], v[148:149], 1, v[4:5]
	v_add_co_u32_e32 v4, vcc, 0x1000, v4
	s_add_u32 s36, s55, s34
	s_nop 0
	v_addc_co_u32_e32 v5, vcc, 0, v5, vcc
	s_addc_u32 s37, s56, s35
	v_lshl_add_u64 v[4:5], s[36:37], 0, v[124:125]
	s_waitcnt vmcnt(4)
	v_mov_b32_e32 v110, v226
	v_mov_b32_e32 v111, v227
	v_mov_b32_e32 v112, v228
	v_mov_b32_e32 v113, v229
	v_cvt_f32_f16_e32 v3, v110
	v_cvt_f32_f16_sdwa v110, v110 dst_sel:DWORD dst_unused:UNUSED_PAD src0_sel:WORD_1
	v_cvt_f32_f16_e32 v114, v111
	v_cvt_f32_f16_sdwa v111, v111 dst_sel:DWORD dst_unused:UNUSED_PAD src0_sel:WORD_1
	v_cvt_f32_f16_e32 v115, v112
	v_cvt_f32_f16_sdwa v112, v112 dst_sel:DWORD dst_unused:UNUSED_PAD src0_sel:WORD_1
	v_cvt_f32_f16_e32 v116, v113
	v_cvt_f32_f16_sdwa v113, v113 dst_sel:DWORD dst_unused:UNUSED_PAD src0_sel:WORD_1
	v_max_f32_e32 v117, 0x38d1b717, v3
	v_max_f32_e32 v118, 0x38d1b717, v110
	v_max_f32_e32 v119, 0x38d1b717, v114
	v_max_f32_e32 v120, 0x38d1b717, v111
	v_max_f32_e32 v121, 0x38d1b717, v115
	v_max_f32_e32 v122, 0x38d1b717, v112
	v_max_f32_e32 v123, 0x38d1b717, v116
	v_max_f32_e32 v124, 0x38d1b717, v113
	v_cndmask_b32_e64 v3, v117, v3, s[4:5]
	v_cndmask_b32_e64 v110, v118, v110, s[4:5]
	v_cndmask_b32_e64 v114, v119, v114, s[4:5]
	v_cndmask_b32_e64 v111, v120, v111, s[4:5]
	v_cndmask_b32_e64 v115, v121, v115, s[4:5]
	v_cndmask_b32_e64 v112, v122, v112, s[4:5]
	v_cndmask_b32_e64 v116, v123, v116, s[4:5]
	v_cndmask_b32_e64 v113, v124, v113, s[4:5]
	v_mul_f32_e32 v104, v104, v116
	v_mul_f32_e32 v103, v103, v112
	v_mul_f32_e32 v102, v102, v115
	v_mul_f32_e32 v109, v109, v111
	v_mul_f32_e32 v108, v108, v114
	v_mul_f32_e32 v107, v107, v110
	v_mul_f32_e32 v3, v106, v3
	v_mul_f32_e32 v105, v105, v113
	v_cvt_pk_f16_f32 v110, v3, v107
	v_cvt_pk_f16_f32 v111, v108, v109
	v_cvt_pk_f16_f32 v112, v102, v103
	v_cvt_pk_f16_f32 v113, v104, v105
.LBB0_993:
	v_lshl_add_u64 v[4:5], v[148:149], 1, v[4:5]
	global_store_dwordx4 v[4:5], v[110:113], off offset:256
	v_mul_u32_u24_e32 v240, 0x3000, v160
	v_add_u32_e32 v240, v240, v213
	v_mov_b32_e32 v241, 0
	v_lshl_add_u64 v[238:239], v[148:149], 1, v[240:241]
	v_lshl_add_u64 v[238:239], s[8:9], 0, v[238:239]
	global_load_dwordx4 v[226:229], v[238:239], off
	v_mov_b64_e32 v[4:5], s[8:9]
	v_ashrrev_i32_e32 v163, 31, v162
	v_lshlrev_b64 v[108:109], 11, v[162:163]
	v_mad_i64_i32 v[106:107], s[36:37], v162, s64, v[4:5]
	s_mov_b64 s[36:37], -1
	s_and_b64 vcc, exec, s[6:7]
	v_lshl_add_u64 v[4:5], s[10:11], 0, v[108:109]
	s_cbranch_vccnz .LBB0_995
	v_lshl_add_u64 v[102:103], v[148:149], 1, v[106:107]
	v_add_co_u32_e32 v102, vcc, 0x2000, v102
	v_mov_b32_e32 v112, v99
	s_nop 0
	v_addc_co_u32_e32 v103, vcc, 0, v103, vcc
	v_mov_b32_e32 v113, v100
	v_pk_mov_b32 v[114:115], v[100:101], v[94:95] op_sel:[1,0]
	v_mov_b32_e32 v116, v95
	v_mov_b32_e32 v117, v96
	v_lshl_add_u64 v[110:111], s[10:11], 0, v[108:109]
	s_mov_b64 s[36:37], 0
	s_waitcnt vmcnt(4)
	v_mov_b32_e32 v102, v230
	v_mov_b32_e32 v103, v231
	v_mov_b32_e32 v104, v232
	v_mov_b32_e32 v105, v233
	v_cvt_f32_f16_e32 v3, v102
	v_cvt_f32_f16_sdwa v102, v102 dst_sel:DWORD dst_unused:UNUSED_PAD src0_sel:WORD_1
	v_cvt_f32_f16_e32 v118, v103
	v_cvt_f32_f16_sdwa v119, v103 dst_sel:DWORD dst_unused:UNUSED_PAD src0_sel:WORD_1
	v_cvt_f32_f16_e32 v120, v104
	v_cvt_f32_f16_sdwa v121, v104 dst_sel:DWORD dst_unused:UNUSED_PAD src0_sel:WORD_1
	v_cvt_f32_f16_e32 v122, v105
	v_cvt_f32_f16_sdwa v123, v105 dst_sel:DWORD dst_unused:UNUSED_PAD src0_sel:WORD_1
	v_max_f32_e32 v102, 0x38d1b717, v102
	v_max_f32_e32 v103, 0x38d1b717, v118
	v_max_f32_e32 v104, 0x38d1b717, v119
	v_max_f32_e32 v105, 0x38d1b717, v120
	v_max_f32_e32 v118, 0x38d1b717, v121
	v_max_f32_e32 v119, 0x38d1b717, v122
	v_max_f32_e32 v3, 0x38d1b717, v3
	v_pk_mul_f32 v[102:103], v[112:113], v[102:103]
	v_pk_mul_f32 v[104:105], v[114:115], v[104:105]
	v_pk_mul_f32 v[112:113], v[116:117], v[118:119]
	v_fma_mixlo_f16 v3, v98, v3, 0
	v_cvt_pk_f16_f32 v103, v102, v103
	v_cvt_pk_f16_f32 v104, v104, v105
	v_cvt_pk_f16_f32 v105, v112, v113
	v_max_f32_e32 v120, 0x38d1b717, v123
	v_pack_b32_f16 v102, v3, v103
	v_alignbit_b32 v103, v104, v103, 16
	v_alignbit_b32 v104, v105, v104, 16
	v_lshrrev_b32_e32 v105, 16, v105
	v_fma_mixhi_f16 v105, v97, v120, 0
.LBB0_995:
	s_andn2_b64 vcc, exec, s[36:37]
	v_lshl_add_u64 v[108:109], v[108:109], 0, s[18:19]
	s_cbranch_vccnz .LBB0_997
	s_lshl_b32 s0, s21, 1
	v_lshl_add_u64 v[102:103], v[106:107], 0, s[0:1]
	v_lshl_add_u64 v[102:103], v[148:149], 1, v[102:103]
	v_add_co_u32_e32 v102, vcc, 0x1000, v102
	s_add_u32 s36, s55, s34
	s_nop 0
	v_addc_co_u32_e32 v103, vcc, 0, v103, vcc
	s_addc_u32 s37, s56, s35
	v_lshl_add_u64 v[110:111], s[36:37], 0, v[108:109]
	s_waitcnt vmcnt(4)
	v_mov_b32_e32 v102, v230
	v_mov_b32_e32 v103, v231
	v_mov_b32_e32 v104, v232
	v_mov_b32_e32 v105, v233
	v_cvt_f32_f16_e32 v3, v102
	v_cvt_f32_f16_sdwa v102, v102 dst_sel:DWORD dst_unused:UNUSED_PAD src0_sel:WORD_1
	v_cvt_f32_f16_e32 v112, v103
	v_cvt_f32_f16_sdwa v103, v103 dst_sel:DWORD dst_unused:UNUSED_PAD src0_sel:WORD_1
	v_cvt_f32_f16_e32 v113, v104
	v_cvt_f32_f16_sdwa v104, v104 dst_sel:DWORD dst_unused:UNUSED_PAD src0_sel:WORD_1
	v_cvt_f32_f16_e32 v114, v105
	v_cvt_f32_f16_sdwa v105, v105 dst_sel:DWORD dst_unused:UNUSED_PAD src0_sel:WORD_1
	v_max_f32_e32 v115, 0x38d1b717, v3
	v_max_f32_e32 v116, 0x38d1b717, v102
	v_max_f32_e32 v117, 0x38d1b717, v112
	v_max_f32_e32 v118, 0x38d1b717, v103
	v_max_f32_e32 v119, 0x38d1b717, v113
	v_max_f32_e32 v120, 0x38d1b717, v104
	v_max_f32_e32 v121, 0x38d1b717, v114
	v_max_f32_e32 v122, 0x38d1b717, v105
	v_cndmask_b32_e64 v3, v115, v3, s[4:5]
	v_cndmask_b32_e64 v102, v116, v102, s[4:5]
	v_cndmask_b32_e64 v112, v117, v112, s[4:5]
	v_cndmask_b32_e64 v103, v118, v103, s[4:5]
	v_cndmask_b32_e64 v113, v119, v113, s[4:5]
	v_cndmask_b32_e64 v104, v120, v104, s[4:5]
	v_cndmask_b32_e64 v114, v121, v114, s[4:5]
	v_cndmask_b32_e64 v105, v122, v105, s[4:5]
	v_mul_f32_e32 v96, v96, v114
	v_mul_f32_e32 v95, v95, v104
	v_mul_f32_e32 v94, v94, v113
	v_mul_f32_e32 v101, v101, v103
	v_mul_f32_e32 v100, v100, v112
	v_mul_f32_e32 v99, v99, v102
	v_mul_f32_e32 v3, v98, v3
	v_mul_f32_e32 v97, v97, v105
	v_cvt_pk_f16_f32 v102, v3, v99
	v_cvt_pk_f16_f32 v103, v100, v101
	v_cvt_pk_f16_f32 v104, v94, v95
	v_cvt_pk_f16_f32 v105, v96, v97
.LBB0_997:
	v_lshl_add_u64 v[94:95], v[148:149], 1, v[110:111]
	s_and_b64 vcc, exec, s[6:7]
	s_mov_b64 s[36:37], -1
	global_store_dwordx4 v[94:95], v[102:105], off
	v_mul_u32_u24_e32 v240, 0x3000, v160
	v_add_u32_e32 v240, v240, v213
	v_mov_b32_e32 v241, 0
	v_lshl_add_u64 v[238:239], v[150:151], 1, v[240:241]
	v_lshl_add_u64 v[238:239], s[8:9], 0, v[238:239]
	global_load_dwordx4 v[230:233], v[238:239], off
	s_cbranch_vccnz .LBB0_999
	v_lshl_add_u64 v[94:95], v[150:151], 1, v[106:107]
	v_add_co_u32_e32 v94, vcc, 0x2000, v94
	v_mov_b32_e32 v98, v91
	s_nop 0
	v_addc_co_u32_e32 v95, vcc, 0, v95, vcc
	v_mov_b32_e32 v99, v92
	v_pk_mov_b32 v[100:101], v[92:93], v[86:87] op_sel:[1,0]
	v_mov_b32_e32 v102, v87
	v_mov_b32_e32 v103, v88
	s_mov_b64 s[36:37], 0
	s_waitcnt vmcnt(4)
	v_mov_b32_e32 v94, v234
	v_mov_b32_e32 v95, v235
	v_mov_b32_e32 v96, v236
	v_mov_b32_e32 v97, v237
	v_cvt_f32_f16_e32 v3, v94
	v_cvt_f32_f16_sdwa v94, v94 dst_sel:DWORD dst_unused:UNUSED_PAD src0_sel:WORD_1
	v_cvt_f32_f16_e32 v104, v95
	v_cvt_f32_f16_sdwa v105, v95 dst_sel:DWORD dst_unused:UNUSED_PAD src0_sel:WORD_1
	v_cvt_f32_f16_e32 v110, v96
	v_cvt_f32_f16_sdwa v111, v96 dst_sel:DWORD dst_unused:UNUSED_PAD src0_sel:WORD_1
	v_cvt_f32_f16_e32 v112, v97
	v_cvt_f32_f16_sdwa v113, v97 dst_sel:DWORD dst_unused:UNUSED_PAD src0_sel:WORD_1
	v_max_f32_e32 v94, 0x38d1b717, v94
	v_max_f32_e32 v95, 0x38d1b717, v104
	v_max_f32_e32 v96, 0x38d1b717, v105
	v_max_f32_e32 v97, 0x38d1b717, v110
	v_max_f32_e32 v104, 0x38d1b717, v111
	v_max_f32_e32 v105, 0x38d1b717, v112
	v_max_f32_e32 v3, 0x38d1b717, v3
	v_pk_mul_f32 v[94:95], v[98:99], v[94:95]
	v_pk_mul_f32 v[96:97], v[100:101], v[96:97]
	v_pk_mul_f32 v[98:99], v[102:103], v[104:105]
	v_fma_mixlo_f16 v3, v90, v3, 0
	v_cvt_pk_f16_f32 v95, v94, v95
	v_cvt_pk_f16_f32 v96, v96, v97
	v_cvt_pk_f16_f32 v97, v98, v99
	v_max_f32_e32 v110, 0x38d1b717, v113
	v_pack_b32_f16 v94, v3, v95
	v_alignbit_b32 v95, v96, v95, 16
	v_alignbit_b32 v96, v97, v96, 16
	v_lshrrev_b32_e32 v97, 16, v97
	v_fma_mixhi_f16 v97, v89, v110, 0
.LBB0_999:
	s_andn2_b64 vcc, exec, s[36:37]
	s_cbranch_vccnz .LBB0_1001
	s_lshl_b32 s0, s21, 1
	v_lshl_add_u64 v[4:5], v[106:107], 0, s[0:1]
	v_lshl_add_u64 v[4:5], v[148:149], 1, v[4:5]
	v_add_co_u32_e32 v4, vcc, 0x1000, v4
	s_add_u32 s36, s55, s34
	s_nop 0
	v_addc_co_u32_e32 v5, vcc, 0, v5, vcc
	s_addc_u32 s37, s56, s35
	v_lshl_add_u64 v[4:5], s[36:37], 0, v[108:109]
	s_waitcnt vmcnt(4)
	v_mov_b32_e32 v94, v234
	v_mov_b32_e32 v95, v235
	v_mov_b32_e32 v96, v236
	v_mov_b32_e32 v97, v237
	v_cvt_f32_f16_e32 v3, v94
	v_cvt_f32_f16_sdwa v94, v94 dst_sel:DWORD dst_unused:UNUSED_PAD src0_sel:WORD_1
	v_cvt_f32_f16_e32 v98, v95
	v_cvt_f32_f16_sdwa v95, v95 dst_sel:DWORD dst_unused:UNUSED_PAD src0_sel:WORD_1
	v_cvt_f32_f16_e32 v99, v96
	v_cvt_f32_f16_sdwa v96, v96 dst_sel:DWORD dst_unused:UNUSED_PAD src0_sel:WORD_1
	v_cvt_f32_f16_e32 v100, v97
	v_cvt_f32_f16_sdwa v97, v97 dst_sel:DWORD dst_unused:UNUSED_PAD src0_sel:WORD_1
	v_max_f32_e32 v101, 0x38d1b717, v3
	v_max_f32_e32 v102, 0x38d1b717, v94
	v_max_f32_e32 v103, 0x38d1b717, v98
	v_max_f32_e32 v104, 0x38d1b717, v95
	v_max_f32_e32 v105, 0x38d1b717, v99
	v_max_f32_e32 v106, 0x38d1b717, v96
	v_max_f32_e32 v107, 0x38d1b717, v100
	v_max_f32_e32 v108, 0x38d1b717, v97
	v_cndmask_b32_e64 v3, v101, v3, s[4:5]
	v_cndmask_b32_e64 v94, v102, v94, s[4:5]
	v_cndmask_b32_e64 v98, v103, v98, s[4:5]
	v_cndmask_b32_e64 v95, v104, v95, s[4:5]
	v_cndmask_b32_e64 v99, v105, v99, s[4:5]
	v_cndmask_b32_e64 v96, v106, v96, s[4:5]
	v_cndmask_b32_e64 v100, v107, v100, s[4:5]
	v_cndmask_b32_e64 v97, v108, v97, s[4:5]
	v_mul_f32_e32 v88, v88, v100
	v_mul_f32_e32 v87, v87, v96
	v_mul_f32_e32 v86, v86, v99
	v_mul_f32_e32 v93, v93, v95
	v_mul_f32_e32 v92, v92, v98
	v_mul_f32_e32 v91, v91, v94
	v_mul_f32_e32 v3, v90, v3
	v_mul_f32_e32 v89, v89, v97
	v_cvt_pk_f16_f32 v94, v3, v91
	v_cvt_pk_f16_f32 v95, v92, v93
	v_cvt_pk_f16_f32 v96, v86, v87
	v_cvt_pk_f16_f32 v97, v88, v89
.LBB0_1001:
	v_lshl_add_u64 v[4:5], v[148:149], 1, v[4:5]
	global_store_dwordx4 v[4:5], v[94:97], off offset:256
	v_mul_u32_u24_e32 v240, 0x3000, v158
	v_add_u32_e32 v240, v240, v213
	v_mov_b32_e32 v241, 0
	v_lshl_add_u64 v[238:239], v[148:149], 1, v[240:241]
	v_lshl_add_u64 v[238:239], s[8:9], 0, v[238:239]
	global_load_dwordx4 v[234:237], v[238:239], off
	v_mov_b64_e32 v[4:5], s[8:9]
	v_ashrrev_i32_e32 v161, 31, v160
	v_lshlrev_b64 v[92:93], 11, v[160:161]
	v_mad_i64_i32 v[90:91], s[36:37], v160, s64, v[4:5]
	s_mov_b64 s[36:37], -1
	s_and_b64 vcc, exec, s[6:7]
	v_lshl_add_u64 v[4:5], s[10:11], 0, v[92:93]
	s_cbranch_vccnz .LBB0_1003
	v_lshl_add_u64 v[86:87], v[148:149], 1, v[90:91]
	v_add_co_u32_e32 v86, vcc, 0x2000, v86
	v_mov_b32_e32 v96, v83
	s_nop 0
	v_addc_co_u32_e32 v87, vcc, 0, v87, vcc
	v_mov_b32_e32 v97, v84
	v_pk_mov_b32 v[98:99], v[84:85], v[78:79] op_sel:[1,0]
	v_mov_b32_e32 v100, v79
	v_mov_b32_e32 v101, v80
	v_lshl_add_u64 v[94:95], s[10:11], 0, v[92:93]
	s_mov_b64 s[36:37], 0
	s_waitcnt vmcnt(4)
	v_mov_b32_e32 v86, v226
	v_mov_b32_e32 v87, v227
	v_mov_b32_e32 v88, v228
	v_mov_b32_e32 v89, v229
	v_cvt_f32_f16_e32 v3, v86
	v_cvt_f32_f16_sdwa v86, v86 dst_sel:DWORD dst_unused:UNUSED_PAD src0_sel:WORD_1
	v_cvt_f32_f16_e32 v102, v87
	v_cvt_f32_f16_sdwa v103, v87 dst_sel:DWORD dst_unused:UNUSED_PAD src0_sel:WORD_1
	v_cvt_f32_f16_e32 v104, v88
	v_cvt_f32_f16_sdwa v105, v88 dst_sel:DWORD dst_unused:UNUSED_PAD src0_sel:WORD_1
	v_cvt_f32_f16_e32 v106, v89
	v_cvt_f32_f16_sdwa v107, v89 dst_sel:DWORD dst_unused:UNUSED_PAD src0_sel:WORD_1
	v_max_f32_e32 v86, 0x38d1b717, v86
	v_max_f32_e32 v87, 0x38d1b717, v102
	v_max_f32_e32 v88, 0x38d1b717, v103
	v_max_f32_e32 v89, 0x38d1b717, v104
	v_max_f32_e32 v102, 0x38d1b717, v105
	v_max_f32_e32 v103, 0x38d1b717, v106
	v_max_f32_e32 v3, 0x38d1b717, v3
	v_pk_mul_f32 v[86:87], v[96:97], v[86:87]
	v_pk_mul_f32 v[88:89], v[98:99], v[88:89]
	v_pk_mul_f32 v[96:97], v[100:101], v[102:103]
	v_fma_mixlo_f16 v3, v82, v3, 0
	v_cvt_pk_f16_f32 v87, v86, v87
	v_cvt_pk_f16_f32 v88, v88, v89
	v_cvt_pk_f16_f32 v89, v96, v97
	v_max_f32_e32 v104, 0x38d1b717, v107
	v_pack_b32_f16 v86, v3, v87
	v_alignbit_b32 v87, v88, v87, 16
	v_alignbit_b32 v88, v89, v88, 16
	v_lshrrev_b32_e32 v89, 16, v89
	v_fma_mixhi_f16 v89, v81, v104, 0
.LBB0_1003:
	s_andn2_b64 vcc, exec, s[36:37]
	v_lshl_add_u64 v[92:93], v[92:93], 0, s[18:19]
	s_cbranch_vccnz .LBB0_1005
	s_lshl_b32 s0, s21, 1
	v_lshl_add_u64 v[86:87], v[90:91], 0, s[0:1]
	v_lshl_add_u64 v[86:87], v[148:149], 1, v[86:87]
	v_add_co_u32_e32 v86, vcc, 0x1000, v86
	s_add_u32 s36, s55, s34
	s_nop 0
	v_addc_co_u32_e32 v87, vcc, 0, v87, vcc
	s_addc_u32 s37, s56, s35
	v_lshl_add_u64 v[94:95], s[36:37], 0, v[92:93]
	s_waitcnt vmcnt(4)
	v_mov_b32_e32 v86, v226
	v_mov_b32_e32 v87, v227
	v_mov_b32_e32 v88, v228
	v_mov_b32_e32 v89, v229
	v_cvt_f32_f16_e32 v3, v86
	v_cvt_f32_f16_sdwa v86, v86 dst_sel:DWORD dst_unused:UNUSED_PAD src0_sel:WORD_1
	v_cvt_f32_f16_e32 v96, v87
	v_cvt_f32_f16_sdwa v87, v87 dst_sel:DWORD dst_unused:UNUSED_PAD src0_sel:WORD_1
	v_cvt_f32_f16_e32 v97, v88
	v_cvt_f32_f16_sdwa v88, v88 dst_sel:DWORD dst_unused:UNUSED_PAD src0_sel:WORD_1
	v_cvt_f32_f16_e32 v98, v89
	v_cvt_f32_f16_sdwa v89, v89 dst_sel:DWORD dst_unused:UNUSED_PAD src0_sel:WORD_1
	v_max_f32_e32 v99, 0x38d1b717, v3
	v_max_f32_e32 v100, 0x38d1b717, v86
	v_max_f32_e32 v101, 0x38d1b717, v96
	v_max_f32_e32 v102, 0x38d1b717, v87
	v_max_f32_e32 v103, 0x38d1b717, v97
	v_max_f32_e32 v104, 0x38d1b717, v88
	v_max_f32_e32 v105, 0x38d1b717, v98
	v_max_f32_e32 v106, 0x38d1b717, v89
	v_cndmask_b32_e64 v3, v99, v3, s[4:5]
	v_cndmask_b32_e64 v86, v100, v86, s[4:5]
	v_cndmask_b32_e64 v96, v101, v96, s[4:5]
	v_cndmask_b32_e64 v87, v102, v87, s[4:5]
	v_cndmask_b32_e64 v97, v103, v97, s[4:5]
	v_cndmask_b32_e64 v88, v104, v88, s[4:5]
	v_cndmask_b32_e64 v98, v105, v98, s[4:5]
	v_cndmask_b32_e64 v89, v106, v89, s[4:5]
	v_mul_f32_e32 v80, v80, v98
	v_mul_f32_e32 v79, v79, v88
	v_mul_f32_e32 v78, v78, v97
	v_mul_f32_e32 v85, v85, v87
	v_mul_f32_e32 v84, v84, v96
	v_mul_f32_e32 v83, v83, v86
	v_mul_f32_e32 v3, v82, v3
	v_mul_f32_e32 v81, v81, v89
	v_cvt_pk_f16_f32 v86, v3, v83
	v_cvt_pk_f16_f32 v87, v84, v85
	v_cvt_pk_f16_f32 v88, v78, v79
	v_cvt_pk_f16_f32 v89, v80, v81
.LBB0_1005:
	v_lshl_add_u64 v[78:79], v[148:149], 1, v[94:95]
	s_and_b64 vcc, exec, s[6:7]
	s_mov_b64 s[36:37], -1
	global_store_dwordx4 v[78:79], v[86:89], off
	v_mul_u32_u24_e32 v240, 0x3000, v158
	v_add_u32_e32 v240, v240, v213
	v_mov_b32_e32 v241, 0
	v_lshl_add_u64 v[238:239], v[150:151], 1, v[240:241]
	v_lshl_add_u64 v[238:239], s[8:9], 0, v[238:239]
	global_load_dwordx4 v[226:229], v[238:239], off
	s_cbranch_vccnz .LBB0_1007
	v_lshl_add_u64 v[78:79], v[150:151], 1, v[90:91]
	v_add_co_u32_e32 v78, vcc, 0x2000, v78
	v_mov_b32_e32 v82, v75
	s_nop 0
	v_addc_co_u32_e32 v79, vcc, 0, v79, vcc
	v_mov_b32_e32 v83, v76
	v_pk_mov_b32 v[84:85], v[76:77], v[70:71] op_sel:[1,0]
	v_mov_b32_e32 v86, v71
	v_mov_b32_e32 v87, v72
	s_mov_b64 s[36:37], 0
	s_waitcnt vmcnt(4)
	v_mov_b32_e32 v78, v230
	v_mov_b32_e32 v79, v231
	v_mov_b32_e32 v80, v232
	v_mov_b32_e32 v81, v233
	v_cvt_f32_f16_e32 v3, v78
	v_cvt_f32_f16_sdwa v78, v78 dst_sel:DWORD dst_unused:UNUSED_PAD src0_sel:WORD_1
	v_cvt_f32_f16_e32 v88, v79
	v_cvt_f32_f16_sdwa v89, v79 dst_sel:DWORD dst_unused:UNUSED_PAD src0_sel:WORD_1
	v_cvt_f32_f16_e32 v94, v80
	v_cvt_f32_f16_sdwa v95, v80 dst_sel:DWORD dst_unused:UNUSED_PAD src0_sel:WORD_1
	v_cvt_f32_f16_e32 v96, v81
	v_cvt_f32_f16_sdwa v97, v81 dst_sel:DWORD dst_unused:UNUSED_PAD src0_sel:WORD_1
	v_max_f32_e32 v78, 0x38d1b717, v78
	v_max_f32_e32 v79, 0x38d1b717, v88
	v_max_f32_e32 v80, 0x38d1b717, v89
	v_max_f32_e32 v81, 0x38d1b717, v94
	v_max_f32_e32 v88, 0x38d1b717, v95
	v_max_f32_e32 v89, 0x38d1b717, v96
	v_max_f32_e32 v3, 0x38d1b717, v3
	v_pk_mul_f32 v[78:79], v[82:83], v[78:79]
	v_pk_mul_f32 v[80:81], v[84:85], v[80:81]
	v_pk_mul_f32 v[82:83], v[86:87], v[88:89]
	v_fma_mixlo_f16 v3, v74, v3, 0
	v_cvt_pk_f16_f32 v79, v78, v79
	v_cvt_pk_f16_f32 v80, v80, v81
	v_cvt_pk_f16_f32 v81, v82, v83
	v_max_f32_e32 v94, 0x38d1b717, v97
	v_pack_b32_f16 v78, v3, v79
	v_alignbit_b32 v79, v80, v79, 16
	v_alignbit_b32 v80, v81, v80, 16
	v_lshrrev_b32_e32 v81, 16, v81
	v_fma_mixhi_f16 v81, v73, v94, 0
.LBB0_1007:
	s_andn2_b64 vcc, exec, s[36:37]
	s_cbranch_vccnz .LBB0_1009
	s_lshl_b32 s0, s21, 1
	v_lshl_add_u64 v[4:5], v[90:91], 0, s[0:1]
	v_lshl_add_u64 v[4:5], v[148:149], 1, v[4:5]
	v_add_co_u32_e32 v4, vcc, 0x1000, v4
	s_add_u32 s36, s55, s34
	s_nop 0
	v_addc_co_u32_e32 v5, vcc, 0, v5, vcc
	s_addc_u32 s37, s56, s35
	v_lshl_add_u64 v[4:5], s[36:37], 0, v[92:93]
	s_waitcnt vmcnt(4)
	v_mov_b32_e32 v78, v230
	v_mov_b32_e32 v79, v231
	v_mov_b32_e32 v80, v232
	v_mov_b32_e32 v81, v233
	v_cvt_f32_f16_e32 v3, v78
	v_cvt_f32_f16_sdwa v78, v78 dst_sel:DWORD dst_unused:UNUSED_PAD src0_sel:WORD_1
	v_cvt_f32_f16_e32 v82, v79
	v_cvt_f32_f16_sdwa v79, v79 dst_sel:DWORD dst_unused:UNUSED_PAD src0_sel:WORD_1
	v_cvt_f32_f16_e32 v83, v80
	v_cvt_f32_f16_sdwa v80, v80 dst_sel:DWORD dst_unused:UNUSED_PAD src0_sel:WORD_1
	v_cvt_f32_f16_e32 v84, v81
	v_cvt_f32_f16_sdwa v81, v81 dst_sel:DWORD dst_unused:UNUSED_PAD src0_sel:WORD_1
	v_max_f32_e32 v85, 0x38d1b717, v3
	v_max_f32_e32 v86, 0x38d1b717, v78
	v_max_f32_e32 v87, 0x38d1b717, v82
	v_max_f32_e32 v88, 0x38d1b717, v79
	v_max_f32_e32 v89, 0x38d1b717, v83
	v_max_f32_e32 v90, 0x38d1b717, v80
	v_max_f32_e32 v91, 0x38d1b717, v84
	v_max_f32_e32 v92, 0x38d1b717, v81
	v_cndmask_b32_e64 v3, v85, v3, s[4:5]
	v_cndmask_b32_e64 v78, v86, v78, s[4:5]
	v_cndmask_b32_e64 v82, v87, v82, s[4:5]
	v_cndmask_b32_e64 v79, v88, v79, s[4:5]
	v_cndmask_b32_e64 v83, v89, v83, s[4:5]
	v_cndmask_b32_e64 v80, v90, v80, s[4:5]
	v_cndmask_b32_e64 v84, v91, v84, s[4:5]
	v_cndmask_b32_e64 v81, v92, v81, s[4:5]
	v_mul_f32_e32 v72, v72, v84
	v_mul_f32_e32 v71, v71, v80
	v_mul_f32_e32 v70, v70, v83
	v_mul_f32_e32 v77, v77, v79
	v_mul_f32_e32 v76, v76, v82
	v_mul_f32_e32 v75, v75, v78
	v_mul_f32_e32 v3, v74, v3
	v_mul_f32_e32 v73, v73, v81
	v_cvt_pk_f16_f32 v78, v3, v75
	v_cvt_pk_f16_f32 v79, v76, v77
	v_cvt_pk_f16_f32 v80, v70, v71
	v_cvt_pk_f16_f32 v81, v72, v73
.LBB0_1009:
	v_lshl_add_u64 v[4:5], v[148:149], 1, v[4:5]
	global_store_dwordx4 v[4:5], v[78:81], off offset:256
	v_mul_u32_u24_e32 v240, 0x3000, v156
	v_add_u32_e32 v240, v240, v213
	v_mov_b32_e32 v241, 0
	v_lshl_add_u64 v[238:239], v[148:149], 1, v[240:241]
	v_lshl_add_u64 v[238:239], s[8:9], 0, v[238:239]
	global_load_dwordx4 v[230:233], v[238:239], off
	v_mov_b64_e32 v[4:5], s[8:9]
	v_ashrrev_i32_e32 v159, 31, v158
	v_lshlrev_b64 v[76:77], 11, v[158:159]
	v_mad_i64_i32 v[74:75], s[36:37], v158, s64, v[4:5]
	s_mov_b64 s[36:37], -1
	s_and_b64 vcc, exec, s[6:7]
	v_lshl_add_u64 v[4:5], s[10:11], 0, v[76:77]
	s_cbranch_vccnz .LBB0_1011
	v_lshl_add_u64 v[70:71], v[148:149], 1, v[74:75]
	v_add_co_u32_e32 v70, vcc, 0x2000, v70
	v_mov_b32_e32 v80, v67
	s_nop 0
	v_addc_co_u32_e32 v71, vcc, 0, v71, vcc
	v_mov_b32_e32 v81, v68
	v_pk_mov_b32 v[82:83], v[68:69], v[62:63] op_sel:[1,0]
	v_mov_b32_e32 v84, v63
	v_mov_b32_e32 v85, v64
	v_lshl_add_u64 v[78:79], s[10:11], 0, v[76:77]
	s_mov_b64 s[36:37], 0
	s_waitcnt vmcnt(4)
	v_mov_b32_e32 v70, v234
	v_mov_b32_e32 v71, v235
	v_mov_b32_e32 v72, v236
	v_mov_b32_e32 v73, v237
	v_cvt_f32_f16_e32 v3, v70
	v_cvt_f32_f16_sdwa v70, v70 dst_sel:DWORD dst_unused:UNUSED_PAD src0_sel:WORD_1
	v_cvt_f32_f16_e32 v86, v71
	v_cvt_f32_f16_sdwa v87, v71 dst_sel:DWORD dst_unused:UNUSED_PAD src0_sel:WORD_1
	v_cvt_f32_f16_e32 v88, v72
	v_cvt_f32_f16_sdwa v89, v72 dst_sel:DWORD dst_unused:UNUSED_PAD src0_sel:WORD_1
	v_cvt_f32_f16_e32 v90, v73
	v_cvt_f32_f16_sdwa v91, v73 dst_sel:DWORD dst_unused:UNUSED_PAD src0_sel:WORD_1
	v_max_f32_e32 v70, 0x38d1b717, v70
	v_max_f32_e32 v71, 0x38d1b717, v86
	v_max_f32_e32 v72, 0x38d1b717, v87
	v_max_f32_e32 v73, 0x38d1b717, v88
	v_max_f32_e32 v86, 0x38d1b717, v89
	v_max_f32_e32 v87, 0x38d1b717, v90
	v_max_f32_e32 v3, 0x38d1b717, v3
	v_pk_mul_f32 v[70:71], v[80:81], v[70:71]
	v_pk_mul_f32 v[72:73], v[82:83], v[72:73]
	v_pk_mul_f32 v[80:81], v[84:85], v[86:87]
	v_fma_mixlo_f16 v3, v66, v3, 0
	v_cvt_pk_f16_f32 v71, v70, v71
	v_cvt_pk_f16_f32 v72, v72, v73
	v_cvt_pk_f16_f32 v73, v80, v81
	v_max_f32_e32 v88, 0x38d1b717, v91
	v_pack_b32_f16 v70, v3, v71
	v_alignbit_b32 v71, v72, v71, 16
	v_alignbit_b32 v72, v73, v72, 16
	v_lshrrev_b32_e32 v73, 16, v73
	v_fma_mixhi_f16 v73, v65, v88, 0
.LBB0_1011:
	s_andn2_b64 vcc, exec, s[36:37]
	v_lshl_add_u64 v[76:77], v[76:77], 0, s[18:19]
	s_cbranch_vccnz .LBB0_1013
	s_lshl_b32 s0, s21, 1
	v_lshl_add_u64 v[70:71], v[74:75], 0, s[0:1]
	v_lshl_add_u64 v[70:71], v[148:149], 1, v[70:71]
	v_add_co_u32_e32 v70, vcc, 0x1000, v70
	s_add_u32 s36, s55, s34
	s_nop 0
	v_addc_co_u32_e32 v71, vcc, 0, v71, vcc
	s_addc_u32 s37, s56, s35
	v_lshl_add_u64 v[78:79], s[36:37], 0, v[76:77]
	s_waitcnt vmcnt(4)
	v_mov_b32_e32 v70, v234
	v_mov_b32_e32 v71, v235
	v_mov_b32_e32 v72, v236
	v_mov_b32_e32 v73, v237
	v_cvt_f32_f16_e32 v3, v70
	v_cvt_f32_f16_sdwa v70, v70 dst_sel:DWORD dst_unused:UNUSED_PAD src0_sel:WORD_1
	v_cvt_f32_f16_e32 v80, v71
	v_cvt_f32_f16_sdwa v71, v71 dst_sel:DWORD dst_unused:UNUSED_PAD src0_sel:WORD_1
	v_cvt_f32_f16_e32 v81, v72
	v_cvt_f32_f16_sdwa v72, v72 dst_sel:DWORD dst_unused:UNUSED_PAD src0_sel:WORD_1
	v_cvt_f32_f16_e32 v82, v73
	v_cvt_f32_f16_sdwa v73, v73 dst_sel:DWORD dst_unused:UNUSED_PAD src0_sel:WORD_1
	v_max_f32_e32 v83, 0x38d1b717, v3
	v_max_f32_e32 v84, 0x38d1b717, v70
	v_max_f32_e32 v85, 0x38d1b717, v80
	v_max_f32_e32 v86, 0x38d1b717, v71
	v_max_f32_e32 v87, 0x38d1b717, v81
	v_max_f32_e32 v88, 0x38d1b717, v72
	v_max_f32_e32 v89, 0x38d1b717, v82
	v_max_f32_e32 v90, 0x38d1b717, v73
	v_cndmask_b32_e64 v3, v83, v3, s[4:5]
	v_cndmask_b32_e64 v70, v84, v70, s[4:5]
	v_cndmask_b32_e64 v80, v85, v80, s[4:5]
	v_cndmask_b32_e64 v71, v86, v71, s[4:5]
	v_cndmask_b32_e64 v81, v87, v81, s[4:5]
	v_cndmask_b32_e64 v72, v88, v72, s[4:5]
	v_cndmask_b32_e64 v82, v89, v82, s[4:5]
	v_cndmask_b32_e64 v73, v90, v73, s[4:5]
	v_mul_f32_e32 v64, v64, v82
	v_mul_f32_e32 v63, v63, v72
	v_mul_f32_e32 v62, v62, v81
	v_mul_f32_e32 v69, v69, v71
	v_mul_f32_e32 v68, v68, v80
	v_mul_f32_e32 v67, v67, v70
	v_mul_f32_e32 v3, v66, v3
	v_mul_f32_e32 v65, v65, v73
	v_cvt_pk_f16_f32 v70, v3, v67
	v_cvt_pk_f16_f32 v71, v68, v69
	v_cvt_pk_f16_f32 v72, v62, v63
	v_cvt_pk_f16_f32 v73, v64, v65
.LBB0_1013:
	v_lshl_add_u64 v[62:63], v[148:149], 1, v[78:79]
	s_and_b64 vcc, exec, s[6:7]
	s_mov_b64 s[36:37], -1
	global_store_dwordx4 v[62:63], v[70:73], off
	v_mul_u32_u24_e32 v240, 0x3000, v156
	v_add_u32_e32 v240, v240, v213
	v_mov_b32_e32 v241, 0
	v_lshl_add_u64 v[238:239], v[150:151], 1, v[240:241]
	v_lshl_add_u64 v[238:239], s[8:9], 0, v[238:239]
	global_load_dwordx4 v[234:237], v[238:239], off
	s_cbranch_vccnz .LBB0_1015
	v_lshl_add_u64 v[62:63], v[150:151], 1, v[74:75]
	v_add_co_u32_e32 v62, vcc, 0x2000, v62
	v_mov_b32_e32 v66, v59
	s_nop 0
	v_addc_co_u32_e32 v63, vcc, 0, v63, vcc
	v_mov_b32_e32 v67, v60
	v_pk_mov_b32 v[68:69], v[60:61], v[54:55] op_sel:[1,0]
	v_mov_b32_e32 v70, v55
	v_mov_b32_e32 v71, v56
	s_mov_b64 s[36:37], 0
	s_waitcnt vmcnt(4)
	v_mov_b32_e32 v62, v226
	v_mov_b32_e32 v63, v227
	v_mov_b32_e32 v64, v228
	v_mov_b32_e32 v65, v229
	v_cvt_f32_f16_e32 v3, v62
	v_cvt_f32_f16_sdwa v62, v62 dst_sel:DWORD dst_unused:UNUSED_PAD src0_sel:WORD_1
	v_cvt_f32_f16_e32 v72, v63
	v_cvt_f32_f16_sdwa v73, v63 dst_sel:DWORD dst_unused:UNUSED_PAD src0_sel:WORD_1
	v_cvt_f32_f16_e32 v78, v64
	v_cvt_f32_f16_sdwa v79, v64 dst_sel:DWORD dst_unused:UNUSED_PAD src0_sel:WORD_1
	v_cvt_f32_f16_e32 v80, v65
	v_cvt_f32_f16_sdwa v81, v65 dst_sel:DWORD dst_unused:UNUSED_PAD src0_sel:WORD_1
	v_max_f32_e32 v62, 0x38d1b717, v62
	v_max_f32_e32 v63, 0x38d1b717, v72
	v_max_f32_e32 v64, 0x38d1b717, v73
	v_max_f32_e32 v65, 0x38d1b717, v78
	v_max_f32_e32 v72, 0x38d1b717, v79
	v_max_f32_e32 v73, 0x38d1b717, v80
	v_max_f32_e32 v3, 0x38d1b717, v3
	v_pk_mul_f32 v[62:63], v[66:67], v[62:63]
	v_pk_mul_f32 v[64:65], v[68:69], v[64:65]
	v_pk_mul_f32 v[66:67], v[70:71], v[72:73]
	v_fma_mixlo_f16 v3, v58, v3, 0
	v_cvt_pk_f16_f32 v63, v62, v63
	v_cvt_pk_f16_f32 v64, v64, v65
	v_cvt_pk_f16_f32 v65, v66, v67
	v_max_f32_e32 v78, 0x38d1b717, v81
	v_pack_b32_f16 v62, v3, v63
	v_alignbit_b32 v63, v64, v63, 16
	v_alignbit_b32 v64, v65, v64, 16
	v_lshrrev_b32_e32 v65, 16, v65
	v_fma_mixhi_f16 v65, v57, v78, 0
.LBB0_1015:
	s_andn2_b64 vcc, exec, s[36:37]
	s_cbranch_vccnz .LBB0_1017
	s_lshl_b32 s0, s21, 1
	v_lshl_add_u64 v[4:5], v[74:75], 0, s[0:1]
	v_lshl_add_u64 v[4:5], v[148:149], 1, v[4:5]
	v_add_co_u32_e32 v4, vcc, 0x1000, v4
	s_add_u32 s36, s55, s34
	s_nop 0
	v_addc_co_u32_e32 v5, vcc, 0, v5, vcc
	s_addc_u32 s37, s56, s35
	v_lshl_add_u64 v[4:5], s[36:37], 0, v[76:77]
	s_waitcnt vmcnt(4)
	v_mov_b32_e32 v62, v226
	v_mov_b32_e32 v63, v227
	v_mov_b32_e32 v64, v228
	v_mov_b32_e32 v65, v229
	v_cvt_f32_f16_e32 v3, v62
	v_cvt_f32_f16_sdwa v62, v62 dst_sel:DWORD dst_unused:UNUSED_PAD src0_sel:WORD_1
	v_cvt_f32_f16_e32 v66, v63
	v_cvt_f32_f16_sdwa v63, v63 dst_sel:DWORD dst_unused:UNUSED_PAD src0_sel:WORD_1
	v_cvt_f32_f16_e32 v67, v64
	v_cvt_f32_f16_sdwa v64, v64 dst_sel:DWORD dst_unused:UNUSED_PAD src0_sel:WORD_1
	v_cvt_f32_f16_e32 v68, v65
	v_cvt_f32_f16_sdwa v65, v65 dst_sel:DWORD dst_unused:UNUSED_PAD src0_sel:WORD_1
	v_max_f32_e32 v69, 0x38d1b717, v3
	v_max_f32_e32 v70, 0x38d1b717, v62
	v_max_f32_e32 v71, 0x38d1b717, v66
	v_max_f32_e32 v72, 0x38d1b717, v63
	v_max_f32_e32 v73, 0x38d1b717, v67
	v_max_f32_e32 v74, 0x38d1b717, v64
	v_max_f32_e32 v75, 0x38d1b717, v68
	v_max_f32_e32 v76, 0x38d1b717, v65
	v_cndmask_b32_e64 v3, v69, v3, s[4:5]
	v_cndmask_b32_e64 v62, v70, v62, s[4:5]
	v_cndmask_b32_e64 v66, v71, v66, s[4:5]
	v_cndmask_b32_e64 v63, v72, v63, s[4:5]
	v_cndmask_b32_e64 v67, v73, v67, s[4:5]
	v_cndmask_b32_e64 v64, v74, v64, s[4:5]
	v_cndmask_b32_e64 v68, v75, v68, s[4:5]
	v_cndmask_b32_e64 v65, v76, v65, s[4:5]
	v_mul_f32_e32 v56, v56, v68
	v_mul_f32_e32 v55, v55, v64
	v_mul_f32_e32 v54, v54, v67
	v_mul_f32_e32 v61, v61, v63
	v_mul_f32_e32 v60, v60, v66
	v_mul_f32_e32 v59, v59, v62
	v_mul_f32_e32 v3, v58, v3
	v_mul_f32_e32 v57, v57, v65
	v_cvt_pk_f16_f32 v62, v3, v59
	v_cvt_pk_f16_f32 v63, v60, v61
	v_cvt_pk_f16_f32 v64, v54, v55
	v_cvt_pk_f16_f32 v65, v56, v57
.LBB0_1017:
	v_lshl_add_u64 v[4:5], v[148:149], 1, v[4:5]
	global_store_dwordx4 v[4:5], v[62:65], off offset:256
	v_mul_u32_u24_e32 v240, 0x3000, v154
	v_add_u32_e32 v240, v240, v213
	v_mov_b32_e32 v241, 0
	v_lshl_add_u64 v[238:239], v[148:149], 1, v[240:241]
	v_lshl_add_u64 v[238:239], s[8:9], 0, v[238:239]
	global_load_dwordx4 v[226:229], v[238:239], off
	v_mov_b64_e32 v[4:5], s[8:9]
	v_ashrrev_i32_e32 v157, 31, v156
	v_lshlrev_b64 v[60:61], 11, v[156:157]
	v_mad_i64_i32 v[58:59], s[36:37], v156, s64, v[4:5]
	s_mov_b64 s[36:37], -1
	s_and_b64 vcc, exec, s[6:7]
	v_lshl_add_u64 v[4:5], s[10:11], 0, v[60:61]
	s_cbranch_vccnz .LBB0_1019
	v_lshl_add_u64 v[54:55], v[148:149], 1, v[58:59]
	v_add_co_u32_e32 v54, vcc, 0x2000, v54
	v_mov_b32_e32 v64, v51
	s_nop 0
	v_addc_co_u32_e32 v55, vcc, 0, v55, vcc
	v_mov_b32_e32 v65, v52
	v_pk_mov_b32 v[66:67], v[52:53], v[46:47] op_sel:[1,0]
	v_mov_b32_e32 v68, v47
	v_mov_b32_e32 v69, v48
	v_lshl_add_u64 v[62:63], s[10:11], 0, v[60:61]
	s_mov_b64 s[36:37], 0
	s_waitcnt vmcnt(4)
	v_mov_b32_e32 v54, v230
	v_mov_b32_e32 v55, v231
	v_mov_b32_e32 v56, v232
	v_mov_b32_e32 v57, v233
	v_cvt_f32_f16_e32 v3, v54
	v_cvt_f32_f16_sdwa v54, v54 dst_sel:DWORD dst_unused:UNUSED_PAD src0_sel:WORD_1
	v_cvt_f32_f16_e32 v70, v55
	v_cvt_f32_f16_sdwa v71, v55 dst_sel:DWORD dst_unused:UNUSED_PAD src0_sel:WORD_1
	v_cvt_f32_f16_e32 v72, v56
	v_cvt_f32_f16_sdwa v73, v56 dst_sel:DWORD dst_unused:UNUSED_PAD src0_sel:WORD_1
	v_cvt_f32_f16_e32 v74, v57
	v_cvt_f32_f16_sdwa v75, v57 dst_sel:DWORD dst_unused:UNUSED_PAD src0_sel:WORD_1
	v_max_f32_e32 v54, 0x38d1b717, v54
	v_max_f32_e32 v55, 0x38d1b717, v70
	v_max_f32_e32 v56, 0x38d1b717, v71
	v_max_f32_e32 v57, 0x38d1b717, v72
	v_max_f32_e32 v70, 0x38d1b717, v73
	v_max_f32_e32 v71, 0x38d1b717, v74
	v_max_f32_e32 v3, 0x38d1b717, v3
	v_pk_mul_f32 v[54:55], v[64:65], v[54:55]
	v_pk_mul_f32 v[56:57], v[66:67], v[56:57]
	v_pk_mul_f32 v[64:65], v[68:69], v[70:71]
	v_fma_mixlo_f16 v3, v50, v3, 0
	v_cvt_pk_f16_f32 v55, v54, v55
	v_cvt_pk_f16_f32 v56, v56, v57
	v_cvt_pk_f16_f32 v57, v64, v65
	v_max_f32_e32 v72, 0x38d1b717, v75
	v_pack_b32_f16 v54, v3, v55
	v_alignbit_b32 v55, v56, v55, 16
	v_alignbit_b32 v56, v57, v56, 16
	v_lshrrev_b32_e32 v57, 16, v57
	v_fma_mixhi_f16 v57, v49, v72, 0
.LBB0_1019:
	s_andn2_b64 vcc, exec, s[36:37]
	v_lshl_add_u64 v[60:61], v[60:61], 0, s[18:19]
	s_cbranch_vccnz .LBB0_1021
	s_lshl_b32 s0, s21, 1
	v_lshl_add_u64 v[54:55], v[58:59], 0, s[0:1]
	v_lshl_add_u64 v[54:55], v[148:149], 1, v[54:55]
	v_add_co_u32_e32 v54, vcc, 0x1000, v54
	s_add_u32 s36, s55, s34
	s_nop 0
	v_addc_co_u32_e32 v55, vcc, 0, v55, vcc
	s_addc_u32 s37, s56, s35
	v_lshl_add_u64 v[62:63], s[36:37], 0, v[60:61]
	s_waitcnt vmcnt(4)
	v_mov_b32_e32 v54, v230
	v_mov_b32_e32 v55, v231
	v_mov_b32_e32 v56, v232
	v_mov_b32_e32 v57, v233
	v_cvt_f32_f16_e32 v3, v54
	v_cvt_f32_f16_sdwa v54, v54 dst_sel:DWORD dst_unused:UNUSED_PAD src0_sel:WORD_1
	v_cvt_f32_f16_e32 v64, v55
	v_cvt_f32_f16_sdwa v55, v55 dst_sel:DWORD dst_unused:UNUSED_PAD src0_sel:WORD_1
	v_cvt_f32_f16_e32 v65, v56
	v_cvt_f32_f16_sdwa v56, v56 dst_sel:DWORD dst_unused:UNUSED_PAD src0_sel:WORD_1
	v_cvt_f32_f16_e32 v66, v57
	v_cvt_f32_f16_sdwa v57, v57 dst_sel:DWORD dst_unused:UNUSED_PAD src0_sel:WORD_1
	v_max_f32_e32 v67, 0x38d1b717, v3
	v_max_f32_e32 v68, 0x38d1b717, v54
	v_max_f32_e32 v69, 0x38d1b717, v64
	v_max_f32_e32 v70, 0x38d1b717, v55
	v_max_f32_e32 v71, 0x38d1b717, v65
	v_max_f32_e32 v72, 0x38d1b717, v56
	v_max_f32_e32 v73, 0x38d1b717, v66
	v_max_f32_e32 v74, 0x38d1b717, v57
	v_cndmask_b32_e64 v3, v67, v3, s[4:5]
	v_cndmask_b32_e64 v54, v68, v54, s[4:5]
	v_cndmask_b32_e64 v64, v69, v64, s[4:5]
	v_cndmask_b32_e64 v55, v70, v55, s[4:5]
	v_cndmask_b32_e64 v65, v71, v65, s[4:5]
	v_cndmask_b32_e64 v56, v72, v56, s[4:5]
	v_cndmask_b32_e64 v66, v73, v66, s[4:5]
	v_cndmask_b32_e64 v57, v74, v57, s[4:5]
	v_mul_f32_e32 v48, v48, v66
	v_mul_f32_e32 v47, v47, v56
	v_mul_f32_e32 v46, v46, v65
	v_mul_f32_e32 v53, v53, v55
	v_mul_f32_e32 v52, v52, v64
	v_mul_f32_e32 v51, v51, v54
	v_mul_f32_e32 v3, v50, v3
	v_mul_f32_e32 v49, v49, v57
	v_cvt_pk_f16_f32 v54, v3, v51
	v_cvt_pk_f16_f32 v55, v52, v53
	v_cvt_pk_f16_f32 v56, v46, v47
	v_cvt_pk_f16_f32 v57, v48, v49
.LBB0_1021:
	v_lshl_add_u64 v[46:47], v[148:149], 1, v[62:63]
	s_and_b64 vcc, exec, s[6:7]
	s_mov_b64 s[36:37], -1
	global_store_dwordx4 v[46:47], v[54:57], off
	v_mul_u32_u24_e32 v240, 0x3000, v154
	v_add_u32_e32 v240, v240, v213
	v_mov_b32_e32 v241, 0
	v_lshl_add_u64 v[238:239], v[150:151], 1, v[240:241]
	v_lshl_add_u64 v[238:239], s[8:9], 0, v[238:239]
	global_load_dwordx4 v[230:233], v[238:239], off
	s_cbranch_vccnz .LBB0_1023
	v_lshl_add_u64 v[46:47], v[150:151], 1, v[58:59]
	v_add_co_u32_e32 v46, vcc, 0x2000, v46
	v_mov_b32_e32 v50, v43
	s_nop 0
	v_addc_co_u32_e32 v47, vcc, 0, v47, vcc
	v_mov_b32_e32 v51, v44
	v_pk_mov_b32 v[52:53], v[44:45], v[38:39] op_sel:[1,0]
	v_mov_b32_e32 v54, v39
	v_mov_b32_e32 v55, v40
	s_mov_b64 s[36:37], 0
	s_waitcnt vmcnt(4)
	v_mov_b32_e32 v46, v234
	v_mov_b32_e32 v47, v235
	v_mov_b32_e32 v48, v236
	v_mov_b32_e32 v49, v237
	v_cvt_f32_f16_e32 v3, v46
	v_cvt_f32_f16_sdwa v46, v46 dst_sel:DWORD dst_unused:UNUSED_PAD src0_sel:WORD_1
	v_cvt_f32_f16_e32 v56, v47
	v_cvt_f32_f16_sdwa v57, v47 dst_sel:DWORD dst_unused:UNUSED_PAD src0_sel:WORD_1
	v_cvt_f32_f16_e32 v62, v48
	v_cvt_f32_f16_sdwa v63, v48 dst_sel:DWORD dst_unused:UNUSED_PAD src0_sel:WORD_1
	v_cvt_f32_f16_e32 v64, v49
	v_cvt_f32_f16_sdwa v65, v49 dst_sel:DWORD dst_unused:UNUSED_PAD src0_sel:WORD_1
	v_max_f32_e32 v46, 0x38d1b717, v46
	v_max_f32_e32 v47, 0x38d1b717, v56
	v_max_f32_e32 v48, 0x38d1b717, v57
	v_max_f32_e32 v49, 0x38d1b717, v62
	v_max_f32_e32 v56, 0x38d1b717, v63
	v_max_f32_e32 v57, 0x38d1b717, v64
	v_max_f32_e32 v3, 0x38d1b717, v3
	v_pk_mul_f32 v[46:47], v[50:51], v[46:47]
	v_pk_mul_f32 v[48:49], v[52:53], v[48:49]
	v_pk_mul_f32 v[50:51], v[54:55], v[56:57]
	v_fma_mixlo_f16 v3, v42, v3, 0
	v_cvt_pk_f16_f32 v47, v46, v47
	v_cvt_pk_f16_f32 v48, v48, v49
	v_cvt_pk_f16_f32 v49, v50, v51
	v_max_f32_e32 v62, 0x38d1b717, v65
	v_pack_b32_f16 v46, v3, v47
	v_alignbit_b32 v47, v48, v47, 16
	v_alignbit_b32 v48, v49, v48, 16
	v_lshrrev_b32_e32 v49, 16, v49
	v_fma_mixhi_f16 v49, v41, v62, 0
.LBB0_1023:
	s_andn2_b64 vcc, exec, s[36:37]
	s_cbranch_vccnz .LBB0_1025
	s_lshl_b32 s0, s21, 1
	v_lshl_add_u64 v[4:5], v[58:59], 0, s[0:1]
	v_lshl_add_u64 v[4:5], v[148:149], 1, v[4:5]
	v_add_co_u32_e32 v4, vcc, 0x1000, v4
	s_add_u32 s36, s55, s34
	s_nop 0
	v_addc_co_u32_e32 v5, vcc, 0, v5, vcc
	s_addc_u32 s37, s56, s35
	v_lshl_add_u64 v[4:5], s[36:37], 0, v[60:61]
	s_waitcnt vmcnt(4)
	v_mov_b32_e32 v46, v234
	v_mov_b32_e32 v47, v235
	v_mov_b32_e32 v48, v236
	v_mov_b32_e32 v49, v237
	v_cvt_f32_f16_e32 v3, v46
	v_cvt_f32_f16_sdwa v46, v46 dst_sel:DWORD dst_unused:UNUSED_PAD src0_sel:WORD_1
	v_cvt_f32_f16_e32 v50, v47
	v_cvt_f32_f16_sdwa v47, v47 dst_sel:DWORD dst_unused:UNUSED_PAD src0_sel:WORD_1
	v_cvt_f32_f16_e32 v51, v48
	v_cvt_f32_f16_sdwa v48, v48 dst_sel:DWORD dst_unused:UNUSED_PAD src0_sel:WORD_1
	v_cvt_f32_f16_e32 v52, v49
	v_cvt_f32_f16_sdwa v49, v49 dst_sel:DWORD dst_unused:UNUSED_PAD src0_sel:WORD_1
	v_max_f32_e32 v53, 0x38d1b717, v3
	v_max_f32_e32 v54, 0x38d1b717, v46
	v_max_f32_e32 v55, 0x38d1b717, v50
	v_max_f32_e32 v56, 0x38d1b717, v47
	v_max_f32_e32 v57, 0x38d1b717, v51
	v_max_f32_e32 v58, 0x38d1b717, v48
	v_max_f32_e32 v59, 0x38d1b717, v52
	v_max_f32_e32 v60, 0x38d1b717, v49
	v_cndmask_b32_e64 v3, v53, v3, s[4:5]
	v_cndmask_b32_e64 v46, v54, v46, s[4:5]
	v_cndmask_b32_e64 v50, v55, v50, s[4:5]
	v_cndmask_b32_e64 v47, v56, v47, s[4:5]
	v_cndmask_b32_e64 v51, v57, v51, s[4:5]
	v_cndmask_b32_e64 v48, v58, v48, s[4:5]
	v_cndmask_b32_e64 v52, v59, v52, s[4:5]
	v_cndmask_b32_e64 v49, v60, v49, s[4:5]
	v_mul_f32_e32 v40, v40, v52
	v_mul_f32_e32 v39, v39, v48
	v_mul_f32_e32 v38, v38, v51
	v_mul_f32_e32 v45, v45, v47
	v_mul_f32_e32 v44, v44, v50
	v_mul_f32_e32 v43, v43, v46
	v_mul_f32_e32 v3, v42, v3
	v_mul_f32_e32 v41, v41, v49
	v_cvt_pk_f16_f32 v46, v3, v43
	v_cvt_pk_f16_f32 v47, v44, v45
	v_cvt_pk_f16_f32 v48, v38, v39
	v_cvt_pk_f16_f32 v49, v40, v41
.LBB0_1025:
	v_lshl_add_u64 v[4:5], v[148:149], 1, v[4:5]
	global_store_dwordx4 v[4:5], v[46:49], off offset:256
	v_mul_u32_u24_e32 v240, 0x3000, v152
	v_add_u32_e32 v240, v240, v213
	v_mov_b32_e32 v241, 0
	v_lshl_add_u64 v[238:239], v[148:149], 1, v[240:241]
	v_lshl_add_u64 v[238:239], s[8:9], 0, v[238:239]
	global_load_dwordx4 v[234:237], v[238:239], off
	v_mov_b64_e32 v[4:5], s[8:9]
	v_ashrrev_i32_e32 v155, 31, v154
	v_lshlrev_b64 v[44:45], 11, v[154:155]
	v_mad_i64_i32 v[42:43], s[36:37], v154, s64, v[4:5]
	s_mov_b64 s[36:37], -1
	s_and_b64 vcc, exec, s[6:7]
	v_lshl_add_u64 v[4:5], s[10:11], 0, v[44:45]
	s_cbranch_vccnz .LBB0_1027
	v_lshl_add_u64 v[38:39], v[148:149], 1, v[42:43]
	v_add_co_u32_e32 v38, vcc, 0x2000, v38
	v_mov_b32_e32 v48, v35
	s_nop 0
	v_addc_co_u32_e32 v39, vcc, 0, v39, vcc
	v_mov_b32_e32 v49, v36
	v_pk_mov_b32 v[50:51], v[36:37], v[30:31] op_sel:[1,0]
	v_mov_b32_e32 v52, v31
	v_mov_b32_e32 v53, v32
	v_lshl_add_u64 v[46:47], s[10:11], 0, v[44:45]
	s_mov_b64 s[36:37], 0
	s_waitcnt vmcnt(4)
	v_mov_b32_e32 v38, v226
	v_mov_b32_e32 v39, v227
	v_mov_b32_e32 v40, v228
	v_mov_b32_e32 v41, v229
	v_cvt_f32_f16_e32 v3, v38
	v_cvt_f32_f16_sdwa v38, v38 dst_sel:DWORD dst_unused:UNUSED_PAD src0_sel:WORD_1
	v_cvt_f32_f16_e32 v54, v39
	v_cvt_f32_f16_sdwa v55, v39 dst_sel:DWORD dst_unused:UNUSED_PAD src0_sel:WORD_1
	v_cvt_f32_f16_e32 v56, v40
	v_cvt_f32_f16_sdwa v57, v40 dst_sel:DWORD dst_unused:UNUSED_PAD src0_sel:WORD_1
	v_cvt_f32_f16_e32 v58, v41
	v_cvt_f32_f16_sdwa v59, v41 dst_sel:DWORD dst_unused:UNUSED_PAD src0_sel:WORD_1
	v_max_f32_e32 v38, 0x38d1b717, v38
	v_max_f32_e32 v39, 0x38d1b717, v54
	v_max_f32_e32 v40, 0x38d1b717, v55
	v_max_f32_e32 v41, 0x38d1b717, v56
	v_max_f32_e32 v54, 0x38d1b717, v57
	v_max_f32_e32 v55, 0x38d1b717, v58
	v_max_f32_e32 v3, 0x38d1b717, v3
	v_pk_mul_f32 v[38:39], v[48:49], v[38:39]
	v_pk_mul_f32 v[40:41], v[50:51], v[40:41]
	v_pk_mul_f32 v[48:49], v[52:53], v[54:55]
	v_fma_mixlo_f16 v3, v34, v3, 0
	v_cvt_pk_f16_f32 v39, v38, v39
	v_cvt_pk_f16_f32 v40, v40, v41
	v_cvt_pk_f16_f32 v41, v48, v49
	v_max_f32_e32 v56, 0x38d1b717, v59
	v_pack_b32_f16 v38, v3, v39
	v_alignbit_b32 v39, v40, v39, 16
	v_alignbit_b32 v40, v41, v40, 16
	v_lshrrev_b32_e32 v41, 16, v41
	v_fma_mixhi_f16 v41, v33, v56, 0
.LBB0_1027:
	s_andn2_b64 vcc, exec, s[36:37]
	v_lshl_add_u64 v[44:45], v[44:45], 0, s[18:19]
	s_cbranch_vccnz .LBB0_1029
	s_lshl_b32 s0, s21, 1
	v_lshl_add_u64 v[38:39], v[42:43], 0, s[0:1]
	v_lshl_add_u64 v[38:39], v[148:149], 1, v[38:39]
	v_add_co_u32_e32 v38, vcc, 0x1000, v38
	s_add_u32 s36, s55, s34
	s_nop 0
	v_addc_co_u32_e32 v39, vcc, 0, v39, vcc
	s_addc_u32 s37, s56, s35
	v_lshl_add_u64 v[46:47], s[36:37], 0, v[44:45]
	s_waitcnt vmcnt(4)
	v_mov_b32_e32 v38, v226
	v_mov_b32_e32 v39, v227
	v_mov_b32_e32 v40, v228
	v_mov_b32_e32 v41, v229
	v_cvt_f32_f16_e32 v3, v38
	v_cvt_f32_f16_sdwa v38, v38 dst_sel:DWORD dst_unused:UNUSED_PAD src0_sel:WORD_1
	v_cvt_f32_f16_e32 v48, v39
	v_cvt_f32_f16_sdwa v39, v39 dst_sel:DWORD dst_unused:UNUSED_PAD src0_sel:WORD_1
	v_cvt_f32_f16_e32 v49, v40
	v_cvt_f32_f16_sdwa v40, v40 dst_sel:DWORD dst_unused:UNUSED_PAD src0_sel:WORD_1
	v_cvt_f32_f16_e32 v50, v41
	v_cvt_f32_f16_sdwa v41, v41 dst_sel:DWORD dst_unused:UNUSED_PAD src0_sel:WORD_1
	v_max_f32_e32 v51, 0x38d1b717, v3
	v_max_f32_e32 v52, 0x38d1b717, v38
	v_max_f32_e32 v53, 0x38d1b717, v48
	v_max_f32_e32 v54, 0x38d1b717, v39
	v_max_f32_e32 v55, 0x38d1b717, v49
	v_max_f32_e32 v56, 0x38d1b717, v40
	v_max_f32_e32 v57, 0x38d1b717, v50
	v_max_f32_e32 v58, 0x38d1b717, v41
	v_cndmask_b32_e64 v3, v51, v3, s[4:5]
	v_cndmask_b32_e64 v38, v52, v38, s[4:5]
	v_cndmask_b32_e64 v48, v53, v48, s[4:5]
	v_cndmask_b32_e64 v39, v54, v39, s[4:5]
	v_cndmask_b32_e64 v49, v55, v49, s[4:5]
	v_cndmask_b32_e64 v40, v56, v40, s[4:5]
	v_cndmask_b32_e64 v50, v57, v50, s[4:5]
	v_cndmask_b32_e64 v41, v58, v41, s[4:5]
	v_mul_f32_e32 v32, v32, v50
	v_mul_f32_e32 v31, v31, v40
	v_mul_f32_e32 v30, v30, v49
	v_mul_f32_e32 v37, v37, v39
	v_mul_f32_e32 v36, v36, v48
	v_mul_f32_e32 v35, v35, v38
	v_mul_f32_e32 v3, v34, v3
	v_mul_f32_e32 v33, v33, v41
	v_cvt_pk_f16_f32 v38, v3, v35
	v_cvt_pk_f16_f32 v39, v36, v37
	v_cvt_pk_f16_f32 v40, v30, v31
	v_cvt_pk_f16_f32 v41, v32, v33
.LBB0_1029:
	v_lshl_add_u64 v[30:31], v[148:149], 1, v[46:47]
	s_and_b64 vcc, exec, s[6:7]
	s_mov_b64 s[36:37], -1
	global_store_dwordx4 v[30:31], v[38:41], off
	v_mul_u32_u24_e32 v240, 0x3000, v152
	v_add_u32_e32 v240, v240, v213
	v_mov_b32_e32 v241, 0
	v_lshl_add_u64 v[238:239], v[150:151], 1, v[240:241]
	v_lshl_add_u64 v[238:239], s[8:9], 0, v[238:239]
	global_load_dwordx4 v[226:229], v[238:239], off
	s_cbranch_vccnz .LBB0_1031
	v_lshl_add_u64 v[30:31], v[150:151], 1, v[42:43]
	v_add_co_u32_e32 v30, vcc, 0x2000, v30
	v_mov_b32_e32 v34, v27
	s_nop 0
	v_addc_co_u32_e32 v31, vcc, 0, v31, vcc
	v_mov_b32_e32 v35, v28
	v_pk_mov_b32 v[36:37], v[28:29], v[22:23] op_sel:[1,0]
	v_mov_b32_e32 v38, v23
	v_mov_b32_e32 v39, v24
	s_mov_b64 s[36:37], 0
	s_waitcnt vmcnt(4)
	v_mov_b32_e32 v30, v230
	v_mov_b32_e32 v31, v231
	v_mov_b32_e32 v32, v232
	v_mov_b32_e32 v33, v233
	v_cvt_f32_f16_e32 v3, v30
	v_cvt_f32_f16_sdwa v30, v30 dst_sel:DWORD dst_unused:UNUSED_PAD src0_sel:WORD_1
	v_cvt_f32_f16_e32 v40, v31
	v_cvt_f32_f16_sdwa v41, v31 dst_sel:DWORD dst_unused:UNUSED_PAD src0_sel:WORD_1
	v_cvt_f32_f16_e32 v46, v32
	v_cvt_f32_f16_sdwa v47, v32 dst_sel:DWORD dst_unused:UNUSED_PAD src0_sel:WORD_1
	v_cvt_f32_f16_e32 v48, v33
	v_cvt_f32_f16_sdwa v49, v33 dst_sel:DWORD dst_unused:UNUSED_PAD src0_sel:WORD_1
	v_max_f32_e32 v30, 0x38d1b717, v30
	v_max_f32_e32 v31, 0x38d1b717, v40
	v_max_f32_e32 v32, 0x38d1b717, v41
	v_max_f32_e32 v33, 0x38d1b717, v46
	v_max_f32_e32 v40, 0x38d1b717, v47
	v_max_f32_e32 v41, 0x38d1b717, v48
	v_max_f32_e32 v3, 0x38d1b717, v3
	v_pk_mul_f32 v[30:31], v[34:35], v[30:31]
	v_pk_mul_f32 v[32:33], v[36:37], v[32:33]
	v_pk_mul_f32 v[34:35], v[38:39], v[40:41]
	v_fma_mixlo_f16 v3, v26, v3, 0
	v_cvt_pk_f16_f32 v31, v30, v31
	v_cvt_pk_f16_f32 v32, v32, v33
	v_cvt_pk_f16_f32 v33, v34, v35
	v_max_f32_e32 v46, 0x38d1b717, v49
	v_pack_b32_f16 v30, v3, v31
	v_alignbit_b32 v31, v32, v31, 16
	v_alignbit_b32 v32, v33, v32, 16
	v_lshrrev_b32_e32 v33, 16, v33
	v_fma_mixhi_f16 v33, v25, v46, 0
.LBB0_1031:
	s_andn2_b64 vcc, exec, s[36:37]
	s_cbranch_vccnz .LBB0_1033
	s_lshl_b32 s0, s21, 1
	v_lshl_add_u64 v[4:5], v[42:43], 0, s[0:1]
	v_lshl_add_u64 v[4:5], v[148:149], 1, v[4:5]
	v_add_co_u32_e32 v4, vcc, 0x1000, v4
	s_add_u32 s36, s55, s34
	s_nop 0
	v_addc_co_u32_e32 v5, vcc, 0, v5, vcc
	s_addc_u32 s37, s56, s35
	v_lshl_add_u64 v[4:5], s[36:37], 0, v[44:45]
	s_waitcnt vmcnt(4)
	v_mov_b32_e32 v30, v230
	v_mov_b32_e32 v31, v231
	v_mov_b32_e32 v32, v232
	v_mov_b32_e32 v33, v233
	v_cvt_f32_f16_e32 v3, v30
	v_cvt_f32_f16_sdwa v30, v30 dst_sel:DWORD dst_unused:UNUSED_PAD src0_sel:WORD_1
	v_cvt_f32_f16_e32 v34, v31
	v_cvt_f32_f16_sdwa v31, v31 dst_sel:DWORD dst_unused:UNUSED_PAD src0_sel:WORD_1
	v_cvt_f32_f16_e32 v35, v32
	v_cvt_f32_f16_sdwa v32, v32 dst_sel:DWORD dst_unused:UNUSED_PAD src0_sel:WORD_1
	v_cvt_f32_f16_e32 v36, v33
	v_cvt_f32_f16_sdwa v33, v33 dst_sel:DWORD dst_unused:UNUSED_PAD src0_sel:WORD_1
	v_max_f32_e32 v37, 0x38d1b717, v3
	v_max_f32_e32 v38, 0x38d1b717, v30
	v_max_f32_e32 v39, 0x38d1b717, v34
	v_max_f32_e32 v40, 0x38d1b717, v31
	v_max_f32_e32 v41, 0x38d1b717, v35
	v_max_f32_e32 v42, 0x38d1b717, v32
	v_max_f32_e32 v43, 0x38d1b717, v36
	v_max_f32_e32 v44, 0x38d1b717, v33
	v_cndmask_b32_e64 v3, v37, v3, s[4:5]
	v_cndmask_b32_e64 v30, v38, v30, s[4:5]
	v_cndmask_b32_e64 v34, v39, v34, s[4:5]
	v_cndmask_b32_e64 v31, v40, v31, s[4:5]
	v_cndmask_b32_e64 v35, v41, v35, s[4:5]
	v_cndmask_b32_e64 v32, v42, v32, s[4:5]
	v_cndmask_b32_e64 v36, v43, v36, s[4:5]
	v_cndmask_b32_e64 v33, v44, v33, s[4:5]
	v_mul_f32_e32 v24, v24, v36
	v_mul_f32_e32 v23, v23, v32
	v_mul_f32_e32 v22, v22, v35
	v_mul_f32_e32 v29, v29, v31
	v_mul_f32_e32 v28, v28, v34
	v_mul_f32_e32 v27, v27, v30
	v_mul_f32_e32 v3, v26, v3
	v_mul_f32_e32 v25, v25, v33
	v_cvt_pk_f16_f32 v30, v3, v27
	v_cvt_pk_f16_f32 v31, v28, v29
	v_cvt_pk_f16_f32 v32, v22, v23
	v_cvt_pk_f16_f32 v33, v24, v25
.LBB0_1033:
	v_lshl_add_u64 v[4:5], v[148:149], 1, v[4:5]
	global_store_dwordx4 v[4:5], v[30:33], off offset:256
	v_mov_b64_e32 v[4:5], s[8:9]
	v_ashrrev_i32_e32 v153, 31, v152
	v_lshlrev_b64 v[28:29], 11, v[152:153]
	v_mad_i64_i32 v[26:27], s[36:37], v152, s64, v[4:5]
	s_mov_b64 s[36:37], -1
	s_and_b64 vcc, exec, s[6:7]
	v_lshl_add_u64 v[4:5], s[10:11], 0, v[28:29]
	s_cbranch_vccnz .LBB0_1035
	v_lshl_add_u64 v[22:23], v[148:149], 1, v[26:27]
	v_add_co_u32_e32 v22, vcc, 0x2000, v22
	v_mov_b32_e32 v32, v19
	s_nop 0
	v_addc_co_u32_e32 v23, vcc, 0, v23, vcc
	v_mov_b32_e32 v33, v20
	v_pk_mov_b32 v[34:35], v[20:21], v[14:15] op_sel:[1,0]
	v_mov_b32_e32 v36, v15
	v_mov_b32_e32 v37, v16
	v_lshl_add_u64 v[30:31], s[10:11], 0, v[28:29]
	s_mov_b64 s[36:37], 0
	s_waitcnt vmcnt(3)
	v_mov_b32_e32 v22, v234
	v_mov_b32_e32 v23, v235
	v_mov_b32_e32 v24, v236
	v_mov_b32_e32 v25, v237
	v_cvt_f32_f16_e32 v3, v22
	v_cvt_f32_f16_sdwa v22, v22 dst_sel:DWORD dst_unused:UNUSED_PAD src0_sel:WORD_1
	v_cvt_f32_f16_e32 v38, v23
	v_cvt_f32_f16_sdwa v39, v23 dst_sel:DWORD dst_unused:UNUSED_PAD src0_sel:WORD_1
	v_cvt_f32_f16_e32 v40, v24
	v_cvt_f32_f16_sdwa v41, v24 dst_sel:DWORD dst_unused:UNUSED_PAD src0_sel:WORD_1
	v_cvt_f32_f16_e32 v42, v25
	v_cvt_f32_f16_sdwa v43, v25 dst_sel:DWORD dst_unused:UNUSED_PAD src0_sel:WORD_1
	v_max_f32_e32 v22, 0x38d1b717, v22
	v_max_f32_e32 v23, 0x38d1b717, v38
	v_max_f32_e32 v24, 0x38d1b717, v39
	v_max_f32_e32 v25, 0x38d1b717, v40
	v_max_f32_e32 v38, 0x38d1b717, v41
	v_max_f32_e32 v39, 0x38d1b717, v42
	v_max_f32_e32 v3, 0x38d1b717, v3
	v_pk_mul_f32 v[22:23], v[32:33], v[22:23]
	v_pk_mul_f32 v[24:25], v[34:35], v[24:25]
	v_pk_mul_f32 v[32:33], v[36:37], v[38:39]
	v_fma_mixlo_f16 v3, v18, v3, 0
	v_cvt_pk_f16_f32 v23, v22, v23
	v_cvt_pk_f16_f32 v24, v24, v25
	v_cvt_pk_f16_f32 v25, v32, v33
	v_max_f32_e32 v40, 0x38d1b717, v43
	v_pack_b32_f16 v22, v3, v23
	v_alignbit_b32 v23, v24, v23, 16
	v_alignbit_b32 v24, v25, v24, 16
	v_lshrrev_b32_e32 v25, 16, v25
	v_fma_mixhi_f16 v25, v17, v40, 0
.LBB0_1035:
	s_andn2_b64 vcc, exec, s[36:37]
	v_lshl_add_u64 v[28:29], v[28:29], 0, s[18:19]
	s_cbranch_vccnz .LBB0_1037
	s_lshl_b32 s0, s21, 1
	v_lshl_add_u64 v[22:23], v[26:27], 0, s[0:1]
	v_lshl_add_u64 v[22:23], v[148:149], 1, v[22:23]
	v_add_co_u32_e32 v22, vcc, 0x1000, v22
	s_add_u32 s36, s55, s34
	s_nop 0
	v_addc_co_u32_e32 v23, vcc, 0, v23, vcc
	s_addc_u32 s37, s56, s35
	v_lshl_add_u64 v[30:31], s[36:37], 0, v[28:29]
	s_waitcnt vmcnt(3)
	v_mov_b32_e32 v22, v234
	v_mov_b32_e32 v23, v235
	v_mov_b32_e32 v24, v236
	v_mov_b32_e32 v25, v237
	v_cvt_f32_f16_e32 v3, v22
	v_cvt_f32_f16_sdwa v22, v22 dst_sel:DWORD dst_unused:UNUSED_PAD src0_sel:WORD_1
	v_cvt_f32_f16_e32 v32, v23
	v_cvt_f32_f16_sdwa v23, v23 dst_sel:DWORD dst_unused:UNUSED_PAD src0_sel:WORD_1
	v_cvt_f32_f16_e32 v33, v24
	v_cvt_f32_f16_sdwa v24, v24 dst_sel:DWORD dst_unused:UNUSED_PAD src0_sel:WORD_1
	v_cvt_f32_f16_e32 v34, v25
	v_cvt_f32_f16_sdwa v25, v25 dst_sel:DWORD dst_unused:UNUSED_PAD src0_sel:WORD_1
	v_max_f32_e32 v35, 0x38d1b717, v3
	v_max_f32_e32 v36, 0x38d1b717, v22
	v_max_f32_e32 v37, 0x38d1b717, v32
	v_max_f32_e32 v38, 0x38d1b717, v23
	v_max_f32_e32 v39, 0x38d1b717, v33
	v_max_f32_e32 v40, 0x38d1b717, v24
	v_max_f32_e32 v41, 0x38d1b717, v34
	v_max_f32_e32 v42, 0x38d1b717, v25
	v_cndmask_b32_e64 v3, v35, v3, s[4:5]
	v_cndmask_b32_e64 v22, v36, v22, s[4:5]
	v_cndmask_b32_e64 v32, v37, v32, s[4:5]
	v_cndmask_b32_e64 v23, v38, v23, s[4:5]
	v_cndmask_b32_e64 v33, v39, v33, s[4:5]
	v_cndmask_b32_e64 v24, v40, v24, s[4:5]
	v_cndmask_b32_e64 v34, v41, v34, s[4:5]
	v_cndmask_b32_e64 v25, v42, v25, s[4:5]
	v_mul_f32_e32 v16, v16, v34
	v_mul_f32_e32 v15, v15, v24
	v_mul_f32_e32 v14, v14, v33
	v_mul_f32_e32 v21, v21, v23
	v_mul_f32_e32 v20, v20, v32
	v_mul_f32_e32 v19, v19, v22
	v_mul_f32_e32 v3, v18, v3
	v_mul_f32_e32 v17, v17, v25
	v_cvt_pk_f16_f32 v22, v3, v19
	v_cvt_pk_f16_f32 v23, v20, v21
	v_cvt_pk_f16_f32 v24, v14, v15
	v_cvt_pk_f16_f32 v25, v16, v17
.LBB0_1037:
	v_lshl_add_u64 v[14:15], v[148:149], 1, v[30:31]
	s_and_b64 vcc, exec, s[6:7]
	s_mov_b64 s[6:7], -1
	global_store_dwordx4 v[14:15], v[22:25], off
	s_cbranch_vccnz .LBB0_1039
	v_lshl_add_u64 v[14:15], v[150:151], 1, v[26:27]
	v_add_co_u32_e32 v14, vcc, 0x2000, v14
	v_mov_b32_e32 v18, v11
	s_nop 0
	v_addc_co_u32_e32 v15, vcc, 0, v15, vcc
	v_mov_b32_e32 v19, v12
	v_pk_mov_b32 v[20:21], v[12:13], v[6:7] op_sel:[1,0]
	v_mov_b32_e32 v22, v7
	v_mov_b32_e32 v23, v8
	s_mov_b64 s[6:7], 0
	s_waitcnt vmcnt(2)
	v_mov_b32_e32 v14, v226
	v_mov_b32_e32 v15, v227
	v_mov_b32_e32 v16, v228
	v_mov_b32_e32 v17, v229
	v_cvt_f32_f16_e32 v3, v14
	v_cvt_f32_f16_sdwa v14, v14 dst_sel:DWORD dst_unused:UNUSED_PAD src0_sel:WORD_1
	v_cvt_f32_f16_e32 v24, v15
	v_cvt_f32_f16_sdwa v25, v15 dst_sel:DWORD dst_unused:UNUSED_PAD src0_sel:WORD_1
	v_cvt_f32_f16_e32 v30, v16
	v_cvt_f32_f16_sdwa v31, v16 dst_sel:DWORD dst_unused:UNUSED_PAD src0_sel:WORD_1
	v_cvt_f32_f16_e32 v32, v17
	v_cvt_f32_f16_sdwa v33, v17 dst_sel:DWORD dst_unused:UNUSED_PAD src0_sel:WORD_1
	v_max_f32_e32 v14, 0x38d1b717, v14
	v_max_f32_e32 v15, 0x38d1b717, v24
	v_max_f32_e32 v16, 0x38d1b717, v25
	v_max_f32_e32 v17, 0x38d1b717, v30
	v_max_f32_e32 v24, 0x38d1b717, v31
	v_max_f32_e32 v25, 0x38d1b717, v32
	v_max_f32_e32 v3, 0x38d1b717, v3
	v_pk_mul_f32 v[14:15], v[18:19], v[14:15]
	v_pk_mul_f32 v[16:17], v[20:21], v[16:17]
	v_pk_mul_f32 v[18:19], v[22:23], v[24:25]
	v_fma_mixlo_f16 v3, v10, v3, 0
	v_cvt_pk_f16_f32 v15, v14, v15
	v_cvt_pk_f16_f32 v16, v16, v17
	v_cvt_pk_f16_f32 v17, v18, v19
	v_max_f32_e32 v30, 0x38d1b717, v33
	v_pack_b32_f16 v14, v3, v15
	v_alignbit_b32 v15, v16, v15, 16
	v_alignbit_b32 v16, v17, v16, 16
	v_lshrrev_b32_e32 v17, 16, v17
	v_fma_mixhi_f16 v17, v9, v30, 0
.LBB0_1039:
	s_andn2_b64 vcc, exec, s[6:7]
	s_cbranch_vccnz .LBB0_1041
	s_lshl_b32 s0, s21, 1
	v_lshl_add_u64 v[4:5], v[26:27], 0, s[0:1]
	v_lshl_add_u64 v[4:5], v[148:149], 1, v[4:5]
	v_add_co_u32_e32 v4, vcc, 0x1000, v4
	s_add_u32 s6, s55, s34
	s_nop 0
	v_addc_co_u32_e32 v5, vcc, 0, v5, vcc
	s_addc_u32 s7, s56, s35
	v_lshl_add_u64 v[4:5], s[6:7], 0, v[28:29]
	s_waitcnt vmcnt(2)
	v_mov_b32_e32 v14, v226
	v_mov_b32_e32 v15, v227
	v_mov_b32_e32 v16, v228
	v_mov_b32_e32 v17, v229
	v_cvt_f32_f16_e32 v3, v14
	v_cvt_f32_f16_sdwa v14, v14 dst_sel:DWORD dst_unused:UNUSED_PAD src0_sel:WORD_1
	v_cvt_f32_f16_e32 v18, v15
	v_cvt_f32_f16_sdwa v15, v15 dst_sel:DWORD dst_unused:UNUSED_PAD src0_sel:WORD_1
	v_cvt_f32_f16_e32 v19, v16
	v_cvt_f32_f16_sdwa v16, v16 dst_sel:DWORD dst_unused:UNUSED_PAD src0_sel:WORD_1
	v_cvt_f32_f16_e32 v20, v17
	v_cvt_f32_f16_sdwa v17, v17 dst_sel:DWORD dst_unused:UNUSED_PAD src0_sel:WORD_1
	v_max_f32_e32 v21, 0x38d1b717, v3
	v_max_f32_e32 v22, 0x38d1b717, v14
	v_max_f32_e32 v23, 0x38d1b717, v18
	v_max_f32_e32 v24, 0x38d1b717, v15
	v_max_f32_e32 v25, 0x38d1b717, v19
	v_max_f32_e32 v26, 0x38d1b717, v16
	v_max_f32_e32 v27, 0x38d1b717, v20
	v_max_f32_e32 v28, 0x38d1b717, v17
	v_cndmask_b32_e64 v3, v21, v3, s[4:5]
	v_cndmask_b32_e64 v14, v22, v14, s[4:5]
	v_cndmask_b32_e64 v18, v23, v18, s[4:5]
	v_cndmask_b32_e64 v15, v24, v15, s[4:5]
	v_cndmask_b32_e64 v19, v25, v19, s[4:5]
	v_cndmask_b32_e64 v16, v26, v16, s[4:5]
	v_cndmask_b32_e64 v20, v27, v20, s[4:5]
	v_cndmask_b32_e64 v17, v28, v17, s[4:5]
	v_mul_f32_e32 v8, v8, v20
	v_mul_f32_e32 v7, v7, v16
	v_mul_f32_e32 v6, v6, v19
	v_mul_f32_e32 v13, v13, v15
	v_mul_f32_e32 v12, v12, v18
	v_mul_f32_e32 v11, v11, v14
	v_mul_f32_e32 v3, v10, v3
	v_mul_f32_e32 v9, v9, v17
	v_cvt_pk_f16_f32 v14, v3, v11
	v_cvt_pk_f16_f32 v15, v12, v13
	v_cvt_pk_f16_f32 v16, v6, v7
	v_cvt_pk_f16_f32 v17, v8, v9

.LBB0_5359:
	v_mov_b32_e32 v213, s30
	v_min_u32_e32 v213, 2, v213
	v_lshlrev_b32_e32 v213, 11, v213
	v_add_u32_e32 v213, 0x1800, v213
	v_mul_u32_u24_e32 v240, 0x3000, v134
	v_add_u32_e32 v240, v240, v213
	v_mov_b32_e32 v241, 0
	v_lshl_add_u64 v[238:239], v[148:149], 1, v[240:241]
	v_lshl_add_u64 v[238:239], s[8:9], 0, v[238:239]
	global_load_dwordx4 v[226:229], v[238:239], off
	v_mul_u32_u24_e32 v240, 0x3000, v134
	v_add_u32_e32 v240, v240, v213
	v_mov_b32_e32 v241, 0
	v_lshl_add_u64 v[238:239], v[150:151], 1, v[240:241]
	v_lshl_add_u64 v[238:239], s[8:9], 0, v[238:239]
	global_load_dwordx4 v[230:233], v[238:239], off
	v_mul_u32_u24_e32 v240, 0x3000, v164
	v_add_u32_e32 v240, v240, v213
	v_mov_b32_e32 v241, 0
	v_lshl_add_u64 v[238:239], v[148:149], 1, v[240:241]
	v_lshl_add_u64 v[238:239], s[8:9], 0, v[238:239]
	global_load_dwordx4 v[234:237], v[238:239], off
	s_cmp_lt_i32 s30, 0
	v_mov_b64_e32 v[4:5], s[8:9]
	v_ashrrev_i32_e32 v135, 31, v134
	s_cselect_b64 s[34:35], -1, 0
	s_cmp_eq_u32 s30, 0
	v_lshlrev_b64 v[168:169], 11, v[134:135]
	v_mad_i64_i32 v[166:167], s[4:5], v134, s62, v[4:5]
	s_cselect_b64 s[0:1], -1, 0
	s_mov_b64 s[4:5], -1
	s_and_b64 vcc, exec, s[34:35]
	v_lshl_add_u64 v[4:5], s[10:11], 0, v[168:169]
	s_cbranch_vccz .LBB0_5361
	v_lshl_add_u64 v[134:135], v[148:149], 1, v[166:167]
	v_add_co_u32_e32 v134, vcc, 0x2000, v134
	v_mov_b32_e32 v176, v131
	s_nop 0
	v_addc_co_u32_e32 v135, vcc, 0, v135, vcc
	v_mov_b32_e32 v177, v132
	v_pk_mov_b32 v[178:179], v[132:133], v[126:127] op_sel:[1,0]
	v_mov_b32_e32 v180, v127
	v_mov_b32_e32 v181, v128
	v_lshl_add_u64 v[170:171], s[10:11], 0, v[168:169]
	s_mov_b64 s[4:5], 0
	s_waitcnt vmcnt(2)
	v_mov_b32_e32 v134, v226
	v_mov_b32_e32 v135, v227
	v_mov_b32_e32 v136, v228
	v_mov_b32_e32 v137, v229
	v_cvt_f32_f16_e32 v3, v134
	v_cvt_f32_f16_sdwa v134, v134 dst_sel:DWORD dst_unused:UNUSED_PAD src0_sel:WORD_1
	v_cvt_f32_f16_e32 v153, v135
	v_cvt_f32_f16_sdwa v155, v135 dst_sel:DWORD dst_unused:UNUSED_PAD src0_sel:WORD_1
	v_cvt_f32_f16_e32 v157, v136
	v_cvt_f32_f16_sdwa v159, v136 dst_sel:DWORD dst_unused:UNUSED_PAD src0_sel:WORD_1
	v_cvt_f32_f16_e32 v161, v137
	v_cvt_f32_f16_sdwa v163, v137 dst_sel:DWORD dst_unused:UNUSED_PAD src0_sel:WORD_1
	v_max_f32_e32 v134, 0x38d1b717, v134
	v_max_f32_e32 v135, 0x38d1b717, v153
	v_max_f32_e32 v136, 0x38d1b717, v155
	v_max_f32_e32 v137, 0x38d1b717, v157
	v_max_f32_e32 v182, 0x38d1b717, v159
	v_max_f32_e32 v183, 0x38d1b717, v161
	v_max_f32_e32 v3, 0x38d1b717, v3
	v_pk_mul_f32 v[134:135], v[176:177], v[134:135]
	v_pk_mul_f32 v[136:137], v[178:179], v[136:137]
	v_pk_mul_f32 v[176:177], v[180:181], v[182:183]
	v_fma_mixlo_f16 v3, v130, v3, 0
	v_cvt_pk_f16_f32 v135, v134, v135
	v_cvt_pk_f16_f32 v136, v136, v137
	v_cvt_pk_f16_f32 v137, v176, v177
	v_max_f32_e32 v153, 0x38d1b717, v163
	v_pack_b32_f16 v134, v3, v135
	v_alignbit_b32 v135, v136, v135, 16
	v_alignbit_b32 v136, v137, v136, 16
	v_lshrrev_b32_e32 v137, 16, v137
	v_fma_mixhi_f16 v137, v129, v153, 0
.LBB0_5361:
	s_min_u32 s2, s30, 2
	s_mov_b32 s31, s3
	s_lshl_b32 s21, s2, 10
	s_lshl_b64 s[30:31], s[30:31], 22
	s_andn2_b64 vcc, exec, s[4:5]
	v_lshl_add_u64 v[168:169], v[168:169], 0, s[18:19]
	s_cbranch_vccnz .LBB0_5363
	s_lshl_b32 s2, s21, 1
	v_lshl_add_u64 v[134:135], v[166:167], 0, s[2:3]
	v_lshl_add_u64 v[134:135], v[148:149], 1, v[134:135]
	v_add_co_u32_e32 v134, vcc, 0x1000, v134
	s_add_u32 s4, s53, s30
	s_nop 0
	v_addc_co_u32_e32 v135, vcc, 0, v135, vcc
	s_addc_u32 s5, s54, s31
	v_lshl_add_u64 v[170:171], s[4:5], 0, v[168:169]
	s_waitcnt vmcnt(2)
	v_mov_b32_e32 v134, v226
	v_mov_b32_e32 v135, v227
	v_mov_b32_e32 v136, v228
	v_mov_b32_e32 v137, v229
	v_cvt_f32_f16_e32 v3, v134
	v_cvt_f32_f16_sdwa v134, v134 dst_sel:DWORD dst_unused:UNUSED_PAD src0_sel:WORD_1
	v_cvt_f32_f16_e32 v153, v135
	v_cvt_f32_f16_sdwa v135, v135 dst_sel:DWORD dst_unused:UNUSED_PAD src0_sel:WORD_1
	v_cvt_f32_f16_e32 v155, v136
	v_cvt_f32_f16_sdwa v136, v136 dst_sel:DWORD dst_unused:UNUSED_PAD src0_sel:WORD_1
	v_cvt_f32_f16_e32 v157, v137
	v_cvt_f32_f16_sdwa v137, v137 dst_sel:DWORD dst_unused:UNUSED_PAD src0_sel:WORD_1
	v_max_f32_e32 v159, 0x38d1b717, v3
	v_max_f32_e32 v161, 0x38d1b717, v134
	v_max_f32_e32 v163, 0x38d1b717, v153
	v_max_f32_e32 v165, 0x38d1b717, v135
	v_max_f32_e32 v175, 0x38d1b717, v155
	v_max_f32_e32 v176, 0x38d1b717, v136
	v_max_f32_e32 v177, 0x38d1b717, v157
	v_max_f32_e32 v178, 0x38d1b717, v137
	v_cndmask_b32_e64 v3, v159, v3, s[0:1]
	v_cndmask_b32_e64 v134, v161, v134, s[0:1]
	v_cndmask_b32_e64 v153, v163, v153, s[0:1]
	v_cndmask_b32_e64 v135, v165, v135, s[0:1]
	v_cndmask_b32_e64 v155, v175, v155, s[0:1]
	v_cndmask_b32_e64 v136, v176, v136, s[0:1]
	v_cndmask_b32_e64 v157, v177, v157, s[0:1]
	v_cndmask_b32_e64 v137, v178, v137, s[0:1]
	v_mul_f32_e32 v128, v128, v157
	v_mul_f32_e32 v127, v127, v136
	v_mul_f32_e32 v126, v126, v155
	v_mul_f32_e32 v133, v133, v135
	v_mul_f32_e32 v132, v132, v153
	v_mul_f32_e32 v131, v131, v134
	v_mul_f32_e32 v3, v130, v3
	v_mul_f32_e32 v129, v129, v137
	v_cvt_pk_f16_f32 v134, v3, v131
	v_cvt_pk_f16_f32 v135, v132, v133
	v_cvt_pk_f16_f32 v136, v126, v127
	v_cvt_pk_f16_f32 v137, v128, v129
.LBB0_5363:
	v_cndmask_b32_e64 v3, 0, 1, s[34:35]
	v_lshl_add_u64 v[126:127], v[148:149], 1, v[170:171]
	v_cmp_ne_u32_e64 s[4:5], 1, v3
	s_andn2_b64 vcc, exec, s[34:35]
	s_mov_b64 s[34:35], -1
	global_store_dwordx4 v[126:127], v[134:137], off
	v_mul_u32_u24_e32 v240, 0x3000, v164
	v_add_u32_e32 v240, v240, v213
	v_mov_b32_e32 v241, 0
	v_lshl_add_u64 v[238:239], v[150:151], 1, v[240:241]
	v_lshl_add_u64 v[238:239], s[8:9], 0, v[238:239]
	global_load_dwordx4 v[226:229], v[238:239], off
	s_cbranch_vccnz .LBB0_5365
	v_lshl_add_u64 v[126:127], v[150:151], 1, v[166:167]
	v_add_co_u32_e32 v126, vcc, 0x2000, v126
	v_mov_b32_e32 v130, v123
	s_nop 0
	v_addc_co_u32_e32 v127, vcc, 0, v127, vcc
	v_mov_b32_e32 v131, v124
	v_pk_mov_b32 v[132:133], v[124:125], v[118:119] op_sel:[1,0]
	v_mov_b32_e32 v134, v119
	v_mov_b32_e32 v135, v120
	s_mov_b64 s[34:35], 0
	s_waitcnt vmcnt(3)
	v_mov_b32_e32 v126, v230
	v_mov_b32_e32 v127, v231
	v_mov_b32_e32 v128, v232
	v_mov_b32_e32 v129, v233
	v_cvt_f32_f16_e32 v3, v126
	v_cvt_f32_f16_sdwa v126, v126 dst_sel:DWORD dst_unused:UNUSED_PAD src0_sel:WORD_1
	v_cvt_f32_f16_e32 v136, v127
	v_cvt_f32_f16_sdwa v137, v127 dst_sel:DWORD dst_unused:UNUSED_PAD src0_sel:WORD_1
	v_cvt_f32_f16_e32 v153, v128
	v_cvt_f32_f16_sdwa v155, v128 dst_sel:DWORD dst_unused:UNUSED_PAD src0_sel:WORD_1
	v_cvt_f32_f16_e32 v157, v129
	v_cvt_f32_f16_sdwa v159, v129 dst_sel:DWORD dst_unused:UNUSED_PAD src0_sel:WORD_1
	v_max_f32_e32 v126, 0x38d1b717, v126
	v_max_f32_e32 v127, 0x38d1b717, v136
	v_max_f32_e32 v128, 0x38d1b717, v137
	v_max_f32_e32 v129, 0x38d1b717, v153
	v_max_f32_e32 v136, 0x38d1b717, v155
	v_max_f32_e32 v137, 0x38d1b717, v157
	v_max_f32_e32 v3, 0x38d1b717, v3
	v_pk_mul_f32 v[126:127], v[130:131], v[126:127]
	v_pk_mul_f32 v[128:129], v[132:133], v[128:129]
	v_pk_mul_f32 v[130:131], v[134:135], v[136:137]
	v_fma_mixlo_f16 v3, v122, v3, 0
	v_cvt_pk_f16_f32 v127, v126, v127
	v_cvt_pk_f16_f32 v128, v128, v129
	v_cvt_pk_f16_f32 v129, v130, v131
	v_max_f32_e32 v153, 0x38d1b717, v159
	v_pack_b32_f16 v126, v3, v127
	v_alignbit_b32 v127, v128, v127, 16
	v_alignbit_b32 v128, v129, v128, 16
	v_lshrrev_b32_e32 v129, 16, v129
	v_fma_mixhi_f16 v129, v121, v153, 0
.LBB0_5365:
	s_andn2_b64 vcc, exec, s[34:35]
	s_cbranch_vccnz .LBB0_5367
	s_lshl_b32 s2, s21, 1
	v_lshl_add_u64 v[4:5], v[166:167], 0, s[2:3]
	v_lshl_add_u64 v[4:5], v[148:149], 1, v[4:5]
	v_add_co_u32_e32 v4, vcc, 0x1000, v4
	s_add_u32 s34, s53, s30
	s_nop 0
	v_addc_co_u32_e32 v5, vcc, 0, v5, vcc
	s_addc_u32 s35, s54, s31
	v_lshl_add_u64 v[4:5], s[34:35], 0, v[168:169]
	s_waitcnt vmcnt(3)
	v_mov_b32_e32 v126, v230
	v_mov_b32_e32 v127, v231
	v_mov_b32_e32 v128, v232
	v_mov_b32_e32 v129, v233
	v_cvt_f32_f16_e32 v3, v126
	v_cvt_f32_f16_sdwa v126, v126 dst_sel:DWORD dst_unused:UNUSED_PAD src0_sel:WORD_1
	v_cvt_f32_f16_e32 v130, v127
	v_cvt_f32_f16_sdwa v127, v127 dst_sel:DWORD dst_unused:UNUSED_PAD src0_sel:WORD_1
	v_cvt_f32_f16_e32 v131, v128
	v_cvt_f32_f16_sdwa v128, v128 dst_sel:DWORD dst_unused:UNUSED_PAD src0_sel:WORD_1
	v_cvt_f32_f16_e32 v132, v129
	v_cvt_f32_f16_sdwa v129, v129 dst_sel:DWORD dst_unused:UNUSED_PAD src0_sel:WORD_1
	v_max_f32_e32 v133, 0x38d1b717, v3
	v_max_f32_e32 v134, 0x38d1b717, v126
	v_max_f32_e32 v135, 0x38d1b717, v130
	v_max_f32_e32 v136, 0x38d1b717, v127
	v_max_f32_e32 v137, 0x38d1b717, v131
	v_max_f32_e32 v153, 0x38d1b717, v128
	v_max_f32_e32 v155, 0x38d1b717, v132
	v_max_f32_e32 v157, 0x38d1b717, v129
	v_cndmask_b32_e64 v3, v133, v3, s[0:1]
	v_cndmask_b32_e64 v126, v134, v126, s[0:1]
	v_cndmask_b32_e64 v130, v135, v130, s[0:1]
	v_cndmask_b32_e64 v127, v136, v127, s[0:1]
	v_cndmask_b32_e64 v131, v137, v131, s[0:1]
	v_cndmask_b32_e64 v128, v153, v128, s[0:1]
	v_cndmask_b32_e64 v132, v155, v132, s[0:1]
	v_cndmask_b32_e64 v129, v157, v129, s[0:1]
	v_mul_f32_e32 v120, v120, v132
	v_mul_f32_e32 v119, v119, v128
	v_mul_f32_e32 v118, v118, v131
	v_mul_f32_e32 v125, v125, v127
	v_mul_f32_e32 v124, v124, v130
	v_mul_f32_e32 v123, v123, v126
	v_mul_f32_e32 v3, v122, v3
	v_mul_f32_e32 v121, v121, v129
	v_cvt_pk_f16_f32 v126, v3, v123
	v_cvt_pk_f16_f32 v127, v124, v125
	v_cvt_pk_f16_f32 v128, v118, v119
	v_cvt_pk_f16_f32 v129, v120, v121
.LBB0_5367:
	v_lshl_add_u64 v[4:5], v[148:149], 1, v[4:5]
	global_store_dwordx4 v[4:5], v[126:129], off offset:256
	v_mul_u32_u24_e32 v240, 0x3000, v162
	v_add_u32_e32 v240, v240, v213
	v_mov_b32_e32 v241, 0
	v_lshl_add_u64 v[238:239], v[148:149], 1, v[240:241]
	v_lshl_add_u64 v[238:239], s[8:9], 0, v[238:239]
	global_load_dwordx4 v[230:233], v[238:239], off
	v_mov_b64_e32 v[4:5], s[8:9]
	v_ashrrev_i32_e32 v165, 31, v164
	v_lshlrev_b64 v[124:125], 11, v[164:165]
	v_mad_i64_i32 v[122:123], s[34:35], v164, s62, v[4:5]
	s_mov_b64 s[34:35], -1
	s_and_b64 vcc, exec, s[4:5]
	v_lshl_add_u64 v[4:5], s[10:11], 0, v[124:125]
	s_cbranch_vccnz .LBB0_5369
	v_lshl_add_u64 v[118:119], v[148:149], 1, v[122:123]
	v_add_co_u32_e32 v118, vcc, 0x2000, v118
	v_mov_b32_e32 v128, v115
	s_nop 0
	v_addc_co_u32_e32 v119, vcc, 0, v119, vcc
	v_mov_b32_e32 v129, v116
	v_pk_mov_b32 v[130:131], v[116:117], v[110:111] op_sel:[1,0]
	v_mov_b32_e32 v132, v111
	v_mov_b32_e32 v133, v112
	v_lshl_add_u64 v[126:127], s[10:11], 0, v[124:125]
	s_mov_b64 s[34:35], 0
	s_waitcnt vmcnt(4)
	v_mov_b32_e32 v118, v234
	v_mov_b32_e32 v119, v235
	v_mov_b32_e32 v120, v236
	v_mov_b32_e32 v121, v237
	v_cvt_f32_f16_e32 v3, v118
	v_cvt_f32_f16_sdwa v118, v118 dst_sel:DWORD dst_unused:UNUSED_PAD src0_sel:WORD_1
	v_cvt_f32_f16_e32 v134, v119
	v_cvt_f32_f16_sdwa v135, v119 dst_sel:DWORD dst_unused:UNUSED_PAD src0_sel:WORD_1
	v_cvt_f32_f16_e32 v136, v120
	v_cvt_f32_f16_sdwa v137, v120 dst_sel:DWORD dst_unused:UNUSED_PAD src0_sel:WORD_1
	v_cvt_f32_f16_e32 v153, v121
	v_cvt_f32_f16_sdwa v155, v121 dst_sel:DWORD dst_unused:UNUSED_PAD src0_sel:WORD_1
	v_max_f32_e32 v118, 0x38d1b717, v118
	v_max_f32_e32 v119, 0x38d1b717, v134
	v_max_f32_e32 v120, 0x38d1b717, v135
	v_max_f32_e32 v121, 0x38d1b717, v136
	v_max_f32_e32 v134, 0x38d1b717, v137
	v_max_f32_e32 v135, 0x38d1b717, v153
	v_max_f32_e32 v3, 0x38d1b717, v3
	v_pk_mul_f32 v[118:119], v[128:129], v[118:119]
	v_pk_mul_f32 v[120:121], v[130:131], v[120:121]
	v_pk_mul_f32 v[128:129], v[132:133], v[134:135]
	v_fma_mixlo_f16 v3, v114, v3, 0
	v_cvt_pk_f16_f32 v119, v118, v119
	v_cvt_pk_f16_f32 v120, v120, v121
	v_cvt_pk_f16_f32 v121, v128, v129
	v_max_f32_e32 v136, 0x38d1b717, v155
	v_pack_b32_f16 v118, v3, v119
	v_alignbit_b32 v119, v120, v119, 16
	v_alignbit_b32 v120, v121, v120, 16
	v_lshrrev_b32_e32 v121, 16, v121
	v_fma_mixhi_f16 v121, v113, v136, 0
.LBB0_5369:
	s_andn2_b64 vcc, exec, s[34:35]
	v_lshl_add_u64 v[124:125], v[124:125], 0, s[18:19]
	s_cbranch_vccnz .LBB0_5371
	s_lshl_b32 s2, s21, 1
	v_lshl_add_u64 v[118:119], v[122:123], 0, s[2:3]
	v_lshl_add_u64 v[118:119], v[148:149], 1, v[118:119]
	v_add_co_u32_e32 v118, vcc, 0x1000, v118
	s_add_u32 s34, s53, s30
	s_nop 0
	v_addc_co_u32_e32 v119, vcc, 0, v119, vcc
	s_addc_u32 s35, s54, s31
	v_lshl_add_u64 v[126:127], s[34:35], 0, v[124:125]
	s_waitcnt vmcnt(4)
	v_mov_b32_e32 v118, v234
	v_mov_b32_e32 v119, v235
	v_mov_b32_e32 v120, v236
	v_mov_b32_e32 v121, v237
	v_cvt_f32_f16_e32 v3, v118
	v_cvt_f32_f16_sdwa v118, v118 dst_sel:DWORD dst_unused:UNUSED_PAD src0_sel:WORD_1
	v_cvt_f32_f16_e32 v128, v119
	v_cvt_f32_f16_sdwa v119, v119 dst_sel:DWORD dst_unused:UNUSED_PAD src0_sel:WORD_1
	v_cvt_f32_f16_e32 v129, v120
	v_cvt_f32_f16_sdwa v120, v120 dst_sel:DWORD dst_unused:UNUSED_PAD src0_sel:WORD_1
	v_cvt_f32_f16_e32 v130, v121
	v_cvt_f32_f16_sdwa v121, v121 dst_sel:DWORD dst_unused:UNUSED_PAD src0_sel:WORD_1
	v_max_f32_e32 v131, 0x38d1b717, v3
	v_max_f32_e32 v132, 0x38d1b717, v118
	v_max_f32_e32 v133, 0x38d1b717, v128
	v_max_f32_e32 v134, 0x38d1b717, v119
	v_max_f32_e32 v135, 0x38d1b717, v129
	v_max_f32_e32 v136, 0x38d1b717, v120
	v_max_f32_e32 v137, 0x38d1b717, v130
	v_max_f32_e32 v153, 0x38d1b717, v121
	v_cndmask_b32_e64 v3, v131, v3, s[0:1]
	v_cndmask_b32_e64 v118, v132, v118, s[0:1]
	v_cndmask_b32_e64 v128, v133, v128, s[0:1]
	v_cndmask_b32_e64 v119, v134, v119, s[0:1]
	v_cndmask_b32_e64 v129, v135, v129, s[0:1]
	v_cndmask_b32_e64 v120, v136, v120, s[0:1]
	v_cndmask_b32_e64 v130, v137, v130, s[0:1]
	v_cndmask_b32_e64 v121, v153, v121, s[0:1]
	v_mul_f32_e32 v112, v112, v130
	v_mul_f32_e32 v111, v111, v120
	v_mul_f32_e32 v110, v110, v129
	v_mul_f32_e32 v117, v117, v119
	v_mul_f32_e32 v116, v116, v128
	v_mul_f32_e32 v115, v115, v118
	v_mul_f32_e32 v3, v114, v3
	v_mul_f32_e32 v113, v113, v121
	v_cvt_pk_f16_f32 v118, v3, v115
	v_cvt_pk_f16_f32 v119, v116, v117
	v_cvt_pk_f16_f32 v120, v110, v111
	v_cvt_pk_f16_f32 v121, v112, v113
.LBB0_5371:
	v_lshl_add_u64 v[110:111], v[148:149], 1, v[126:127]
	s_and_b64 vcc, exec, s[4:5]
	s_mov_b64 s[34:35], -1
	global_store_dwordx4 v[110:111], v[118:121], off
	v_mul_u32_u24_e32 v240, 0x3000, v162
	v_add_u32_e32 v240, v240, v213
	v_mov_b32_e32 v241, 0
	v_lshl_add_u64 v[238:239], v[150:151], 1, v[240:241]
	v_lshl_add_u64 v[238:239], s[8:9], 0, v[238:239]
	global_load_dwordx4 v[234:237], v[238:239], off
	s_cbranch_vccnz .LBB0_5373
	v_lshl_add_u64 v[110:111], v[150:151], 1, v[122:123]
	v_add_co_u32_e32 v110, vcc, 0x2000, v110
	v_mov_b32_e32 v114, v107
	s_nop 0
	v_addc_co_u32_e32 v111, vcc, 0, v111, vcc
	v_mov_b32_e32 v115, v108
	v_pk_mov_b32 v[116:117], v[108:109], v[102:103] op_sel:[1,0]
	v_mov_b32_e32 v118, v103
	v_mov_b32_e32 v119, v104
	s_mov_b64 s[34:35], 0
	s_waitcnt vmcnt(4)
	v_mov_b32_e32 v110, v226
	v_mov_b32_e32 v111, v227
	v_mov_b32_e32 v112, v228
	v_mov_b32_e32 v113, v229
	v_cvt_f32_f16_e32 v3, v110
	v_cvt_f32_f16_sdwa v110, v110 dst_sel:DWORD dst_unused:UNUSED_PAD src0_sel:WORD_1
	v_cvt_f32_f16_e32 v120, v111
	v_cvt_f32_f16_sdwa v121, v111 dst_sel:DWORD dst_unused:UNUSED_PAD src0_sel:WORD_1
	v_cvt_f32_f16_e32 v126, v112
	v_cvt_f32_f16_sdwa v127, v112 dst_sel:DWORD dst_unused:UNUSED_PAD src0_sel:WORD_1
	v_cvt_f32_f16_e32 v128, v113
	v_cvt_f32_f16_sdwa v129, v113 dst_sel:DWORD dst_unused:UNUSED_PAD src0_sel:WORD_1
	v_max_f32_e32 v110, 0x38d1b717, v110
	v_max_f32_e32 v111, 0x38d1b717, v120
	v_max_f32_e32 v112, 0x38d1b717, v121
	v_max_f32_e32 v113, 0x38d1b717, v126
	v_max_f32_e32 v120, 0x38d1b717, v127
	v_max_f32_e32 v121, 0x38d1b717, v128
	v_max_f32_e32 v3, 0x38d1b717, v3
	v_pk_mul_f32 v[110:111], v[114:115], v[110:111]
	v_pk_mul_f32 v[112:113], v[116:117], v[112:113]
	v_pk_mul_f32 v[114:115], v[118:119], v[120:121]
	v_fma_mixlo_f16 v3, v106, v3, 0
	v_cvt_pk_f16_f32 v111, v110, v111
	v_cvt_pk_f16_f32 v112, v112, v113
	v_cvt_pk_f16_f32 v113, v114, v115
	v_max_f32_e32 v126, 0x38d1b717, v129
	v_pack_b32_f16 v110, v3, v111
	v_alignbit_b32 v111, v112, v111, 16
	v_alignbit_b32 v112, v113, v112, 16
	v_lshrrev_b32_e32 v113, 16, v113
	v_fma_mixhi_f16 v113, v105, v126, 0
.LBB0_5373:
	s_andn2_b64 vcc, exec, s[34:35]
	s_cbranch_vccnz .LBB0_5375
	s_lshl_b32 s2, s21, 1
	v_lshl_add_u64 v[4:5], v[122:123], 0, s[2:3]
	v_lshl_add_u64 v[4:5], v[148:149], 1, v[4:5]
	v_add_co_u32_e32 v4, vcc, 0x1000, v4
	s_add_u32 s34, s53, s30
	s_nop 0
	v_addc_co_u32_e32 v5, vcc, 0, v5, vcc
	s_addc_u32 s35, s54, s31
	v_lshl_add_u64 v[4:5], s[34:35], 0, v[124:125]
	s_waitcnt vmcnt(4)
	v_mov_b32_e32 v110, v226
	v_mov_b32_e32 v111, v227
	v_mov_b32_e32 v112, v228
	v_mov_b32_e32 v113, v229
	v_cvt_f32_f16_e32 v3, v110
	v_cvt_f32_f16_sdwa v110, v110 dst_sel:DWORD dst_unused:UNUSED_PAD src0_sel:WORD_1
	v_cvt_f32_f16_e32 v114, v111
	v_cvt_f32_f16_sdwa v111, v111 dst_sel:DWORD dst_unused:UNUSED_PAD src0_sel:WORD_1
	v_cvt_f32_f16_e32 v115, v112
	v_cvt_f32_f16_sdwa v112, v112 dst_sel:DWORD dst_unused:UNUSED_PAD src0_sel:WORD_1
	v_cvt_f32_f16_e32 v116, v113
	v_cvt_f32_f16_sdwa v113, v113 dst_sel:DWORD dst_unused:UNUSED_PAD src0_sel:WORD_1
	v_max_f32_e32 v117, 0x38d1b717, v3
	v_max_f32_e32 v118, 0x38d1b717, v110
	v_max_f32_e32 v119, 0x38d1b717, v114
	v_max_f32_e32 v120, 0x38d1b717, v111
	v_max_f32_e32 v121, 0x38d1b717, v115
	v_max_f32_e32 v122, 0x38d1b717, v112
	v_max_f32_e32 v123, 0x38d1b717, v116
	v_max_f32_e32 v124, 0x38d1b717, v113
	v_cndmask_b32_e64 v3, v117, v3, s[0:1]
	v_cndmask_b32_e64 v110, v118, v110, s[0:1]
	v_cndmask_b32_e64 v114, v119, v114, s[0:1]
	v_cndmask_b32_e64 v111, v120, v111, s[0:1]
	v_cndmask_b32_e64 v115, v121, v115, s[0:1]
	v_cndmask_b32_e64 v112, v122, v112, s[0:1]
	v_cndmask_b32_e64 v116, v123, v116, s[0:1]
	v_cndmask_b32_e64 v113, v124, v113, s[0:1]
	v_mul_f32_e32 v104, v104, v116
	v_mul_f32_e32 v103, v103, v112
	v_mul_f32_e32 v102, v102, v115
	v_mul_f32_e32 v109, v109, v111
	v_mul_f32_e32 v108, v108, v114
	v_mul_f32_e32 v107, v107, v110
	v_mul_f32_e32 v3, v106, v3
	v_mul_f32_e32 v105, v105, v113
	v_cvt_pk_f16_f32 v110, v3, v107
	v_cvt_pk_f16_f32 v111, v108, v109
	v_cvt_pk_f16_f32 v112, v102, v103
	v_cvt_pk_f16_f32 v113, v104, v105
.LBB0_5375:
	v_lshl_add_u64 v[4:5], v[148:149], 1, v[4:5]
	global_store_dwordx4 v[4:5], v[110:113], off offset:256
	v_mul_u32_u24_e32 v240, 0x3000, v160
	v_add_u32_e32 v240, v240, v213
	v_mov_b32_e32 v241, 0
	v_lshl_add_u64 v[238:239], v[148:149], 1, v[240:241]
	v_lshl_add_u64 v[238:239], s[8:9], 0, v[238:239]
	global_load_dwordx4 v[226:229], v[238:239], off
	v_mov_b64_e32 v[4:5], s[8:9]
	v_ashrrev_i32_e32 v163, 31, v162
	v_lshlrev_b64 v[108:109], 11, v[162:163]
	v_mad_i64_i32 v[106:107], s[34:35], v162, s62, v[4:5]
	s_mov_b64 s[34:35], -1
	s_and_b64 vcc, exec, s[4:5]
	v_lshl_add_u64 v[4:5], s[10:11], 0, v[108:109]
	s_cbranch_vccnz .LBB0_5377
	v_lshl_add_u64 v[102:103], v[148:149], 1, v[106:107]
	v_add_co_u32_e32 v102, vcc, 0x2000, v102
	v_mov_b32_e32 v112, v99
	s_nop 0
	v_addc_co_u32_e32 v103, vcc, 0, v103, vcc
	v_mov_b32_e32 v113, v100
	v_pk_mov_b32 v[114:115], v[100:101], v[94:95] op_sel:[1,0]
	v_mov_b32_e32 v116, v95
	v_mov_b32_e32 v117, v96
	v_lshl_add_u64 v[110:111], s[10:11], 0, v[108:109]
	s_mov_b64 s[34:35], 0
	s_waitcnt vmcnt(4)
	v_mov_b32_e32 v102, v230
	v_mov_b32_e32 v103, v231
	v_mov_b32_e32 v104, v232
	v_mov_b32_e32 v105, v233
	v_cvt_f32_f16_e32 v3, v102
	v_cvt_f32_f16_sdwa v102, v102 dst_sel:DWORD dst_unused:UNUSED_PAD src0_sel:WORD_1
	v_cvt_f32_f16_e32 v118, v103
	v_cvt_f32_f16_sdwa v119, v103 dst_sel:DWORD dst_unused:UNUSED_PAD src0_sel:WORD_1
	v_cvt_f32_f16_e32 v120, v104
	v_cvt_f32_f16_sdwa v121, v104 dst_sel:DWORD dst_unused:UNUSED_PAD src0_sel:WORD_1
	v_cvt_f32_f16_e32 v122, v105
	v_cvt_f32_f16_sdwa v123, v105 dst_sel:DWORD dst_unused:UNUSED_PAD src0_sel:WORD_1
	v_max_f32_e32 v102, 0x38d1b717, v102
	v_max_f32_e32 v103, 0x38d1b717, v118
	v_max_f32_e32 v104, 0x38d1b717, v119
	v_max_f32_e32 v105, 0x38d1b717, v120
	v_max_f32_e32 v118, 0x38d1b717, v121
	v_max_f32_e32 v119, 0x38d1b717, v122
	v_max_f32_e32 v3, 0x38d1b717, v3
	v_pk_mul_f32 v[102:103], v[112:113], v[102:103]
	v_pk_mul_f32 v[104:105], v[114:115], v[104:105]
	v_pk_mul_f32 v[112:113], v[116:117], v[118:119]
	v_fma_mixlo_f16 v3, v98, v3, 0
	v_cvt_pk_f16_f32 v103, v102, v103
	v_cvt_pk_f16_f32 v104, v104, v105
	v_cvt_pk_f16_f32 v105, v112, v113
	v_max_f32_e32 v120, 0x38d1b717, v123
	v_pack_b32_f16 v102, v3, v103
	v_alignbit_b32 v103, v104, v103, 16
	v_alignbit_b32 v104, v105, v104, 16
	v_lshrrev_b32_e32 v105, 16, v105
	v_fma_mixhi_f16 v105, v97, v120, 0
.LBB0_5377:
	s_andn2_b64 vcc, exec, s[34:35]
	v_lshl_add_u64 v[108:109], v[108:109], 0, s[18:19]
	s_cbranch_vccnz .LBB0_5379
	s_lshl_b32 s2, s21, 1
	v_lshl_add_u64 v[102:103], v[106:107], 0, s[2:3]
	v_lshl_add_u64 v[102:103], v[148:149], 1, v[102:103]
	v_add_co_u32_e32 v102, vcc, 0x1000, v102
	s_add_u32 s34, s53, s30
	s_nop 0
	v_addc_co_u32_e32 v103, vcc, 0, v103, vcc
	s_addc_u32 s35, s54, s31
	v_lshl_add_u64 v[110:111], s[34:35], 0, v[108:109]
	s_waitcnt vmcnt(4)
	v_mov_b32_e32 v102, v230
	v_mov_b32_e32 v103, v231
	v_mov_b32_e32 v104, v232
	v_mov_b32_e32 v105, v233
	v_cvt_f32_f16_e32 v3, v102
	v_cvt_f32_f16_sdwa v102, v102 dst_sel:DWORD dst_unused:UNUSED_PAD src0_sel:WORD_1
	v_cvt_f32_f16_e32 v112, v103
	v_cvt_f32_f16_sdwa v103, v103 dst_sel:DWORD dst_unused:UNUSED_PAD src0_sel:WORD_1
	v_cvt_f32_f16_e32 v113, v104
	v_cvt_f32_f16_sdwa v104, v104 dst_sel:DWORD dst_unused:UNUSED_PAD src0_sel:WORD_1
	v_cvt_f32_f16_e32 v114, v105
	v_cvt_f32_f16_sdwa v105, v105 dst_sel:DWORD dst_unused:UNUSED_PAD src0_sel:WORD_1
	v_max_f32_e32 v115, 0x38d1b717, v3
	v_max_f32_e32 v116, 0x38d1b717, v102
	v_max_f32_e32 v117, 0x38d1b717, v112
	v_max_f32_e32 v118, 0x38d1b717, v103
	v_max_f32_e32 v119, 0x38d1b717, v113
	v_max_f32_e32 v120, 0x38d1b717, v104
	v_max_f32_e32 v121, 0x38d1b717, v114
	v_max_f32_e32 v122, 0x38d1b717, v105
	v_cndmask_b32_e64 v3, v115, v3, s[0:1]
	v_cndmask_b32_e64 v102, v116, v102, s[0:1]
	v_cndmask_b32_e64 v112, v117, v112, s[0:1]
	v_cndmask_b32_e64 v103, v118, v103, s[0:1]
	v_cndmask_b32_e64 v113, v119, v113, s[0:1]
	v_cndmask_b32_e64 v104, v120, v104, s[0:1]
	v_cndmask_b32_e64 v114, v121, v114, s[0:1]
	v_cndmask_b32_e64 v105, v122, v105, s[0:1]
	v_mul_f32_e32 v96, v96, v114
	v_mul_f32_e32 v95, v95, v104
	v_mul_f32_e32 v94, v94, v113
	v_mul_f32_e32 v101, v101, v103
	v_mul_f32_e32 v100, v100, v112
	v_mul_f32_e32 v99, v99, v102
	v_mul_f32_e32 v3, v98, v3
	v_mul_f32_e32 v97, v97, v105
	v_cvt_pk_f16_f32 v102, v3, v99
	v_cvt_pk_f16_f32 v103, v100, v101
	v_cvt_pk_f16_f32 v104, v94, v95
	v_cvt_pk_f16_f32 v105, v96, v97
.LBB0_5379:
	v_lshl_add_u64 v[94:95], v[148:149], 1, v[110:111]
	s_and_b64 vcc, exec, s[4:5]
	s_mov_b64 s[34:35], -1
	global_store_dwordx4 v[94:95], v[102:105], off
	v_mul_u32_u24_e32 v240, 0x3000, v160
	v_add_u32_e32 v240, v240, v213
	v_mov_b32_e32 v241, 0
	v_lshl_add_u64 v[238:239], v[150:151], 1, v[240:241]
	v_lshl_add_u64 v[238:239], s[8:9], 0, v[238:239]
	global_load_dwordx4 v[230:233], v[238:239], off
	s_cbranch_vccnz .LBB0_5381
	v_lshl_add_u64 v[94:95], v[150:151], 1, v[106:107]
	v_add_co_u32_e32 v94, vcc, 0x2000, v94
	v_mov_b32_e32 v98, v91
	s_nop 0
	v_addc_co_u32_e32 v95, vcc, 0, v95, vcc
	v_mov_b32_e32 v99, v92
	v_pk_mov_b32 v[100:101], v[92:93], v[86:87] op_sel:[1,0]
	v_mov_b32_e32 v102, v87
	v_mov_b32_e32 v103, v88
	s_mov_b64 s[34:35], 0
	s_waitcnt vmcnt(4)
	v_mov_b32_e32 v94, v234
	v_mov_b32_e32 v95, v235
	v_mov_b32_e32 v96, v236
	v_mov_b32_e32 v97, v237
	v_cvt_f32_f16_e32 v3, v94
	v_cvt_f32_f16_sdwa v94, v94 dst_sel:DWORD dst_unused:UNUSED_PAD src0_sel:WORD_1
	v_cvt_f32_f16_e32 v104, v95
	v_cvt_f32_f16_sdwa v105, v95 dst_sel:DWORD dst_unused:UNUSED_PAD src0_sel:WORD_1
	v_cvt_f32_f16_e32 v110, v96
	v_cvt_f32_f16_sdwa v111, v96 dst_sel:DWORD dst_unused:UNUSED_PAD src0_sel:WORD_1
	v_cvt_f32_f16_e32 v112, v97
	v_cvt_f32_f16_sdwa v113, v97 dst_sel:DWORD dst_unused:UNUSED_PAD src0_sel:WORD_1
	v_max_f32_e32 v94, 0x38d1b717, v94
	v_max_f32_e32 v95, 0x38d1b717, v104
	v_max_f32_e32 v96, 0x38d1b717, v105
	v_max_f32_e32 v97, 0x38d1b717, v110
	v_max_f32_e32 v104, 0x38d1b717, v111
	v_max_f32_e32 v105, 0x38d1b717, v112
	v_max_f32_e32 v3, 0x38d1b717, v3
	v_pk_mul_f32 v[94:95], v[98:99], v[94:95]
	v_pk_mul_f32 v[96:97], v[100:101], v[96:97]
	v_pk_mul_f32 v[98:99], v[102:103], v[104:105]
	v_fma_mixlo_f16 v3, v90, v3, 0
	v_cvt_pk_f16_f32 v95, v94, v95
	v_cvt_pk_f16_f32 v96, v96, v97
	v_cvt_pk_f16_f32 v97, v98, v99
	v_max_f32_e32 v110, 0x38d1b717, v113
	v_pack_b32_f16 v94, v3, v95
	v_alignbit_b32 v95, v96, v95, 16
	v_alignbit_b32 v96, v97, v96, 16
	v_lshrrev_b32_e32 v97, 16, v97
	v_fma_mixhi_f16 v97, v89, v110, 0
.LBB0_5381:
	s_andn2_b64 vcc, exec, s[34:35]
	s_cbranch_vccnz .LBB0_5383
	s_lshl_b32 s2, s21, 1
	v_lshl_add_u64 v[4:5], v[106:107], 0, s[2:3]
	v_lshl_add_u64 v[4:5], v[148:149], 1, v[4:5]
	v_add_co_u32_e32 v4, vcc, 0x1000, v4
	s_add_u32 s34, s53, s30
	s_nop 0
	v_addc_co_u32_e32 v5, vcc, 0, v5, vcc
	s_addc_u32 s35, s54, s31
	v_lshl_add_u64 v[4:5], s[34:35], 0, v[108:109]
	s_waitcnt vmcnt(4)
	v_mov_b32_e32 v94, v234
	v_mov_b32_e32 v95, v235
	v_mov_b32_e32 v96, v236
	v_mov_b32_e32 v97, v237
	v_cvt_f32_f16_e32 v3, v94
	v_cvt_f32_f16_sdwa v94, v94 dst_sel:DWORD dst_unused:UNUSED_PAD src0_sel:WORD_1
	v_cvt_f32_f16_e32 v98, v95
	v_cvt_f32_f16_sdwa v95, v95 dst_sel:DWORD dst_unused:UNUSED_PAD src0_sel:WORD_1
	v_cvt_f32_f16_e32 v99, v96
	v_cvt_f32_f16_sdwa v96, v96 dst_sel:DWORD dst_unused:UNUSED_PAD src0_sel:WORD_1
	v_cvt_f32_f16_e32 v100, v97
	v_cvt_f32_f16_sdwa v97, v97 dst_sel:DWORD dst_unused:UNUSED_PAD src0_sel:WORD_1
	v_max_f32_e32 v101, 0x38d1b717, v3
	v_max_f32_e32 v102, 0x38d1b717, v94
	v_max_f32_e32 v103, 0x38d1b717, v98
	v_max_f32_e32 v104, 0x38d1b717, v95
	v_max_f32_e32 v105, 0x38d1b717, v99
	v_max_f32_e32 v106, 0x38d1b717, v96
	v_max_f32_e32 v107, 0x38d1b717, v100
	v_max_f32_e32 v108, 0x38d1b717, v97
	v_cndmask_b32_e64 v3, v101, v3, s[0:1]
	v_cndmask_b32_e64 v94, v102, v94, s[0:1]
	v_cndmask_b32_e64 v98, v103, v98, s[0:1]
	v_cndmask_b32_e64 v95, v104, v95, s[0:1]
	v_cndmask_b32_e64 v99, v105, v99, s[0:1]
	v_cndmask_b32_e64 v96, v106, v96, s[0:1]
	v_cndmask_b32_e64 v100, v107, v100, s[0:1]
	v_cndmask_b32_e64 v97, v108, v97, s[0:1]
	v_mul_f32_e32 v88, v88, v100
	v_mul_f32_e32 v87, v87, v96
	v_mul_f32_e32 v86, v86, v99
	v_mul_f32_e32 v93, v93, v95
	v_mul_f32_e32 v92, v92, v98
	v_mul_f32_e32 v91, v91, v94
	v_mul_f32_e32 v3, v90, v3
	v_mul_f32_e32 v89, v89, v97
	v_cvt_pk_f16_f32 v94, v3, v91
	v_cvt_pk_f16_f32 v95, v92, v93
	v_cvt_pk_f16_f32 v96, v86, v87
	v_cvt_pk_f16_f32 v97, v88, v89
.LBB0_5383:
	v_lshl_add_u64 v[4:5], v[148:149], 1, v[4:5]
	global_store_dwordx4 v[4:5], v[94:97], off offset:256
	v_mul_u32_u24_e32 v240, 0x3000, v158
	v_add_u32_e32 v240, v240, v213
	v_mov_b32_e32 v241, 0
	v_lshl_add_u64 v[238:239], v[148:149], 1, v[240:241]
	v_lshl_add_u64 v[238:239], s[8:9], 0, v[238:239]
	global_load_dwordx4 v[234:237], v[238:239], off
	v_mov_b64_e32 v[4:5], s[8:9]
	v_ashrrev_i32_e32 v161, 31, v160
	v_lshlrev_b64 v[92:93], 11, v[160:161]
	v_mad_i64_i32 v[90:91], s[34:35], v160, s62, v[4:5]
	s_mov_b64 s[34:35], -1
	s_and_b64 vcc, exec, s[4:5]
	v_lshl_add_u64 v[4:5], s[10:11], 0, v[92:93]
	s_cbranch_vccnz .LBB0_5385
	v_lshl_add_u64 v[86:87], v[148:149], 1, v[90:91]
	v_add_co_u32_e32 v86, vcc, 0x2000, v86
	v_mov_b32_e32 v96, v83
	s_nop 0
	v_addc_co_u32_e32 v87, vcc, 0, v87, vcc
	v_mov_b32_e32 v97, v84
	v_pk_mov_b32 v[98:99], v[84:85], v[78:79] op_sel:[1,0]
	v_mov_b32_e32 v100, v79
	v_mov_b32_e32 v101, v80
	v_lshl_add_u64 v[94:95], s[10:11], 0, v[92:93]
	s_mov_b64 s[34:35], 0
	s_waitcnt vmcnt(4)
	v_mov_b32_e32 v86, v226
	v_mov_b32_e32 v87, v227
	v_mov_b32_e32 v88, v228
	v_mov_b32_e32 v89, v229
	v_cvt_f32_f16_e32 v3, v86
	v_cvt_f32_f16_sdwa v86, v86 dst_sel:DWORD dst_unused:UNUSED_PAD src0_sel:WORD_1
	v_cvt_f32_f16_e32 v102, v87
	v_cvt_f32_f16_sdwa v103, v87 dst_sel:DWORD dst_unused:UNUSED_PAD src0_sel:WORD_1
	v_cvt_f32_f16_e32 v104, v88
	v_cvt_f32_f16_sdwa v105, v88 dst_sel:DWORD dst_unused:UNUSED_PAD src0_sel:WORD_1
	v_cvt_f32_f16_e32 v106, v89
	v_cvt_f32_f16_sdwa v107, v89 dst_sel:DWORD dst_unused:UNUSED_PAD src0_sel:WORD_1
	v_max_f32_e32 v86, 0x38d1b717, v86
	v_max_f32_e32 v87, 0x38d1b717, v102
	v_max_f32_e32 v88, 0x38d1b717, v103
	v_max_f32_e32 v89, 0x38d1b717, v104
	v_max_f32_e32 v102, 0x38d1b717, v105
	v_max_f32_e32 v103, 0x38d1b717, v106
	v_max_f32_e32 v3, 0x38d1b717, v3
	v_pk_mul_f32 v[86:87], v[96:97], v[86:87]
	v_pk_mul_f32 v[88:89], v[98:99], v[88:89]
	v_pk_mul_f32 v[96:97], v[100:101], v[102:103]
	v_fma_mixlo_f16 v3, v82, v3, 0
	v_cvt_pk_f16_f32 v87, v86, v87
	v_cvt_pk_f16_f32 v88, v88, v89
	v_cvt_pk_f16_f32 v89, v96, v97
	v_max_f32_e32 v104, 0x38d1b717, v107
	v_pack_b32_f16 v86, v3, v87
	v_alignbit_b32 v87, v88, v87, 16
	v_alignbit_b32 v88, v89, v88, 16
	v_lshrrev_b32_e32 v89, 16, v89
	v_fma_mixhi_f16 v89, v81, v104, 0
.LBB0_5385:
	s_andn2_b64 vcc, exec, s[34:35]
	v_lshl_add_u64 v[92:93], v[92:93], 0, s[18:19]
	s_cbranch_vccnz .LBB0_5387
	s_lshl_b32 s2, s21, 1
	v_lshl_add_u64 v[86:87], v[90:91], 0, s[2:3]
	v_lshl_add_u64 v[86:87], v[148:149], 1, v[86:87]
	v_add_co_u32_e32 v86, vcc, 0x1000, v86
	s_add_u32 s34, s53, s30
	s_nop 0
	v_addc_co_u32_e32 v87, vcc, 0, v87, vcc
	s_addc_u32 s35, s54, s31
	v_lshl_add_u64 v[94:95], s[34:35], 0, v[92:93]
	s_waitcnt vmcnt(4)
	v_mov_b32_e32 v86, v226
	v_mov_b32_e32 v87, v227
	v_mov_b32_e32 v88, v228
	v_mov_b32_e32 v89, v229
	v_cvt_f32_f16_e32 v3, v86
	v_cvt_f32_f16_sdwa v86, v86 dst_sel:DWORD dst_unused:UNUSED_PAD src0_sel:WORD_1
	v_cvt_f32_f16_e32 v96, v87
	v_cvt_f32_f16_sdwa v87, v87 dst_sel:DWORD dst_unused:UNUSED_PAD src0_sel:WORD_1
	v_cvt_f32_f16_e32 v97, v88
	v_cvt_f32_f16_sdwa v88, v88 dst_sel:DWORD dst_unused:UNUSED_PAD src0_sel:WORD_1
	v_cvt_f32_f16_e32 v98, v89
	v_cvt_f32_f16_sdwa v89, v89 dst_sel:DWORD dst_unused:UNUSED_PAD src0_sel:WORD_1
	v_max_f32_e32 v99, 0x38d1b717, v3
	v_max_f32_e32 v100, 0x38d1b717, v86
	v_max_f32_e32 v101, 0x38d1b717, v96
	v_max_f32_e32 v102, 0x38d1b717, v87
	v_max_f32_e32 v103, 0x38d1b717, v97
	v_max_f32_e32 v104, 0x38d1b717, v88
	v_max_f32_e32 v105, 0x38d1b717, v98
	v_max_f32_e32 v106, 0x38d1b717, v89
	v_cndmask_b32_e64 v3, v99, v3, s[0:1]
	v_cndmask_b32_e64 v86, v100, v86, s[0:1]
	v_cndmask_b32_e64 v96, v101, v96, s[0:1]
	v_cndmask_b32_e64 v87, v102, v87, s[0:1]
	v_cndmask_b32_e64 v97, v103, v97, s[0:1]
	v_cndmask_b32_e64 v88, v104, v88, s[0:1]
	v_cndmask_b32_e64 v98, v105, v98, s[0:1]
	v_cndmask_b32_e64 v89, v106, v89, s[0:1]
	v_mul_f32_e32 v80, v80, v98
	v_mul_f32_e32 v79, v79, v88
	v_mul_f32_e32 v78, v78, v97
	v_mul_f32_e32 v85, v85, v87
	v_mul_f32_e32 v84, v84, v96
	v_mul_f32_e32 v83, v83, v86
	v_mul_f32_e32 v3, v82, v3
	v_mul_f32_e32 v81, v81, v89
	v_cvt_pk_f16_f32 v86, v3, v83
	v_cvt_pk_f16_f32 v87, v84, v85
	v_cvt_pk_f16_f32 v88, v78, v79
	v_cvt_pk_f16_f32 v89, v80, v81
.LBB0_5387:
	v_lshl_add_u64 v[78:79], v[148:149], 1, v[94:95]
	s_and_b64 vcc, exec, s[4:5]
	s_mov_b64 s[34:35], -1
	global_store_dwordx4 v[78:79], v[86:89], off
	v_mul_u32_u24_e32 v240, 0x3000, v158
	v_add_u32_e32 v240, v240, v213
	v_mov_b32_e32 v241, 0
	v_lshl_add_u64 v[238:239], v[150:151], 1, v[240:241]
	v_lshl_add_u64 v[238:239], s[8:9], 0, v[238:239]
	global_load_dwordx4 v[226:229], v[238:239], off
	s_cbranch_vccnz .LBB0_5389
	v_lshl_add_u64 v[78:79], v[150:151], 1, v[90:91]
	v_add_co_u32_e32 v78, vcc, 0x2000, v78
	v_mov_b32_e32 v82, v75
	s_nop 0
	v_addc_co_u32_e32 v79, vcc, 0, v79, vcc
	v_mov_b32_e32 v83, v76
	v_pk_mov_b32 v[84:85], v[76:77], v[70:71] op_sel:[1,0]
	v_mov_b32_e32 v86, v71
	v_mov_b32_e32 v87, v72
	s_mov_b64 s[34:35], 0
	s_waitcnt vmcnt(4)
	v_mov_b32_e32 v78, v230
	v_mov_b32_e32 v79, v231
	v_mov_b32_e32 v80, v232
	v_mov_b32_e32 v81, v233
	v_cvt_f32_f16_e32 v3, v78
	v_cvt_f32_f16_sdwa v78, v78 dst_sel:DWORD dst_unused:UNUSED_PAD src0_sel:WORD_1
	v_cvt_f32_f16_e32 v88, v79
	v_cvt_f32_f16_sdwa v89, v79 dst_sel:DWORD dst_unused:UNUSED_PAD src0_sel:WORD_1
	v_cvt_f32_f16_e32 v94, v80
	v_cvt_f32_f16_sdwa v95, v80 dst_sel:DWORD dst_unused:UNUSED_PAD src0_sel:WORD_1
	v_cvt_f32_f16_e32 v96, v81
	v_cvt_f32_f16_sdwa v97, v81 dst_sel:DWORD dst_unused:UNUSED_PAD src0_sel:WORD_1
	v_max_f32_e32 v78, 0x38d1b717, v78
	v_max_f32_e32 v79, 0x38d1b717, v88
	v_max_f32_e32 v80, 0x38d1b717, v89
	v_max_f32_e32 v81, 0x38d1b717, v94
	v_max_f32_e32 v88, 0x38d1b717, v95
	v_max_f32_e32 v89, 0x38d1b717, v96
	v_max_f32_e32 v3, 0x38d1b717, v3
	v_pk_mul_f32 v[78:79], v[82:83], v[78:79]
	v_pk_mul_f32 v[80:81], v[84:85], v[80:81]
	v_pk_mul_f32 v[82:83], v[86:87], v[88:89]
	v_fma_mixlo_f16 v3, v74, v3, 0
	v_cvt_pk_f16_f32 v79, v78, v79
	v_cvt_pk_f16_f32 v80, v80, v81
	v_cvt_pk_f16_f32 v81, v82, v83
	v_max_f32_e32 v94, 0x38d1b717, v97
	v_pack_b32_f16 v78, v3, v79
	v_alignbit_b32 v79, v80, v79, 16
	v_alignbit_b32 v80, v81, v80, 16
	v_lshrrev_b32_e32 v81, 16, v81
	v_fma_mixhi_f16 v81, v73, v94, 0
.LBB0_5389:
	s_andn2_b64 vcc, exec, s[34:35]
	s_cbranch_vccnz .LBB0_5391
	s_lshl_b32 s2, s21, 1
	v_lshl_add_u64 v[4:5], v[90:91], 0, s[2:3]
	v_lshl_add_u64 v[4:5], v[148:149], 1, v[4:5]
	v_add_co_u32_e32 v4, vcc, 0x1000, v4
	s_add_u32 s34, s53, s30
	s_nop 0
	v_addc_co_u32_e32 v5, vcc, 0, v5, vcc
	s_addc_u32 s35, s54, s31
	v_lshl_add_u64 v[4:5], s[34:35], 0, v[92:93]
	s_waitcnt vmcnt(4)
	v_mov_b32_e32 v78, v230
	v_mov_b32_e32 v79, v231
	v_mov_b32_e32 v80, v232
	v_mov_b32_e32 v81, v233
	v_cvt_f32_f16_e32 v3, v78
	v_cvt_f32_f16_sdwa v78, v78 dst_sel:DWORD dst_unused:UNUSED_PAD src0_sel:WORD_1
	v_cvt_f32_f16_e32 v82, v79
	v_cvt_f32_f16_sdwa v79, v79 dst_sel:DWORD dst_unused:UNUSED_PAD src0_sel:WORD_1
	v_cvt_f32_f16_e32 v83, v80
	v_cvt_f32_f16_sdwa v80, v80 dst_sel:DWORD dst_unused:UNUSED_PAD src0_sel:WORD_1
	v_cvt_f32_f16_e32 v84, v81
	v_cvt_f32_f16_sdwa v81, v81 dst_sel:DWORD dst_unused:UNUSED_PAD src0_sel:WORD_1
	v_max_f32_e32 v85, 0x38d1b717, v3
	v_max_f32_e32 v86, 0x38d1b717, v78
	v_max_f32_e32 v87, 0x38d1b717, v82
	v_max_f32_e32 v88, 0x38d1b717, v79
	v_max_f32_e32 v89, 0x38d1b717, v83
	v_max_f32_e32 v90, 0x38d1b717, v80
	v_max_f32_e32 v91, 0x38d1b717, v84
	v_max_f32_e32 v92, 0x38d1b717, v81
	v_cndmask_b32_e64 v3, v85, v3, s[0:1]
	v_cndmask_b32_e64 v78, v86, v78, s[0:1]
	v_cndmask_b32_e64 v82, v87, v82, s[0:1]
	v_cndmask_b32_e64 v79, v88, v79, s[0:1]
	v_cndmask_b32_e64 v83, v89, v83, s[0:1]
	v_cndmask_b32_e64 v80, v90, v80, s[0:1]
	v_cndmask_b32_e64 v84, v91, v84, s[0:1]
	v_cndmask_b32_e64 v81, v92, v81, s[0:1]
	v_mul_f32_e32 v72, v72, v84
	v_mul_f32_e32 v71, v71, v80
	v_mul_f32_e32 v70, v70, v83
	v_mul_f32_e32 v77, v77, v79
	v_mul_f32_e32 v76, v76, v82
	v_mul_f32_e32 v75, v75, v78
	v_mul_f32_e32 v3, v74, v3
	v_mul_f32_e32 v73, v73, v81
	v_cvt_pk_f16_f32 v78, v3, v75
	v_cvt_pk_f16_f32 v79, v76, v77
	v_cvt_pk_f16_f32 v80, v70, v71
	v_cvt_pk_f16_f32 v81, v72, v73
.LBB0_5391:
	v_lshl_add_u64 v[4:5], v[148:149], 1, v[4:5]
	global_store_dwordx4 v[4:5], v[78:81], off offset:256
	v_mul_u32_u24_e32 v240, 0x3000, v156
	v_add_u32_e32 v240, v240, v213
	v_mov_b32_e32 v241, 0
	v_lshl_add_u64 v[238:239], v[148:149], 1, v[240:241]
	v_lshl_add_u64 v[238:239], s[8:9], 0, v[238:239]
	global_load_dwordx4 v[230:233], v[238:239], off
	v_mov_b64_e32 v[4:5], s[8:9]
	v_ashrrev_i32_e32 v159, 31, v158
	v_lshlrev_b64 v[76:77], 11, v[158:159]
	v_mad_i64_i32 v[74:75], s[34:35], v158, s62, v[4:5]
	s_mov_b64 s[34:35], -1
	s_and_b64 vcc, exec, s[4:5]
	v_lshl_add_u64 v[4:5], s[10:11], 0, v[76:77]
	s_cbranch_vccnz .LBB0_5393
	v_lshl_add_u64 v[70:71], v[148:149], 1, v[74:75]
	v_add_co_u32_e32 v70, vcc, 0x2000, v70
	v_mov_b32_e32 v80, v67
	s_nop 0
	v_addc_co_u32_e32 v71, vcc, 0, v71, vcc
	v_mov_b32_e32 v81, v68
	v_pk_mov_b32 v[82:83], v[68:69], v[62:63] op_sel:[1,0]
	v_mov_b32_e32 v84, v63
	v_mov_b32_e32 v85, v64
	v_lshl_add_u64 v[78:79], s[10:11], 0, v[76:77]
	s_mov_b64 s[34:35], 0
	s_waitcnt vmcnt(4)
	v_mov_b32_e32 v70, v234
	v_mov_b32_e32 v71, v235
	v_mov_b32_e32 v72, v236
	v_mov_b32_e32 v73, v237
	v_cvt_f32_f16_e32 v3, v70
	v_cvt_f32_f16_sdwa v70, v70 dst_sel:DWORD dst_unused:UNUSED_PAD src0_sel:WORD_1
	v_cvt_f32_f16_e32 v86, v71
	v_cvt_f32_f16_sdwa v87, v71 dst_sel:DWORD dst_unused:UNUSED_PAD src0_sel:WORD_1
	v_cvt_f32_f16_e32 v88, v72
	v_cvt_f32_f16_sdwa v89, v72 dst_sel:DWORD dst_unused:UNUSED_PAD src0_sel:WORD_1
	v_cvt_f32_f16_e32 v90, v73
	v_cvt_f32_f16_sdwa v91, v73 dst_sel:DWORD dst_unused:UNUSED_PAD src0_sel:WORD_1
	v_max_f32_e32 v70, 0x38d1b717, v70
	v_max_f32_e32 v71, 0x38d1b717, v86
	v_max_f32_e32 v72, 0x38d1b717, v87
	v_max_f32_e32 v73, 0x38d1b717, v88
	v_max_f32_e32 v86, 0x38d1b717, v89
	v_max_f32_e32 v87, 0x38d1b717, v90
	v_max_f32_e32 v3, 0x38d1b717, v3
	v_pk_mul_f32 v[70:71], v[80:81], v[70:71]
	v_pk_mul_f32 v[72:73], v[82:83], v[72:73]
	v_pk_mul_f32 v[80:81], v[84:85], v[86:87]
	v_fma_mixlo_f16 v3, v66, v3, 0
	v_cvt_pk_f16_f32 v71, v70, v71
	v_cvt_pk_f16_f32 v72, v72, v73
	v_cvt_pk_f16_f32 v73, v80, v81
	v_max_f32_e32 v88, 0x38d1b717, v91
	v_pack_b32_f16 v70, v3, v71
	v_alignbit_b32 v71, v72, v71, 16
	v_alignbit_b32 v72, v73, v72, 16
	v_lshrrev_b32_e32 v73, 16, v73
	v_fma_mixhi_f16 v73, v65, v88, 0
.LBB0_5393:
	s_andn2_b64 vcc, exec, s[34:35]
	v_lshl_add_u64 v[76:77], v[76:77], 0, s[18:19]
	s_cbranch_vccnz .LBB0_5395
	s_lshl_b32 s2, s21, 1
	v_lshl_add_u64 v[70:71], v[74:75], 0, s[2:3]
	v_lshl_add_u64 v[70:71], v[148:149], 1, v[70:71]
	v_add_co_u32_e32 v70, vcc, 0x1000, v70
	s_add_u32 s34, s53, s30
	s_nop 0
	v_addc_co_u32_e32 v71, vcc, 0, v71, vcc
	s_addc_u32 s35, s54, s31
	v_lshl_add_u64 v[78:79], s[34:35], 0, v[76:77]
	s_waitcnt vmcnt(4)
	v_mov_b32_e32 v70, v234
	v_mov_b32_e32 v71, v235
	v_mov_b32_e32 v72, v236
	v_mov_b32_e32 v73, v237
	v_cvt_f32_f16_e32 v3, v70
	v_cvt_f32_f16_sdwa v70, v70 dst_sel:DWORD dst_unused:UNUSED_PAD src0_sel:WORD_1
	v_cvt_f32_f16_e32 v80, v71
	v_cvt_f32_f16_sdwa v71, v71 dst_sel:DWORD dst_unused:UNUSED_PAD src0_sel:WORD_1
	v_cvt_f32_f16_e32 v81, v72
	v_cvt_f32_f16_sdwa v72, v72 dst_sel:DWORD dst_unused:UNUSED_PAD src0_sel:WORD_1
	v_cvt_f32_f16_e32 v82, v73
	v_cvt_f32_f16_sdwa v73, v73 dst_sel:DWORD dst_unused:UNUSED_PAD src0_sel:WORD_1
	v_max_f32_e32 v83, 0x38d1b717, v3
	v_max_f32_e32 v84, 0x38d1b717, v70
	v_max_f32_e32 v85, 0x38d1b717, v80
	v_max_f32_e32 v86, 0x38d1b717, v71
	v_max_f32_e32 v87, 0x38d1b717, v81
	v_max_f32_e32 v88, 0x38d1b717, v72
	v_max_f32_e32 v89, 0x38d1b717, v82
	v_max_f32_e32 v90, 0x38d1b717, v73
	v_cndmask_b32_e64 v3, v83, v3, s[0:1]
	v_cndmask_b32_e64 v70, v84, v70, s[0:1]
	v_cndmask_b32_e64 v80, v85, v80, s[0:1]
	v_cndmask_b32_e64 v71, v86, v71, s[0:1]
	v_cndmask_b32_e64 v81, v87, v81, s[0:1]
	v_cndmask_b32_e64 v72, v88, v72, s[0:1]
	v_cndmask_b32_e64 v82, v89, v82, s[0:1]
	v_cndmask_b32_e64 v73, v90, v73, s[0:1]
	v_mul_f32_e32 v64, v64, v82
	v_mul_f32_e32 v63, v63, v72
	v_mul_f32_e32 v62, v62, v81
	v_mul_f32_e32 v69, v69, v71
	v_mul_f32_e32 v68, v68, v80
	v_mul_f32_e32 v67, v67, v70
	v_mul_f32_e32 v3, v66, v3
	v_mul_f32_e32 v65, v65, v73
	v_cvt_pk_f16_f32 v70, v3, v67
	v_cvt_pk_f16_f32 v71, v68, v69
	v_cvt_pk_f16_f32 v72, v62, v63
	v_cvt_pk_f16_f32 v73, v64, v65
.LBB0_5395:
	v_lshl_add_u64 v[62:63], v[148:149], 1, v[78:79]
	s_and_b64 vcc, exec, s[4:5]
	s_mov_b64 s[34:35], -1
	global_store_dwordx4 v[62:63], v[70:73], off
	v_mul_u32_u24_e32 v240, 0x3000, v156
	v_add_u32_e32 v240, v240, v213
	v_mov_b32_e32 v241, 0
	v_lshl_add_u64 v[238:239], v[150:151], 1, v[240:241]
	v_lshl_add_u64 v[238:239], s[8:9], 0, v[238:239]
	global_load_dwordx4 v[234:237], v[238:239], off
	s_cbranch_vccnz .LBB0_5397
	v_lshl_add_u64 v[62:63], v[150:151], 1, v[74:75]
	v_add_co_u32_e32 v62, vcc, 0x2000, v62
	v_mov_b32_e32 v66, v59
	s_nop 0
	v_addc_co_u32_e32 v63, vcc, 0, v63, vcc
	v_mov_b32_e32 v67, v60
	v_pk_mov_b32 v[68:69], v[60:61], v[54:55] op_sel:[1,0]
	v_mov_b32_e32 v70, v55
	v_mov_b32_e32 v71, v56
	s_mov_b64 s[34:35], 0
	s_waitcnt vmcnt(4)
	v_mov_b32_e32 v62, v226
	v_mov_b32_e32 v63, v227
	v_mov_b32_e32 v64, v228
	v_mov_b32_e32 v65, v229
	v_cvt_f32_f16_e32 v3, v62
	v_cvt_f32_f16_sdwa v62, v62 dst_sel:DWORD dst_unused:UNUSED_PAD src0_sel:WORD_1
	v_cvt_f32_f16_e32 v72, v63
	v_cvt_f32_f16_sdwa v73, v63 dst_sel:DWORD dst_unused:UNUSED_PAD src0_sel:WORD_1
	v_cvt_f32_f16_e32 v78, v64
	v_cvt_f32_f16_sdwa v79, v64 dst_sel:DWORD dst_unused:UNUSED_PAD src0_sel:WORD_1
	v_cvt_f32_f16_e32 v80, v65
	v_cvt_f32_f16_sdwa v81, v65 dst_sel:DWORD dst_unused:UNUSED_PAD src0_sel:WORD_1
	v_max_f32_e32 v62, 0x38d1b717, v62
	v_max_f32_e32 v63, 0x38d1b717, v72
	v_max_f32_e32 v64, 0x38d1b717, v73
	v_max_f32_e32 v65, 0x38d1b717, v78
	v_max_f32_e32 v72, 0x38d1b717, v79
	v_max_f32_e32 v73, 0x38d1b717, v80
	v_max_f32_e32 v3, 0x38d1b717, v3
	v_pk_mul_f32 v[62:63], v[66:67], v[62:63]
	v_pk_mul_f32 v[64:65], v[68:69], v[64:65]
	v_pk_mul_f32 v[66:67], v[70:71], v[72:73]
	v_fma_mixlo_f16 v3, v58, v3, 0
	v_cvt_pk_f16_f32 v63, v62, v63
	v_cvt_pk_f16_f32 v64, v64, v65
	v_cvt_pk_f16_f32 v65, v66, v67
	v_max_f32_e32 v78, 0x38d1b717, v81
	v_pack_b32_f16 v62, v3, v63
	v_alignbit_b32 v63, v64, v63, 16
	v_alignbit_b32 v64, v65, v64, 16
	v_lshrrev_b32_e32 v65, 16, v65
	v_fma_mixhi_f16 v65, v57, v78, 0
.LBB0_5397:
	s_andn2_b64 vcc, exec, s[34:35]
	s_cbranch_vccnz .LBB0_5399
	s_lshl_b32 s2, s21, 1
	v_lshl_add_u64 v[4:5], v[74:75], 0, s[2:3]
	v_lshl_add_u64 v[4:5], v[148:149], 1, v[4:5]
	v_add_co_u32_e32 v4, vcc, 0x1000, v4
	s_add_u32 s34, s53, s30
	s_nop 0
	v_addc_co_u32_e32 v5, vcc, 0, v5, vcc
	s_addc_u32 s35, s54, s31
	v_lshl_add_u64 v[4:5], s[34:35], 0, v[76:77]
	s_waitcnt vmcnt(4)
	v_mov_b32_e32 v62, v226
	v_mov_b32_e32 v63, v227
	v_mov_b32_e32 v64, v228
	v_mov_b32_e32 v65, v229
	v_cvt_f32_f16_e32 v3, v62
	v_cvt_f32_f16_sdwa v62, v62 dst_sel:DWORD dst_unused:UNUSED_PAD src0_sel:WORD_1
	v_cvt_f32_f16_e32 v66, v63
	v_cvt_f32_f16_sdwa v63, v63 dst_sel:DWORD dst_unused:UNUSED_PAD src0_sel:WORD_1
	v_cvt_f32_f16_e32 v67, v64
	v_cvt_f32_f16_sdwa v64, v64 dst_sel:DWORD dst_unused:UNUSED_PAD src0_sel:WORD_1
	v_cvt_f32_f16_e32 v68, v65
	v_cvt_f32_f16_sdwa v65, v65 dst_sel:DWORD dst_unused:UNUSED_PAD src0_sel:WORD_1
	v_max_f32_e32 v69, 0x38d1b717, v3
	v_max_f32_e32 v70, 0x38d1b717, v62
	v_max_f32_e32 v71, 0x38d1b717, v66
	v_max_f32_e32 v72, 0x38d1b717, v63
	v_max_f32_e32 v73, 0x38d1b717, v67
	v_max_f32_e32 v74, 0x38d1b717, v64
	v_max_f32_e32 v75, 0x38d1b717, v68
	v_max_f32_e32 v76, 0x38d1b717, v65
	v_cndmask_b32_e64 v3, v69, v3, s[0:1]
	v_cndmask_b32_e64 v62, v70, v62, s[0:1]
	v_cndmask_b32_e64 v66, v71, v66, s[0:1]
	v_cndmask_b32_e64 v63, v72, v63, s[0:1]
	v_cndmask_b32_e64 v67, v73, v67, s[0:1]
	v_cndmask_b32_e64 v64, v74, v64, s[0:1]
	v_cndmask_b32_e64 v68, v75, v68, s[0:1]
	v_cndmask_b32_e64 v65, v76, v65, s[0:1]
	v_mul_f32_e32 v56, v56, v68
	v_mul_f32_e32 v55, v55, v64
	v_mul_f32_e32 v54, v54, v67
	v_mul_f32_e32 v61, v61, v63
	v_mul_f32_e32 v60, v60, v66
	v_mul_f32_e32 v59, v59, v62
	v_mul_f32_e32 v3, v58, v3
	v_mul_f32_e32 v57, v57, v65
	v_cvt_pk_f16_f32 v62, v3, v59
	v_cvt_pk_f16_f32 v63, v60, v61
	v_cvt_pk_f16_f32 v64, v54, v55
	v_cvt_pk_f16_f32 v65, v56, v57
.LBB0_5399:
	v_lshl_add_u64 v[4:5], v[148:149], 1, v[4:5]
	global_store_dwordx4 v[4:5], v[62:65], off offset:256
	v_mul_u32_u24_e32 v240, 0x3000, v154
	v_add_u32_e32 v240, v240, v213
	v_mov_b32_e32 v241, 0
	v_lshl_add_u64 v[238:239], v[148:149], 1, v[240:241]
	v_lshl_add_u64 v[238:239], s[8:9], 0, v[238:239]
	global_load_dwordx4 v[226:229], v[238:239], off
	v_mov_b64_e32 v[4:5], s[8:9]
	v_ashrrev_i32_e32 v157, 31, v156
	v_lshlrev_b64 v[60:61], 11, v[156:157]
	v_mad_i64_i32 v[58:59], s[34:35], v156, s62, v[4:5]
	s_mov_b64 s[34:35], -1
	s_and_b64 vcc, exec, s[4:5]
	v_lshl_add_u64 v[4:5], s[10:11], 0, v[60:61]
	s_cbranch_vccnz .LBB0_5401
	v_lshl_add_u64 v[54:55], v[148:149], 1, v[58:59]
	v_add_co_u32_e32 v54, vcc, 0x2000, v54
	v_mov_b32_e32 v64, v51
	s_nop 0
	v_addc_co_u32_e32 v55, vcc, 0, v55, vcc
	v_mov_b32_e32 v65, v52
	v_pk_mov_b32 v[66:67], v[52:53], v[46:47] op_sel:[1,0]
	v_mov_b32_e32 v68, v47
	v_mov_b32_e32 v69, v48
	v_lshl_add_u64 v[62:63], s[10:11], 0, v[60:61]
	s_mov_b64 s[34:35], 0
	s_waitcnt vmcnt(4)
	v_mov_b32_e32 v54, v230
	v_mov_b32_e32 v55, v231
	v_mov_b32_e32 v56, v232
	v_mov_b32_e32 v57, v233
	v_cvt_f32_f16_e32 v3, v54
	v_cvt_f32_f16_sdwa v54, v54 dst_sel:DWORD dst_unused:UNUSED_PAD src0_sel:WORD_1
	v_cvt_f32_f16_e32 v70, v55
	v_cvt_f32_f16_sdwa v71, v55 dst_sel:DWORD dst_unused:UNUSED_PAD src0_sel:WORD_1
	v_cvt_f32_f16_e32 v72, v56
	v_cvt_f32_f16_sdwa v73, v56 dst_sel:DWORD dst_unused:UNUSED_PAD src0_sel:WORD_1
	v_cvt_f32_f16_e32 v74, v57
	v_cvt_f32_f16_sdwa v75, v57 dst_sel:DWORD dst_unused:UNUSED_PAD src0_sel:WORD_1
	v_max_f32_e32 v54, 0x38d1b717, v54
	v_max_f32_e32 v55, 0x38d1b717, v70
	v_max_f32_e32 v56, 0x38d1b717, v71
	v_max_f32_e32 v57, 0x38d1b717, v72
	v_max_f32_e32 v70, 0x38d1b717, v73
	v_max_f32_e32 v71, 0x38d1b717, v74
	v_max_f32_e32 v3, 0x38d1b717, v3
	v_pk_mul_f32 v[54:55], v[64:65], v[54:55]
	v_pk_mul_f32 v[56:57], v[66:67], v[56:57]
	v_pk_mul_f32 v[64:65], v[68:69], v[70:71]
	v_fma_mixlo_f16 v3, v50, v3, 0
	v_cvt_pk_f16_f32 v55, v54, v55
	v_cvt_pk_f16_f32 v56, v56, v57
	v_cvt_pk_f16_f32 v57, v64, v65
	v_max_f32_e32 v72, 0x38d1b717, v75
	v_pack_b32_f16 v54, v3, v55
	v_alignbit_b32 v55, v56, v55, 16
	v_alignbit_b32 v56, v57, v56, 16
	v_lshrrev_b32_e32 v57, 16, v57
	v_fma_mixhi_f16 v57, v49, v72, 0
.LBB0_5401:
	s_andn2_b64 vcc, exec, s[34:35]
	v_lshl_add_u64 v[60:61], v[60:61], 0, s[18:19]
	s_cbranch_vccnz .LBB0_5403
	s_lshl_b32 s2, s21, 1
	v_lshl_add_u64 v[54:55], v[58:59], 0, s[2:3]
	v_lshl_add_u64 v[54:55], v[148:149], 1, v[54:55]
	v_add_co_u32_e32 v54, vcc, 0x1000, v54
	s_add_u32 s34, s53, s30
	s_nop 0
	v_addc_co_u32_e32 v55, vcc, 0, v55, vcc
	s_addc_u32 s35, s54, s31
	v_lshl_add_u64 v[62:63], s[34:35], 0, v[60:61]
	s_waitcnt vmcnt(4)
	v_mov_b32_e32 v54, v230
	v_mov_b32_e32 v55, v231
	v_mov_b32_e32 v56, v232
	v_mov_b32_e32 v57, v233
	v_cvt_f32_f16_e32 v3, v54
	v_cvt_f32_f16_sdwa v54, v54 dst_sel:DWORD dst_unused:UNUSED_PAD src0_sel:WORD_1
	v_cvt_f32_f16_e32 v64, v55
	v_cvt_f32_f16_sdwa v55, v55 dst_sel:DWORD dst_unused:UNUSED_PAD src0_sel:WORD_1
	v_cvt_f32_f16_e32 v65, v56
	v_cvt_f32_f16_sdwa v56, v56 dst_sel:DWORD dst_unused:UNUSED_PAD src0_sel:WORD_1
	v_cvt_f32_f16_e32 v66, v57
	v_cvt_f32_f16_sdwa v57, v57 dst_sel:DWORD dst_unused:UNUSED_PAD src0_sel:WORD_1
	v_max_f32_e32 v67, 0x38d1b717, v3
	v_max_f32_e32 v68, 0x38d1b717, v54
	v_max_f32_e32 v69, 0x38d1b717, v64
	v_max_f32_e32 v70, 0x38d1b717, v55
	v_max_f32_e32 v71, 0x38d1b717, v65
	v_max_f32_e32 v72, 0x38d1b717, v56
	v_max_f32_e32 v73, 0x38d1b717, v66
	v_max_f32_e32 v74, 0x38d1b717, v57
	v_cndmask_b32_e64 v3, v67, v3, s[0:1]
	v_cndmask_b32_e64 v54, v68, v54, s[0:1]
	v_cndmask_b32_e64 v64, v69, v64, s[0:1]
	v_cndmask_b32_e64 v55, v70, v55, s[0:1]
	v_cndmask_b32_e64 v65, v71, v65, s[0:1]
	v_cndmask_b32_e64 v56, v72, v56, s[0:1]
	v_cndmask_b32_e64 v66, v73, v66, s[0:1]
	v_cndmask_b32_e64 v57, v74, v57, s[0:1]
	v_mul_f32_e32 v48, v48, v66
	v_mul_f32_e32 v47, v47, v56
	v_mul_f32_e32 v46, v46, v65
	v_mul_f32_e32 v53, v53, v55
	v_mul_f32_e32 v52, v52, v64
	v_mul_f32_e32 v51, v51, v54
	v_mul_f32_e32 v3, v50, v3
	v_mul_f32_e32 v49, v49, v57
	v_cvt_pk_f16_f32 v54, v3, v51
	v_cvt_pk_f16_f32 v55, v52, v53
	v_cvt_pk_f16_f32 v56, v46, v47
	v_cvt_pk_f16_f32 v57, v48, v49
.LBB0_5403:
	v_lshl_add_u64 v[46:47], v[148:149], 1, v[62:63]
	s_and_b64 vcc, exec, s[4:5]
	s_mov_b64 s[34:35], -1
	global_store_dwordx4 v[46:47], v[54:57], off
	v_mul_u32_u24_e32 v240, 0x3000, v154
	v_add_u32_e32 v240, v240, v213
	v_mov_b32_e32 v241, 0
	v_lshl_add_u64 v[238:239], v[150:151], 1, v[240:241]
	v_lshl_add_u64 v[238:239], s[8:9], 0, v[238:239]
	global_load_dwordx4 v[230:233], v[238:239], off
	s_cbranch_vccnz .LBB0_5405
	v_lshl_add_u64 v[46:47], v[150:151], 1, v[58:59]
	v_add_co_u32_e32 v46, vcc, 0x2000, v46
	v_mov_b32_e32 v50, v43
	s_nop 0
	v_addc_co_u32_e32 v47, vcc, 0, v47, vcc
	v_mov_b32_e32 v51, v44
	v_pk_mov_b32 v[52:53], v[44:45], v[38:39] op_sel:[1,0]
	v_mov_b32_e32 v54, v39
	v_mov_b32_e32 v55, v40
	s_mov_b64 s[34:35], 0
	s_waitcnt vmcnt(4)
	v_mov_b32_e32 v46, v234
	v_mov_b32_e32 v47, v235
	v_mov_b32_e32 v48, v236
	v_mov_b32_e32 v49, v237
	v_cvt_f32_f16_e32 v3, v46
	v_cvt_f32_f16_sdwa v46, v46 dst_sel:DWORD dst_unused:UNUSED_PAD src0_sel:WORD_1
	v_cvt_f32_f16_e32 v56, v47
	v_cvt_f32_f16_sdwa v57, v47 dst_sel:DWORD dst_unused:UNUSED_PAD src0_sel:WORD_1
	v_cvt_f32_f16_e32 v62, v48
	v_cvt_f32_f16_sdwa v63, v48 dst_sel:DWORD dst_unused:UNUSED_PAD src0_sel:WORD_1
	v_cvt_f32_f16_e32 v64, v49
	v_cvt_f32_f16_sdwa v65, v49 dst_sel:DWORD dst_unused:UNUSED_PAD src0_sel:WORD_1
	v_max_f32_e32 v46, 0x38d1b717, v46
	v_max_f32_e32 v47, 0x38d1b717, v56
	v_max_f32_e32 v48, 0x38d1b717, v57
	v_max_f32_e32 v49, 0x38d1b717, v62
	v_max_f32_e32 v56, 0x38d1b717, v63
	v_max_f32_e32 v57, 0x38d1b717, v64
	v_max_f32_e32 v3, 0x38d1b717, v3
	v_pk_mul_f32 v[46:47], v[50:51], v[46:47]
	v_pk_mul_f32 v[48:49], v[52:53], v[48:49]
	v_pk_mul_f32 v[50:51], v[54:55], v[56:57]
	v_fma_mixlo_f16 v3, v42, v3, 0
	v_cvt_pk_f16_f32 v47, v46, v47
	v_cvt_pk_f16_f32 v48, v48, v49
	v_cvt_pk_f16_f32 v49, v50, v51
	v_max_f32_e32 v62, 0x38d1b717, v65
	v_pack_b32_f16 v46, v3, v47
	v_alignbit_b32 v47, v48, v47, 16
	v_alignbit_b32 v48, v49, v48, 16
	v_lshrrev_b32_e32 v49, 16, v49
	v_fma_mixhi_f16 v49, v41, v62, 0
.LBB0_5405:
	s_andn2_b64 vcc, exec, s[34:35]
	s_cbranch_vccnz .LBB0_5407
	s_lshl_b32 s2, s21, 1
	v_lshl_add_u64 v[4:5], v[58:59], 0, s[2:3]
	v_lshl_add_u64 v[4:5], v[148:149], 1, v[4:5]
	v_add_co_u32_e32 v4, vcc, 0x1000, v4
	s_add_u32 s34, s53, s30
	s_nop 0
	v_addc_co_u32_e32 v5, vcc, 0, v5, vcc
	s_addc_u32 s35, s54, s31
	v_lshl_add_u64 v[4:5], s[34:35], 0, v[60:61]
	s_waitcnt vmcnt(4)
	v_mov_b32_e32 v46, v234
	v_mov_b32_e32 v47, v235
	v_mov_b32_e32 v48, v236
	v_mov_b32_e32 v49, v237
	v_cvt_f32_f16_e32 v3, v46
	v_cvt_f32_f16_sdwa v46, v46 dst_sel:DWORD dst_unused:UNUSED_PAD src0_sel:WORD_1
	v_cvt_f32_f16_e32 v50, v47
	v_cvt_f32_f16_sdwa v47, v47 dst_sel:DWORD dst_unused:UNUSED_PAD src0_sel:WORD_1
	v_cvt_f32_f16_e32 v51, v48
	v_cvt_f32_f16_sdwa v48, v48 dst_sel:DWORD dst_unused:UNUSED_PAD src0_sel:WORD_1
	v_cvt_f32_f16_e32 v52, v49
	v_cvt_f32_f16_sdwa v49, v49 dst_sel:DWORD dst_unused:UNUSED_PAD src0_sel:WORD_1
	v_max_f32_e32 v53, 0x38d1b717, v3
	v_max_f32_e32 v54, 0x38d1b717, v46
	v_max_f32_e32 v55, 0x38d1b717, v50
	v_max_f32_e32 v56, 0x38d1b717, v47
	v_max_f32_e32 v57, 0x38d1b717, v51
	v_max_f32_e32 v58, 0x38d1b717, v48
	v_max_f32_e32 v59, 0x38d1b717, v52
	v_max_f32_e32 v60, 0x38d1b717, v49
	v_cndmask_b32_e64 v3, v53, v3, s[0:1]
	v_cndmask_b32_e64 v46, v54, v46, s[0:1]
	v_cndmask_b32_e64 v50, v55, v50, s[0:1]
	v_cndmask_b32_e64 v47, v56, v47, s[0:1]
	v_cndmask_b32_e64 v51, v57, v51, s[0:1]
	v_cndmask_b32_e64 v48, v58, v48, s[0:1]
	v_cndmask_b32_e64 v52, v59, v52, s[0:1]
	v_cndmask_b32_e64 v49, v60, v49, s[0:1]
	v_mul_f32_e32 v40, v40, v52
	v_mul_f32_e32 v39, v39, v48
	v_mul_f32_e32 v38, v38, v51
	v_mul_f32_e32 v45, v45, v47
	v_mul_f32_e32 v44, v44, v50
	v_mul_f32_e32 v43, v43, v46
	v_mul_f32_e32 v3, v42, v3
	v_mul_f32_e32 v41, v41, v49
	v_cvt_pk_f16_f32 v46, v3, v43
	v_cvt_pk_f16_f32 v47, v44, v45
	v_cvt_pk_f16_f32 v48, v38, v39
	v_cvt_pk_f16_f32 v49, v40, v41
.LBB0_5407:
	v_lshl_add_u64 v[4:5], v[148:149], 1, v[4:5]
	global_store_dwordx4 v[4:5], v[46:49], off offset:256
	v_mul_u32_u24_e32 v240, 0x3000, v152
	v_add_u32_e32 v240, v240, v213
	v_mov_b32_e32 v241, 0
	v_lshl_add_u64 v[238:239], v[148:149], 1, v[240:241]
	v_lshl_add_u64 v[238:239], s[8:9], 0, v[238:239]
	global_load_dwordx4 v[234:237], v[238:239], off
	v_mov_b64_e32 v[4:5], s[8:9]
	v_ashrrev_i32_e32 v155, 31, v154
	v_lshlrev_b64 v[44:45], 11, v[154:155]
	v_mad_i64_i32 v[42:43], s[34:35], v154, s62, v[4:5]
	s_mov_b64 s[34:35], -1
	s_and_b64 vcc, exec, s[4:5]
	v_lshl_add_u64 v[4:5], s[10:11], 0, v[44:45]
	s_cbranch_vccnz .LBB0_5409
	v_lshl_add_u64 v[38:39], v[148:149], 1, v[42:43]
	v_add_co_u32_e32 v38, vcc, 0x2000, v38
	v_mov_b32_e32 v48, v35
	s_nop 0
	v_addc_co_u32_e32 v39, vcc, 0, v39, vcc
	v_mov_b32_e32 v49, v36
	v_pk_mov_b32 v[50:51], v[36:37], v[30:31] op_sel:[1,0]
	v_mov_b32_e32 v52, v31
	v_mov_b32_e32 v53, v32
	v_lshl_add_u64 v[46:47], s[10:11], 0, v[44:45]
	s_mov_b64 s[34:35], 0
	s_waitcnt vmcnt(4)
	v_mov_b32_e32 v38, v226
	v_mov_b32_e32 v39, v227
	v_mov_b32_e32 v40, v228
	v_mov_b32_e32 v41, v229
	v_cvt_f32_f16_e32 v3, v38
	v_cvt_f32_f16_sdwa v38, v38 dst_sel:DWORD dst_unused:UNUSED_PAD src0_sel:WORD_1
	v_cvt_f32_f16_e32 v54, v39
	v_cvt_f32_f16_sdwa v55, v39 dst_sel:DWORD dst_unused:UNUSED_PAD src0_sel:WORD_1
	v_cvt_f32_f16_e32 v56, v40
	v_cvt_f32_f16_sdwa v57, v40 dst_sel:DWORD dst_unused:UNUSED_PAD src0_sel:WORD_1
	v_cvt_f32_f16_e32 v58, v41
	v_cvt_f32_f16_sdwa v59, v41 dst_sel:DWORD dst_unused:UNUSED_PAD src0_sel:WORD_1
	v_max_f32_e32 v38, 0x38d1b717, v38
	v_max_f32_e32 v39, 0x38d1b717, v54
	v_max_f32_e32 v40, 0x38d1b717, v55
	v_max_f32_e32 v41, 0x38d1b717, v56
	v_max_f32_e32 v54, 0x38d1b717, v57
	v_max_f32_e32 v55, 0x38d1b717, v58
	v_max_f32_e32 v3, 0x38d1b717, v3
	v_pk_mul_f32 v[38:39], v[48:49], v[38:39]
	v_pk_mul_f32 v[40:41], v[50:51], v[40:41]
	v_pk_mul_f32 v[48:49], v[52:53], v[54:55]
	v_fma_mixlo_f16 v3, v34, v3, 0
	v_cvt_pk_f16_f32 v39, v38, v39
	v_cvt_pk_f16_f32 v40, v40, v41
	v_cvt_pk_f16_f32 v41, v48, v49
	v_max_f32_e32 v56, 0x38d1b717, v59
	v_pack_b32_f16 v38, v3, v39
	v_alignbit_b32 v39, v40, v39, 16
	v_alignbit_b32 v40, v41, v40, 16
	v_lshrrev_b32_e32 v41, 16, v41
	v_fma_mixhi_f16 v41, v33, v56, 0
.LBB0_5409:
	s_andn2_b64 vcc, exec, s[34:35]
	v_lshl_add_u64 v[44:45], v[44:45], 0, s[18:19]
	s_cbranch_vccnz .LBB0_5411
	s_lshl_b32 s2, s21, 1
	v_lshl_add_u64 v[38:39], v[42:43], 0, s[2:3]
	v_lshl_add_u64 v[38:39], v[148:149], 1, v[38:39]
	v_add_co_u32_e32 v38, vcc, 0x1000, v38
	s_add_u32 s34, s53, s30
	s_nop 0
	v_addc_co_u32_e32 v39, vcc, 0, v39, vcc
	s_addc_u32 s35, s54, s31
	v_lshl_add_u64 v[46:47], s[34:35], 0, v[44:45]
	s_waitcnt vmcnt(4)
	v_mov_b32_e32 v38, v226
	v_mov_b32_e32 v39, v227
	v_mov_b32_e32 v40, v228
	v_mov_b32_e32 v41, v229
	v_cvt_f32_f16_e32 v3, v38
	v_cvt_f32_f16_sdwa v38, v38 dst_sel:DWORD dst_unused:UNUSED_PAD src0_sel:WORD_1
	v_cvt_f32_f16_e32 v48, v39
	v_cvt_f32_f16_sdwa v39, v39 dst_sel:DWORD dst_unused:UNUSED_PAD src0_sel:WORD_1
	v_cvt_f32_f16_e32 v49, v40
	v_cvt_f32_f16_sdwa v40, v40 dst_sel:DWORD dst_unused:UNUSED_PAD src0_sel:WORD_1
	v_cvt_f32_f16_e32 v50, v41
	v_cvt_f32_f16_sdwa v41, v41 dst_sel:DWORD dst_unused:UNUSED_PAD src0_sel:WORD_1
	v_max_f32_e32 v51, 0x38d1b717, v3
	v_max_f32_e32 v52, 0x38d1b717, v38
	v_max_f32_e32 v53, 0x38d1b717, v48
	v_max_f32_e32 v54, 0x38d1b717, v39
	v_max_f32_e32 v55, 0x38d1b717, v49
	v_max_f32_e32 v56, 0x38d1b717, v40
	v_max_f32_e32 v57, 0x38d1b717, v50
	v_max_f32_e32 v58, 0x38d1b717, v41
	v_cndmask_b32_e64 v3, v51, v3, s[0:1]
	v_cndmask_b32_e64 v38, v52, v38, s[0:1]
	v_cndmask_b32_e64 v48, v53, v48, s[0:1]
	v_cndmask_b32_e64 v39, v54, v39, s[0:1]
	v_cndmask_b32_e64 v49, v55, v49, s[0:1]
	v_cndmask_b32_e64 v40, v56, v40, s[0:1]
	v_cndmask_b32_e64 v50, v57, v50, s[0:1]
	v_cndmask_b32_e64 v41, v58, v41, s[0:1]
	v_mul_f32_e32 v32, v32, v50
	v_mul_f32_e32 v31, v31, v40
	v_mul_f32_e32 v30, v30, v49
	v_mul_f32_e32 v37, v37, v39
	v_mul_f32_e32 v36, v36, v48
	v_mul_f32_e32 v35, v35, v38
	v_mul_f32_e32 v3, v34, v3
	v_mul_f32_e32 v33, v33, v41
	v_cvt_pk_f16_f32 v38, v3, v35
	v_cvt_pk_f16_f32 v39, v36, v37
	v_cvt_pk_f16_f32 v40, v30, v31
	v_cvt_pk_f16_f32 v41, v32, v33
.LBB0_5411:
	v_lshl_add_u64 v[30:31], v[148:149], 1, v[46:47]
	s_and_b64 vcc, exec, s[4:5]
	s_mov_b64 s[34:35], -1
	global_store_dwordx4 v[30:31], v[38:41], off
	v_mul_u32_u24_e32 v240, 0x3000, v152
	v_add_u32_e32 v240, v240, v213
	v_mov_b32_e32 v241, 0
	v_lshl_add_u64 v[238:239], v[150:151], 1, v[240:241]
	v_lshl_add_u64 v[238:239], s[8:9], 0, v[238:239]
	global_load_dwordx4 v[226:229], v[238:239], off
	s_cbranch_vccnz .LBB0_5413
	v_lshl_add_u64 v[30:31], v[150:151], 1, v[42:43]
	v_add_co_u32_e32 v30, vcc, 0x2000, v30
	v_mov_b32_e32 v34, v27
	s_nop 0
	v_addc_co_u32_e32 v31, vcc, 0, v31, vcc
	v_mov_b32_e32 v35, v28
	v_pk_mov_b32 v[36:37], v[28:29], v[22:23] op_sel:[1,0]
	v_mov_b32_e32 v38, v23
	v_mov_b32_e32 v39, v24
	s_mov_b64 s[34:35], 0
	s_waitcnt vmcnt(4)
	v_mov_b32_e32 v30, v230
	v_mov_b32_e32 v31, v231
	v_mov_b32_e32 v32, v232
	v_mov_b32_e32 v33, v233
	v_cvt_f32_f16_e32 v3, v30
	v_cvt_f32_f16_sdwa v30, v30 dst_sel:DWORD dst_unused:UNUSED_PAD src0_sel:WORD_1
	v_cvt_f32_f16_e32 v40, v31
	v_cvt_f32_f16_sdwa v41, v31 dst_sel:DWORD dst_unused:UNUSED_PAD src0_sel:WORD_1
	v_cvt_f32_f16_e32 v46, v32
	v_cvt_f32_f16_sdwa v47, v32 dst_sel:DWORD dst_unused:UNUSED_PAD src0_sel:WORD_1
	v_cvt_f32_f16_e32 v48, v33
	v_cvt_f32_f16_sdwa v49, v33 dst_sel:DWORD dst_unused:UNUSED_PAD src0_sel:WORD_1
	v_max_f32_e32 v30, 0x38d1b717, v30
	v_max_f32_e32 v31, 0x38d1b717, v40
	v_max_f32_e32 v32, 0x38d1b717, v41
	v_max_f32_e32 v33, 0x38d1b717, v46
	v_max_f32_e32 v40, 0x38d1b717, v47
	v_max_f32_e32 v41, 0x38d1b717, v48
	v_max_f32_e32 v3, 0x38d1b717, v3
	v_pk_mul_f32 v[30:31], v[34:35], v[30:31]
	v_pk_mul_f32 v[32:33], v[36:37], v[32:33]
	v_pk_mul_f32 v[34:35], v[38:39], v[40:41]
	v_fma_mixlo_f16 v3, v26, v3, 0
	v_cvt_pk_f16_f32 v31, v30, v31
	v_cvt_pk_f16_f32 v32, v32, v33
	v_cvt_pk_f16_f32 v33, v34, v35
	v_max_f32_e32 v46, 0x38d1b717, v49
	v_pack_b32_f16 v30, v3, v31
	v_alignbit_b32 v31, v32, v31, 16
	v_alignbit_b32 v32, v33, v32, 16
	v_lshrrev_b32_e32 v33, 16, v33
	v_fma_mixhi_f16 v33, v25, v46, 0
.LBB0_5413:
	s_andn2_b64 vcc, exec, s[34:35]
	s_cbranch_vccnz .LBB0_5415
	s_lshl_b32 s2, s21, 1
	v_lshl_add_u64 v[4:5], v[42:43], 0, s[2:3]
	v_lshl_add_u64 v[4:5], v[148:149], 1, v[4:5]
	v_add_co_u32_e32 v4, vcc, 0x1000, v4
	s_add_u32 s34, s53, s30
	s_nop 0
	v_addc_co_u32_e32 v5, vcc, 0, v5, vcc
	s_addc_u32 s35, s54, s31
	v_lshl_add_u64 v[4:5], s[34:35], 0, v[44:45]
	s_waitcnt vmcnt(4)
	v_mov_b32_e32 v30, v230
	v_mov_b32_e32 v31, v231
	v_mov_b32_e32 v32, v232
	v_mov_b32_e32 v33, v233
	v_cvt_f32_f16_e32 v3, v30
	v_cvt_f32_f16_sdwa v30, v30 dst_sel:DWORD dst_unused:UNUSED_PAD src0_sel:WORD_1
	v_cvt_f32_f16_e32 v34, v31
	v_cvt_f32_f16_sdwa v31, v31 dst_sel:DWORD dst_unused:UNUSED_PAD src0_sel:WORD_1
	v_cvt_f32_f16_e32 v35, v32
	v_cvt_f32_f16_sdwa v32, v32 dst_sel:DWORD dst_unused:UNUSED_PAD src0_sel:WORD_1
	v_cvt_f32_f16_e32 v36, v33
	v_cvt_f32_f16_sdwa v33, v33 dst_sel:DWORD dst_unused:UNUSED_PAD src0_sel:WORD_1
	v_max_f32_e32 v37, 0x38d1b717, v3
	v_max_f32_e32 v38, 0x38d1b717, v30
	v_max_f32_e32 v39, 0x38d1b717, v34
	v_max_f32_e32 v40, 0x38d1b717, v31
	v_max_f32_e32 v41, 0x38d1b717, v35
	v_max_f32_e32 v42, 0x38d1b717, v32
	v_max_f32_e32 v43, 0x38d1b717, v36
	v_max_f32_e32 v44, 0x38d1b717, v33
	v_cndmask_b32_e64 v3, v37, v3, s[0:1]
	v_cndmask_b32_e64 v30, v38, v30, s[0:1]
	v_cndmask_b32_e64 v34, v39, v34, s[0:1]
	v_cndmask_b32_e64 v31, v40, v31, s[0:1]
	v_cndmask_b32_e64 v35, v41, v35, s[0:1]
	v_cndmask_b32_e64 v32, v42, v32, s[0:1]
	v_cndmask_b32_e64 v36, v43, v36, s[0:1]
	v_cndmask_b32_e64 v33, v44, v33, s[0:1]
	v_mul_f32_e32 v24, v24, v36
	v_mul_f32_e32 v23, v23, v32
	v_mul_f32_e32 v22, v22, v35
	v_mul_f32_e32 v29, v29, v31
	v_mul_f32_e32 v28, v28, v34
	v_mul_f32_e32 v27, v27, v30
	v_mul_f32_e32 v3, v26, v3
	v_mul_f32_e32 v25, v25, v33
	v_cvt_pk_f16_f32 v30, v3, v27
	v_cvt_pk_f16_f32 v31, v28, v29
	v_cvt_pk_f16_f32 v32, v22, v23
	v_cvt_pk_f16_f32 v33, v24, v25
.LBB0_5415:
	v_lshl_add_u64 v[4:5], v[148:149], 1, v[4:5]
	global_store_dwordx4 v[4:5], v[30:33], off offset:256
	v_mov_b64_e32 v[4:5], s[8:9]
	v_ashrrev_i32_e32 v153, 31, v152
	v_lshlrev_b64 v[28:29], 11, v[152:153]
	v_mad_i64_i32 v[26:27], s[34:35], v152, s62, v[4:5]
	s_mov_b64 s[34:35], -1
	s_and_b64 vcc, exec, s[4:5]
	v_lshl_add_u64 v[4:5], s[10:11], 0, v[28:29]
	s_cbranch_vccnz .LBB0_5417
	v_lshl_add_u64 v[22:23], v[148:149], 1, v[26:27]
	v_add_co_u32_e32 v22, vcc, 0x2000, v22
	v_mov_b32_e32 v32, v19
	s_nop 0
	v_addc_co_u32_e32 v23, vcc, 0, v23, vcc
	v_mov_b32_e32 v33, v20
	v_pk_mov_b32 v[34:35], v[20:21], v[14:15] op_sel:[1,0]
	v_mov_b32_e32 v36, v15
	v_mov_b32_e32 v37, v16
	v_lshl_add_u64 v[30:31], s[10:11], 0, v[28:29]
	s_mov_b64 s[34:35], 0
	s_waitcnt vmcnt(3)
	v_mov_b32_e32 v22, v234
	v_mov_b32_e32 v23, v235
	v_mov_b32_e32 v24, v236
	v_mov_b32_e32 v25, v237
	v_cvt_f32_f16_e32 v3, v22
	v_cvt_f32_f16_sdwa v22, v22 dst_sel:DWORD dst_unused:UNUSED_PAD src0_sel:WORD_1
	v_cvt_f32_f16_e32 v38, v23
	v_cvt_f32_f16_sdwa v39, v23 dst_sel:DWORD dst_unused:UNUSED_PAD src0_sel:WORD_1
	v_cvt_f32_f16_e32 v40, v24
	v_cvt_f32_f16_sdwa v41, v24 dst_sel:DWORD dst_unused:UNUSED_PAD src0_sel:WORD_1
	v_cvt_f32_f16_e32 v42, v25
	v_cvt_f32_f16_sdwa v43, v25 dst_sel:DWORD dst_unused:UNUSED_PAD src0_sel:WORD_1
	v_max_f32_e32 v22, 0x38d1b717, v22
	v_max_f32_e32 v23, 0x38d1b717, v38
	v_max_f32_e32 v24, 0x38d1b717, v39
	v_max_f32_e32 v25, 0x38d1b717, v40
	v_max_f32_e32 v38, 0x38d1b717, v41
	v_max_f32_e32 v39, 0x38d1b717, v42
	v_max_f32_e32 v3, 0x38d1b717, v3
	v_pk_mul_f32 v[22:23], v[32:33], v[22:23]
	v_pk_mul_f32 v[24:25], v[34:35], v[24:25]
	v_pk_mul_f32 v[32:33], v[36:37], v[38:39]
	v_fma_mixlo_f16 v3, v18, v3, 0
	v_cvt_pk_f16_f32 v23, v22, v23
	v_cvt_pk_f16_f32 v24, v24, v25
	v_cvt_pk_f16_f32 v25, v32, v33
	v_max_f32_e32 v40, 0x38d1b717, v43
	v_pack_b32_f16 v22, v3, v23
	v_alignbit_b32 v23, v24, v23, 16
	v_alignbit_b32 v24, v25, v24, 16
	v_lshrrev_b32_e32 v25, 16, v25
	v_fma_mixhi_f16 v25, v17, v40, 0
.LBB0_5417:
	s_andn2_b64 vcc, exec, s[34:35]
	v_lshl_add_u64 v[28:29], v[28:29], 0, s[18:19]
	s_cbranch_vccnz .LBB0_5419
	s_lshl_b32 s2, s21, 1
	v_lshl_add_u64 v[22:23], v[26:27], 0, s[2:3]
	v_lshl_add_u64 v[22:23], v[148:149], 1, v[22:23]
	v_add_co_u32_e32 v22, vcc, 0x1000, v22
	s_add_u32 s34, s53, s30
	s_nop 0
	v_addc_co_u32_e32 v23, vcc, 0, v23, vcc
	s_addc_u32 s35, s54, s31
	v_lshl_add_u64 v[30:31], s[34:35], 0, v[28:29]
	s_waitcnt vmcnt(3)
	v_mov_b32_e32 v22, v234
	v_mov_b32_e32 v23, v235
	v_mov_b32_e32 v24, v236
	v_mov_b32_e32 v25, v237
	v_cvt_f32_f16_e32 v3, v22
	v_cvt_f32_f16_sdwa v22, v22 dst_sel:DWORD dst_unused:UNUSED_PAD src0_sel:WORD_1
	v_cvt_f32_f16_e32 v32, v23
	v_cvt_f32_f16_sdwa v23, v23 dst_sel:DWORD dst_unused:UNUSED_PAD src0_sel:WORD_1
	v_cvt_f32_f16_e32 v33, v24
	v_cvt_f32_f16_sdwa v24, v24 dst_sel:DWORD dst_unused:UNUSED_PAD src0_sel:WORD_1
	v_cvt_f32_f16_e32 v34, v25
	v_cvt_f32_f16_sdwa v25, v25 dst_sel:DWORD dst_unused:UNUSED_PAD src0_sel:WORD_1
	v_max_f32_e32 v35, 0x38d1b717, v3
	v_max_f32_e32 v36, 0x38d1b717, v22
	v_max_f32_e32 v37, 0x38d1b717, v32
	v_max_f32_e32 v38, 0x38d1b717, v23
	v_max_f32_e32 v39, 0x38d1b717, v33
	v_max_f32_e32 v40, 0x38d1b717, v24
	v_max_f32_e32 v41, 0x38d1b717, v34
	v_max_f32_e32 v42, 0x38d1b717, v25
	v_cndmask_b32_e64 v3, v35, v3, s[0:1]
	v_cndmask_b32_e64 v22, v36, v22, s[0:1]
	v_cndmask_b32_e64 v32, v37, v32, s[0:1]
	v_cndmask_b32_e64 v23, v38, v23, s[0:1]
	v_cndmask_b32_e64 v33, v39, v33, s[0:1]
	v_cndmask_b32_e64 v24, v40, v24, s[0:1]
	v_cndmask_b32_e64 v34, v41, v34, s[0:1]
	v_cndmask_b32_e64 v25, v42, v25, s[0:1]
	v_mul_f32_e32 v16, v16, v34
	v_mul_f32_e32 v15, v15, v24
	v_mul_f32_e32 v14, v14, v33
	v_mul_f32_e32 v21, v21, v23
	v_mul_f32_e32 v20, v20, v32
	v_mul_f32_e32 v19, v19, v22
	v_mul_f32_e32 v3, v18, v3
	v_mul_f32_e32 v17, v17, v25
	v_cvt_pk_f16_f32 v22, v3, v19
	v_cvt_pk_f16_f32 v23, v20, v21
	v_cvt_pk_f16_f32 v24, v14, v15
	v_cvt_pk_f16_f32 v25, v16, v17
.LBB0_5419:
	v_lshl_add_u64 v[14:15], v[148:149], 1, v[30:31]
	s_and_b64 vcc, exec, s[4:5]
	s_mov_b64 s[4:5], -1
	global_store_dwordx4 v[14:15], v[22:25], off
	s_cbranch_vccnz .LBB0_5421
	v_lshl_add_u64 v[14:15], v[150:151], 1, v[26:27]
	v_add_co_u32_e32 v14, vcc, 0x2000, v14
	v_mov_b32_e32 v18, v11
	s_nop 0
	v_addc_co_u32_e32 v15, vcc, 0, v15, vcc
	v_mov_b32_e32 v19, v12
	v_pk_mov_b32 v[20:21], v[12:13], v[6:7] op_sel:[1,0]
	v_mov_b32_e32 v22, v7
	v_mov_b32_e32 v23, v8
	s_mov_b64 s[4:5], 0
	s_waitcnt vmcnt(2)
	v_mov_b32_e32 v14, v226
	v_mov_b32_e32 v15, v227
	v_mov_b32_e32 v16, v228
	v_mov_b32_e32 v17, v229
	v_cvt_f32_f16_e32 v3, v14
	v_cvt_f32_f16_sdwa v14, v14 dst_sel:DWORD dst_unused:UNUSED_PAD src0_sel:WORD_1
	v_cvt_f32_f16_e32 v24, v15
	v_cvt_f32_f16_sdwa v25, v15 dst_sel:DWORD dst_unused:UNUSED_PAD src0_sel:WORD_1
	v_cvt_f32_f16_e32 v30, v16
	v_cvt_f32_f16_sdwa v31, v16 dst_sel:DWORD dst_unused:UNUSED_PAD src0_sel:WORD_1
	v_cvt_f32_f16_e32 v32, v17
	v_cvt_f32_f16_sdwa v33, v17 dst_sel:DWORD dst_unused:UNUSED_PAD src0_sel:WORD_1
	v_max_f32_e32 v14, 0x38d1b717, v14
	v_max_f32_e32 v15, 0x38d1b717, v24
	v_max_f32_e32 v16, 0x38d1b717, v25
	v_max_f32_e32 v17, 0x38d1b717, v30
	v_max_f32_e32 v24, 0x38d1b717, v31
	v_max_f32_e32 v25, 0x38d1b717, v32
	v_max_f32_e32 v3, 0x38d1b717, v3
	v_pk_mul_f32 v[14:15], v[18:19], v[14:15]
	v_pk_mul_f32 v[16:17], v[20:21], v[16:17]
	v_pk_mul_f32 v[18:19], v[22:23], v[24:25]
	v_fma_mixlo_f16 v3, v10, v3, 0
	v_cvt_pk_f16_f32 v15, v14, v15
	v_cvt_pk_f16_f32 v16, v16, v17
	v_cvt_pk_f16_f32 v17, v18, v19
	v_max_f32_e32 v30, 0x38d1b717, v33
	v_pack_b32_f16 v14, v3, v15
	v_alignbit_b32 v15, v16, v15, 16
	v_alignbit_b32 v16, v17, v16, 16
	v_lshrrev_b32_e32 v17, 16, v17
	v_fma_mixhi_f16 v17, v9, v30, 0
.LBB0_5421:
	s_andn2_b64 vcc, exec, s[4:5]
	s_cbranch_vccnz .LBB0_5423
	s_lshl_b32 s2, s21, 1
	v_lshl_add_u64 v[4:5], v[26:27], 0, s[2:3]
	v_lshl_add_u64 v[4:5], v[148:149], 1, v[4:5]
	v_add_co_u32_e32 v4, vcc, 0x1000, v4
	s_add_u32 s4, s53, s30
	s_nop 0
	v_addc_co_u32_e32 v5, vcc, 0, v5, vcc
	s_addc_u32 s5, s54, s31
	v_lshl_add_u64 v[4:5], s[4:5], 0, v[28:29]
	s_waitcnt vmcnt(2)
	v_mov_b32_e32 v14, v226
	v_mov_b32_e32 v15, v227
	v_mov_b32_e32 v16, v228
	v_mov_b32_e32 v17, v229
	v_cvt_f32_f16_e32 v3, v14
	v_cvt_f32_f16_sdwa v14, v14 dst_sel:DWORD dst_unused:UNUSED_PAD src0_sel:WORD_1
	v_cvt_f32_f16_e32 v18, v15
	v_cvt_f32_f16_sdwa v15, v15 dst_sel:DWORD dst_unused:UNUSED_PAD src0_sel:WORD_1
	v_cvt_f32_f16_e32 v19, v16
	v_cvt_f32_f16_sdwa v16, v16 dst_sel:DWORD dst_unused:UNUSED_PAD src0_sel:WORD_1
	v_cvt_f32_f16_e32 v20, v17
	v_cvt_f32_f16_sdwa v17, v17 dst_sel:DWORD dst_unused:UNUSED_PAD src0_sel:WORD_1
	v_max_f32_e32 v21, 0x38d1b717, v3
	v_max_f32_e32 v22, 0x38d1b717, v14
	v_max_f32_e32 v23, 0x38d1b717, v18
	v_max_f32_e32 v24, 0x38d1b717, v15
	v_max_f32_e32 v25, 0x38d1b717, v19
	v_max_f32_e32 v26, 0x38d1b717, v16
	v_max_f32_e32 v27, 0x38d1b717, v20
	v_max_f32_e32 v28, 0x38d1b717, v17
	v_cndmask_b32_e64 v3, v21, v3, s[0:1]
	v_cndmask_b32_e64 v14, v22, v14, s[0:1]
	v_cndmask_b32_e64 v18, v23, v18, s[0:1]
	v_cndmask_b32_e64 v15, v24, v15, s[0:1]
	v_cndmask_b32_e64 v19, v25, v19, s[0:1]
	v_cndmask_b32_e64 v16, v26, v16, s[0:1]
	v_cndmask_b32_e64 v20, v27, v20, s[0:1]
	v_cndmask_b32_e64 v17, v28, v17, s[0:1]
	v_mul_f32_e32 v8, v8, v20
	v_mul_f32_e32 v7, v7, v16
	v_mul_f32_e32 v6, v6, v19
	v_mul_f32_e32 v13, v13, v15
	v_mul_f32_e32 v12, v12, v18
	v_mul_f32_e32 v11, v11, v14
	v_mul_f32_e32 v3, v10, v3
	v_mul_f32_e32 v9, v9, v17
	v_cvt_pk_f16_f32 v14, v3, v11
	v_cvt_pk_f16_f32 v15, v12, v13
	v_cvt_pk_f16_f32 v16, v6, v7
	v_cvt_pk_f16_f32 v17, v8, v9
